# baseline (speedup 1.0000x reference)
_Z7k_stageILi0ELi4EEv8AttnArgsPKDF16_PKfPDF16_iii:
	s_load_dwordx16 s[64:79], s[0:1], 0x0
	v_readfirstlane_b32 s94, v0
	s_nop 0
	s_lshr_b32 s94, s94, 6
	s_load_dwordx4 s[8:11], s[0:1], 0x70
	s_load_dwordx2 s[20:21], s[0:1], 0x80
	s_load_dwordx4 s[12:15], s[0:1], 0x88
	s_lshl_b32 s5, s2, 5
	s_waitcnt lgkmcnt(0)
	s_and_b32 s15, s5, 0xe0
	s_lshr_b32 s5, s2, 3
	s_add_i32 s15, s15, s5
	s_and_b32 s2, s2, 56
	v_readfirstlane_b32 s4, v0
	v_and_b32_e32 v1, 15, v0
	s_cmp_lt_i32 s14, 1
	v_bfe_u32 v158, v0, 4, 2
	s_cbranch_scc1 .LBB5_79
	s_bfe_u32 s5, s4, 0x10006
	s_lshl_b32 s6, s5, 4
	s_mul_i32 s16, s3, 40
	s_mul_hi_i32 s7, s3, 40
	s_add_u32 s22, s0, s16
	s_addc_u32 s23, s1, s7
	s_load_dwordx4 s[16:19], s[22:23], 0x0
	s_load_dwordx2 s[0:1], s[22:23], 0x10
	v_or_b32_e32 v159, s6, v1
	v_lshlrev_b32_e32 v18, 5, v159
	s_waitcnt lgkmcnt(0)
	global_load_dwordx4 v[230:233], v18, s[18:19]
	global_load_dwordx4 v[234:237], v18, s[0:1]
	global_load_dwordx4 v[238:241], v18, s[18:19] offset:16
	global_load_dwordx4 v[242:245], v18, s[0:1] offset:16
	v_bfe_u32 v21, v0, 7, 1
	v_lshrrev_b32_e32 v19, 4, v0
	v_lshlrev_b16_e32 v23, 2, v21
	v_lshrrev_b32_e32 v18, 5, v0
	v_lshrrev_b32_e32 v20, 6, v0
	v_and_b32_e32 v24, 3, v19
	v_bitop3_b16 v19, v23, v19, 3 bitop3:0xf8
	s_movk_i32 s0, 0x3000
	v_and_b32_e32 v18, 4, v18
	v_and_b32_e32 v22, 4, v20
	v_lshlrev_b32_e32 v20, 12, v20
	v_lshlrev_b32_e32 v21, 11, v21
	v_and_b32_e32 v19, 0xffff, v19
	s_bitcmp1_b32 s4, 6
	v_or_b32_e32 v161, v18, v158
	v_and_or_b32 v162, s15, 56, v22
	v_bitop3_b16 v23, v23, 8, v24 bitop3:0xfe
	v_lshlrev_b32_e32 v24, 3, v22
	v_lshl_or_b32 v22, v22, 12, v21
	v_or3_b32 v163, v20, v21, s0
	v_bitop3_b32 v18, v18, v159, v158 bitop3:0x36
	v_bitop3_b32 v19, s6, v19, v1 bitop3:0x36
	s_cselect_b64 s[24:25], -1, 0
	s_and_b32 s0, s15, 0x1ffc0
	s_movk_i32 s1, 0x2000
	v_lshl_or_b32 v168, v18, 4, v22
	v_lshlrev_b32_e32 v18, 4, v19
	v_or_b32_e32 v19, s0, v162
	v_add3_u32 v170, v22, v18, s1
	v_lshl_or_b32 v18, v19, 6, s2
	v_add_u32_e32 v18, v161, v18
	v_mul_u32_u24_e32 v18, 0x600, v18
	v_and_b32_e32 v20, 0xffff, v23
	v_lshl_or_b32 v18, s5, 8, v18
	v_lshlrev_b32_e32 v160, 9, v158
	v_bitop3_b32 v20, s6, v20, v1 bitop3:0x36
	v_lshl_or_b32 v18, v1, 4, v18
	v_add_u32_e32 v164, -1, v162
	v_add_u32_e32 v165, 4, v162
	v_or3_b32 v166, v161, v24, 8
	v_or_b32_e32 v167, 0x1000, v22
	v_lshl_or_b32 v169, v20, 4, v160
	s_and_b32 s17, s17, 0xffff
	s_mov_b32 s19, 0x20000
	s_mov_b32 s18, 0x1800000
	v_add_u32_e32 v171, 0xfffe7c00, v18
	s_mov_b32 s30, s2
	s_mov_b32 s93, 0
	s_branch .LBB5_4
.LBB5_2:
	s_waitcnt lgkmcnt(0)
	v_cvt_f16_f32_e32 v180, s7
	v_cvt_f16_f32_e32 v182, s6
	v_cvt_f16_f32_e32 v181, s28
	s_cmp_lt_u32 s94, 4
	s_cbranch_scc1 .Lmylp5_1
	s_setprio 1
.Lmylp5_1:
	s_waitcnt vmcnt(3)
	v_pk_mul_f16 v183, v182, v184 op_sel_hi:[0,1]
	v_pk_mul_f16 v190, v182, v187 op_sel_hi:[0,1]
	v_pk_mul_f16 v194, v180, v187 op_sel_hi:[0,1]
	v_pk_mul_f16 v198, v181, v187 op_sel_hi:[0,1]
	v_pk_mul_f16 v188, v182, v185 op_sel_hi:[0,1]
	v_pk_mul_f16 v189, v182, v186 op_sel_hi:[0,1]
	v_pk_mul_f16 v191, v180, v184 op_sel_hi:[0,1]
	s_mov_b64 exec, s[64:65]
	buffer_load_dwordx4 v[18:21], v224, s[16:19], 0 offen
	buffer_load_dwordx4 v[6:9], v224, s[16:19], 0 offen offset:512
	s_mov_b64 exec, -1
	v_pk_mul_f16 v192, v180, v185 op_sel_hi:[0,1]
	v_pk_mul_f16 v193, v180, v186 op_sel_hi:[0,1]
	v_pk_mul_f16 v195, v181, v184 op_sel_hi:[0,1]
	v_pk_mul_f16 v196, v181, v185 op_sel_hi:[0,1]
	v_pk_mul_f16 v197, v181, v186 op_sel_hi:[0,1]
	v_pk_fma_f16 v113, v113, v187, v190
	v_pk_fma_f16 v110, v110, v184, v183
	v_pk_fma_f16 v129, v129, v187, v190
	v_pk_fma_f16 v126, v126, v184, v183
	v_pk_fma_f16 v137, v137, v187, v190
	v_pk_fma_f16 v134, v134, v184, v183
	v_pk_fma_f16 v183, v85, v187, v194
	v_pk_fma_f16 v199, v109, v187, v194
	buffer_load_dwordx4 v[30:33], v225, s[16:19], 0 offen offset:512
	buffer_load_dwordx4 v[10:13], v225, s[16:19], 0 offen offset:1024
	v_pk_fma_f16 v194, v125, v187, v194
	v_pk_fma_f16 v203, v53, v187, v198
	v_pk_fma_f16 v207, v69, v187, v198
	v_pk_fma_f16 v187, v97, v187, v198
	v_pk_maximum3_f16 v198, v113, v129, v137
	v_pk_fma_f16 v112, v112, v186, v189
	v_pk_fma_f16 v111, v111, v185, v188
	v_pk_fma_f16 v128, v128, v186, v189
	v_pk_fma_f16 v127, v127, v185, v188
	v_pk_fma_f16 v136, v136, v186, v189
	v_pk_fma_f16 v135, v135, v185, v188
	v_pk_fma_f16 v188, v84, v186, v193
	v_pk_fma_f16 v189, v83, v185, v192
	v_pk_fma_f16 v190, v82, v184, v191
	v_pk_fma_f16 v200, v108, v186, v193
	v_pk_fma_f16 v201, v107, v185, v192
	s_mov_b64 exec, s[66:67]
	buffer_load_dwordx4 v[54:57], v225, s[16:19], 0 offen offset:2048
	buffer_load_dwordx4 v[14:17], v225, s[16:19], 0 offen offset:2560
	s_mov_b64 exec, -1
	v_pk_fma_f16 v202, v106, v184, v191
	v_pk_fma_f16 v193, v124, v186, v193
	v_pk_fma_f16 v192, v123, v185, v192
	v_pk_fma_f16 v191, v122, v184, v191
	v_pk_fma_f16 v204, v52, v186, v197
	v_pk_fma_f16 v205, v51, v185, v196
	v_pk_fma_f16 v206, v50, v184, v195
	v_pk_fma_f16 v208, v68, v186, v197
	v_pk_fma_f16 v209, v67, v185, v196
	v_pk_fma_f16 v210, v66, v184, v195
	v_pk_fma_f16 v186, v96, v186, v197
	v_pk_fma_f16 v185, v95, v185, v196
	v_pk_fma_f16 v184, v94, v184, v195
	v_pk_maximum3_f16 v195, v110, v126, v134
	v_pk_maximum3_f16 v196, v111, v127, v135
	v_pk_maximum3_f16 v197, v112, v128, v136
	v_pk_maximum3_f16 v214, v183, v199, v194
	v_pk_maximum3_f16 v218, v203, v207, v187
	v_pk_maximum3_f16 v211, v190, v202, v191
	v_pk_maximum3_f16 v212, v189, v201, v192
	v_pk_maximum3_f16 v213, v188, v200, v193
	v_pk_maximum3_f16 v215, v206, v210, v184
	v_pk_maximum3_f16 v216, v205, v209, v185
	v_pk_maximum3_f16 v198, v198, v214, v218
	v_pk_maximum3_f16 v217, v204, v208, v186
	v_pk_maximum3_f16 v195, v195, v211, v215
	v_pk_maximum3_f16 v196, v196, v212, v216
	v_pk_maximum3_f16 v197, v197, v213, v217
	v_pk_add_f16 v113, v113, v198 neg_lo:[0,1] neg_hi:[0,1]
	s_mov_b64 exec, s[64:65]
	buffer_load_dwordx4 v[74:77], v226, s[16:19], 0 offen
	buffer_load_dwordx4 v[26:29], v226, s[16:19], 0 offen offset:512
	s_mov_b64 exec, -1
	v_pk_add_f16 v110, v110, v195 neg_lo:[0,1] neg_hi:[0,1]
	v_pk_add_f16 v111, v111, v196 neg_lo:[0,1] neg_hi:[0,1]
	v_pk_add_f16 v112, v112, v197 neg_lo:[0,1] neg_hi:[0,1]
	v_pk_add_f16 v126, v126, v195 neg_lo:[0,1] neg_hi:[0,1]
	v_exp_f16_sdwa v211, v110 dst_sel:WORD_0 dst_unused:UNUSED_PAD src0_sel:WORD_0
	v_exp_f16_sdwa v212, v111 dst_sel:WORD_0 dst_unused:UNUSED_PAD src0_sel:WORD_0
	v_exp_f16_sdwa v213, v112 dst_sel:WORD_0 dst_unused:UNUSED_PAD src0_sel:WORD_0
	v_exp_f16_sdwa v214, v113 dst_sel:WORD_0 dst_unused:UNUSED_PAD src0_sel:WORD_0
	v_exp_f16_sdwa v211, v110 dst_sel:WORD_1 dst_unused:UNUSED_PRESERVE src0_sel:WORD_1
	v_exp_f16_sdwa v212, v111 dst_sel:WORD_1 dst_unused:UNUSED_PRESERVE src0_sel:WORD_1
	v_exp_f16_sdwa v213, v112 dst_sel:WORD_1 dst_unused:UNUSED_PRESERVE src0_sel:WORD_1
	v_exp_f16_sdwa v214, v113 dst_sel:WORD_1 dst_unused:UNUSED_PRESERVE src0_sel:WORD_1
	v_pk_add_f16 v127, v127, v196 neg_lo:[0,1] neg_hi:[0,1]
	v_pk_add_f16 v113, v211, 0
	v_pk_fma_f16 v81, v81, v214, 0
	v_pk_add_f16 v110, v214, 0
	v_pk_add_f16 v111, v213, 0
	v_pk_add_f16 v112, v212, 0
	v_pk_fma_f16 v80, v80, v213, 0
	v_pk_fma_f16 v79, v79, v212, 0
	v_pk_fma_f16 v78, v78, v211, 0
	v_pk_add_f16 v128, v128, v197 neg_lo:[0,1] neg_hi:[0,1]
	buffer_load_dwordx4 v[98:101], v227, s[16:19], 0 offen offset:512
	buffer_load_dwordx4 v[38:41], v227, s[16:19], 0 offen offset:1024
	v_pk_add_f16 v129, v129, v198 neg_lo:[0,1] neg_hi:[0,1]
	v_exp_f16_sdwa v211, v126 dst_sel:WORD_0 dst_unused:UNUSED_PAD src0_sel:WORD_0
	v_exp_f16_sdwa v212, v127 dst_sel:WORD_0 dst_unused:UNUSED_PAD src0_sel:WORD_0
	v_exp_f16_sdwa v213, v128 dst_sel:WORD_0 dst_unused:UNUSED_PAD src0_sel:WORD_0
	v_exp_f16_sdwa v214, v129 dst_sel:WORD_0 dst_unused:UNUSED_PAD src0_sel:WORD_0
	v_exp_f16_sdwa v211, v126 dst_sel:WORD_1 dst_unused:UNUSED_PRESERVE src0_sel:WORD_1
	v_exp_f16_sdwa v212, v127 dst_sel:WORD_1 dst_unused:UNUSED_PRESERVE src0_sel:WORD_1
	v_exp_f16_sdwa v213, v128 dst_sel:WORD_1 dst_unused:UNUSED_PRESERVE src0_sel:WORD_1
	v_exp_f16_sdwa v214, v129 dst_sel:WORD_1 dst_unused:UNUSED_PRESERVE src0_sel:WORD_1
	v_pk_add_f16 v113, v113, v211
	v_pk_fma_f16 v81, v105, v214, v81
	v_pk_add_f16 v105, v137, v198 neg_lo:[0,1] neg_hi:[0,1]
	v_pk_add_f16 v112, v112, v212
	v_pk_add_f16 v111, v111, v213
	v_pk_add_f16 v110, v110, v214
	v_pk_fma_f16 v78, v102, v211, v78
	v_pk_fma_f16 v79, v103, v212, v79
	v_pk_fma_f16 v80, v104, v213, v80
	v_pk_add_f16 v102, v134, v195 neg_lo:[0,1] neg_hi:[0,1]
	v_pk_add_f16 v103, v135, v196 neg_lo:[0,1] neg_hi:[0,1]
	v_pk_add_f16 v104, v136, v197 neg_lo:[0,1] neg_hi:[0,1]
	v_exp_f16_sdwa v126, v102 dst_sel:WORD_0 dst_unused:UNUSED_PAD src0_sel:WORD_0
	v_exp_f16_sdwa v127, v103 dst_sel:WORD_0 dst_unused:UNUSED_PAD src0_sel:WORD_0
	v_exp_f16_sdwa v128, v104 dst_sel:WORD_0 dst_unused:UNUSED_PAD src0_sel:WORD_0
	v_exp_f16_sdwa v129, v105 dst_sel:WORD_0 dst_unused:UNUSED_PAD src0_sel:WORD_0
	v_exp_f16_sdwa v126, v102 dst_sel:WORD_1 dst_unused:UNUSED_PRESERVE src0_sel:WORD_1
	v_exp_f16_sdwa v127, v103 dst_sel:WORD_1 dst_unused:UNUSED_PRESERVE src0_sel:WORD_1
	v_exp_f16_sdwa v128, v104 dst_sel:WORD_1 dst_unused:UNUSED_PRESERVE src0_sel:WORD_1
	v_exp_f16_sdwa v129, v105 dst_sel:WORD_1 dst_unused:UNUSED_PRESERVE src0_sel:WORD_1
	v_pk_add_f16 v105, v113, v126
	v_pk_add_f16 v102, v110, v129
	s_mov_b64 exec, s[66:67]
	buffer_load_dwordx4 v[118:121], v227, s[16:19], 0 offen offset:2048
	buffer_load_dwordx4 v[58:61], v227, s[16:19], 0 offen offset:2560
	s_mov_b64 exec, -1
	v_pk_add_f16 v103, v111, v128
	v_pk_add_f16 v104, v112, v127
	v_pk_fma_f16 v81, v117, v129, v81
	v_pk_fma_f16 v80, v116, v128, v80
	v_pk_fma_f16 v79, v115, v127, v79
	v_pk_fma_f16 v78, v114, v126, v78
	v_pk_add_f16 v110, v190, v195 neg_lo:[0,1] neg_hi:[0,1]
	v_pk_add_f16 v111, v189, v196 neg_lo:[0,1] neg_hi:[0,1]
	v_pk_add_f16 v112, v188, v197 neg_lo:[0,1] neg_hi:[0,1]
	v_pk_add_f16 v113, v183, v198 neg_lo:[0,1] neg_hi:[0,1]
	v_exp_f16_sdwa v114, v110 dst_sel:WORD_0 dst_unused:UNUSED_PAD src0_sel:WORD_0
	v_exp_f16_sdwa v115, v111 dst_sel:WORD_0 dst_unused:UNUSED_PAD src0_sel:WORD_0
	v_exp_f16_sdwa v116, v112 dst_sel:WORD_0 dst_unused:UNUSED_PAD src0_sel:WORD_0
	v_exp_f16_sdwa v117, v113 dst_sel:WORD_0 dst_unused:UNUSED_PAD src0_sel:WORD_0
	v_exp_f16_sdwa v114, v110 dst_sel:WORD_1 dst_unused:UNUSED_PRESERVE src0_sel:WORD_1
	v_exp_f16_sdwa v115, v111 dst_sel:WORD_1 dst_unused:UNUSED_PRESERVE src0_sel:WORD_1
	v_exp_f16_sdwa v116, v112 dst_sel:WORD_1 dst_unused:UNUSED_PRESERVE src0_sel:WORD_1
	v_exp_f16_sdwa v117, v113 dst_sel:WORD_1 dst_unused:UNUSED_PRESERVE src0_sel:WORD_1
	v_pk_add_f16 v110, v202, v195 neg_lo:[0,1] neg_hi:[0,1]
	v_pk_add_f16 v105, v105, v114
	v_pk_add_f16 v104, v104, v115
	v_pk_add_f16 v103, v103, v116
	s_mov_b64 exec, s[76:77]
	buffer_load_dwordx4 v[130:133], v228, s[16:19], 0 offen
	buffer_load_dwordx4 v[70:73], v228, s[16:19], 0 offen offset:512
	s_mov_b64 exec, -1
	v_pk_add_f16 v102, v102, v117
	v_pk_fma_f16 v78, v42, v114, v78
	v_pk_fma_f16 v79, v43, v115, v79
	v_pk_fma_f16 v80, v44, v116, v80
	v_pk_fma_f16 v81, v45, v117, v81
	v_pk_add_f16 v111, v201, v196 neg_lo:[0,1] neg_hi:[0,1]
	v_pk_add_f16 v112, v200, v197 neg_lo:[0,1] neg_hi:[0,1]
	v_pk_add_f16 v113, v199, v198 neg_lo:[0,1] neg_hi:[0,1]
	v_exp_f16_sdwa v114, v110 dst_sel:WORD_0 dst_unused:UNUSED_PAD src0_sel:WORD_0
	v_exp_f16_sdwa v115, v111 dst_sel:WORD_0 dst_unused:UNUSED_PAD src0_sel:WORD_0
	v_exp_f16_sdwa v116, v112 dst_sel:WORD_0 dst_unused:UNUSED_PAD src0_sel:WORD_0
	v_exp_f16_sdwa v117, v113 dst_sel:WORD_0 dst_unused:UNUSED_PAD src0_sel:WORD_0
	v_exp_f16_sdwa v114, v110 dst_sel:WORD_1 dst_unused:UNUSED_PRESERVE src0_sel:WORD_1
	v_exp_f16_sdwa v115, v111 dst_sel:WORD_1 dst_unused:UNUSED_PRESERVE src0_sel:WORD_1
	v_exp_f16_sdwa v116, v112 dst_sel:WORD_1 dst_unused:UNUSED_PRESERVE src0_sel:WORD_1
	v_exp_f16_sdwa v117, v113 dst_sel:WORD_1 dst_unused:UNUSED_PRESERVE src0_sel:WORD_1
	v_pk_add_f16 v110, v191, v195 neg_lo:[0,1] neg_hi:[0,1]
	v_pk_add_f16 v105, v105, v114
	v_pk_add_f16 v102, v102, v117
	v_pk_add_f16 v103, v103, v116
	v_pk_add_f16 v104, v104, v115
	v_pk_fma_f16 v81, v65, v117, v81
	v_pk_fma_f16 v80, v64, v116, v80
	s_mov_b64 exec, s[70:71]
	buffer_load_dwordx4 v[138:141], v229, s[16:19], 0 offen offset:512
	buffer_load_dwordx4 v[90:93], v229, s[16:19], 0 offen offset:1024
	s_mov_b64 exec, -1
	v_pk_fma_f16 v79, v63, v115, v79
	v_pk_fma_f16 v78, v62, v114, v78
	v_pk_add_f16 v111, v192, v196 neg_lo:[0,1] neg_hi:[0,1]
	v_pk_add_f16 v112, v193, v197 neg_lo:[0,1] neg_hi:[0,1]
	v_pk_add_f16 v113, v194, v198 neg_lo:[0,1] neg_hi:[0,1]
	v_exp_f16_sdwa v114, v110 dst_sel:WORD_0 dst_unused:UNUSED_PAD src0_sel:WORD_0
	v_exp_f16_sdwa v115, v111 dst_sel:WORD_0 dst_unused:UNUSED_PAD src0_sel:WORD_0
	v_exp_f16_sdwa v116, v112 dst_sel:WORD_0 dst_unused:UNUSED_PAD src0_sel:WORD_0
	v_exp_f16_sdwa v117, v113 dst_sel:WORD_0 dst_unused:UNUSED_PAD src0_sel:WORD_0
	v_exp_f16_sdwa v114, v110 dst_sel:WORD_1 dst_unused:UNUSED_PRESERVE src0_sel:WORD_1
	v_exp_f16_sdwa v115, v111 dst_sel:WORD_1 dst_unused:UNUSED_PRESERVE src0_sel:WORD_1
	v_exp_f16_sdwa v116, v112 dst_sel:WORD_1 dst_unused:UNUSED_PRESERVE src0_sel:WORD_1
	v_exp_f16_sdwa v117, v113 dst_sel:WORD_1 dst_unused:UNUSED_PRESERVE src0_sel:WORD_1
	v_pk_add_f16 v110, v206, v195 neg_lo:[0,1] neg_hi:[0,1]
	v_pk_add_f16 v105, v105, v114
	v_pk_add_f16 v104, v104, v115
	v_pk_add_f16 v103, v103, v116
	v_pk_add_f16 v102, v102, v117
	v_pk_fma_f16 v78, v86, v114, v78
	v_pk_fma_f16 v79, v87, v115, v79
	v_pk_fma_f16 v80, v88, v116, v80
	v_pk_fma_f16 v81, v89, v117, v81
	s_mov_b64 exec, s[78:79]
	buffer_load_dwordx4 v[142:145], v229, s[16:19], 0 offen offset:2048
	buffer_load_dwordx4 v[2:5], v229, s[16:19], 0 offen offset:2560
	s_mov_b64 exec, -1
	v_pk_add_f16 v111, v205, v196 neg_lo:[0,1] neg_hi:[0,1]
	v_pk_add_f16 v112, v204, v197 neg_lo:[0,1] neg_hi:[0,1]
	v_pk_add_f16 v113, v203, v198 neg_lo:[0,1] neg_hi:[0,1]
	v_exp_f16_sdwa v114, v110 dst_sel:WORD_0 dst_unused:UNUSED_PAD src0_sel:WORD_0
	v_exp_f16_sdwa v115, v111 dst_sel:WORD_0 dst_unused:UNUSED_PAD src0_sel:WORD_0
	v_exp_f16_sdwa v116, v112 dst_sel:WORD_0 dst_unused:UNUSED_PAD src0_sel:WORD_0
	v_exp_f16_sdwa v117, v113 dst_sel:WORD_0 dst_unused:UNUSED_PAD src0_sel:WORD_0
	v_exp_f16_sdwa v114, v110 dst_sel:WORD_1 dst_unused:UNUSED_PRESERVE src0_sel:WORD_1
	v_exp_f16_sdwa v115, v111 dst_sel:WORD_1 dst_unused:UNUSED_PRESERVE src0_sel:WORD_1
	v_exp_f16_sdwa v116, v112 dst_sel:WORD_1 dst_unused:UNUSED_PRESERVE src0_sel:WORD_1
	v_exp_f16_sdwa v117, v113 dst_sel:WORD_1 dst_unused:UNUSED_PRESERVE src0_sel:WORD_1
	v_pk_add_f16 v110, v210, v195 neg_lo:[0,1] neg_hi:[0,1]
	v_pk_add_f16 v105, v105, v114
	v_pk_add_f16 v102, v102, v117
	v_pk_add_f16 v103, v103, v116
	v_pk_add_f16 v104, v104, v115
	v_pk_fma_f16 v81, v25, v117, v81
	v_pk_fma_f16 v80, v24, v116, v80
	v_pk_fma_f16 v79, v23, v115, v79
	v_pk_fma_f16 v78, v22, v114, v78
	v_pk_add_f16 v111, v209, v196 neg_lo:[0,1] neg_hi:[0,1]
	v_pk_add_f16 v112, v208, v197 neg_lo:[0,1] neg_hi:[0,1]
	v_pk_add_f16 v113, v207, v198 neg_lo:[0,1] neg_hi:[0,1]
	v_exp_f16_sdwa v114, v110 dst_sel:WORD_0 dst_unused:UNUSED_PAD src0_sel:WORD_0
	v_exp_f16_sdwa v115, v111 dst_sel:WORD_0 dst_unused:UNUSED_PAD src0_sel:WORD_0
	v_exp_f16_sdwa v116, v112 dst_sel:WORD_0 dst_unused:UNUSED_PAD src0_sel:WORD_0
	v_exp_f16_sdwa v117, v113 dst_sel:WORD_0 dst_unused:UNUSED_PAD src0_sel:WORD_0
	v_exp_f16_sdwa v114, v110 dst_sel:WORD_1 dst_unused:UNUSED_PRESERVE src0_sel:WORD_1
	v_exp_f16_sdwa v115, v111 dst_sel:WORD_1 dst_unused:UNUSED_PRESERVE src0_sel:WORD_1
	v_exp_f16_sdwa v116, v112 dst_sel:WORD_1 dst_unused:UNUSED_PRESERVE src0_sel:WORD_1
	v_exp_f16_sdwa v117, v113 dst_sel:WORD_1 dst_unused:UNUSED_PRESERVE src0_sel:WORD_1
	v_pk_add_f16 v110, v184, v195 neg_lo:[0,1] neg_hi:[0,1]
	v_pk_add_f16 v105, v105, v114
	v_pk_add_f16 v104, v104, v115
	v_pk_add_f16 v103, v103, v116
	v_pk_add_f16 v102, v102, v117
	v_pk_fma_f16 v78, v34, v114, v78
	v_pk_fma_f16 v79, v35, v115, v79
	v_pk_fma_f16 v80, v36, v116, v80
	v_pk_fma_f16 v81, v37, v117, v81
	v_pk_add_f16 v111, v185, v196 neg_lo:[0,1] neg_hi:[0,1]
	v_pk_add_f16 v112, v186, v197 neg_lo:[0,1] neg_hi:[0,1]
	v_pk_add_f16 v113, v187, v198 neg_lo:[0,1] neg_hi:[0,1]
	v_exp_f16_sdwa v114, v110 dst_sel:WORD_0 dst_unused:UNUSED_PAD src0_sel:WORD_0
	v_exp_f16_sdwa v115, v111 dst_sel:WORD_0 dst_unused:UNUSED_PAD src0_sel:WORD_0
	v_exp_f16_sdwa v116, v112 dst_sel:WORD_0 dst_unused:UNUSED_PAD src0_sel:WORD_0
	v_exp_f16_sdwa v117, v113 dst_sel:WORD_0 dst_unused:UNUSED_PAD src0_sel:WORD_0
	v_exp_f16_sdwa v114, v110 dst_sel:WORD_1 dst_unused:UNUSED_PRESERVE src0_sel:WORD_1
	v_exp_f16_sdwa v115, v111 dst_sel:WORD_1 dst_unused:UNUSED_PRESERVE src0_sel:WORD_1
	v_exp_f16_sdwa v116, v112 dst_sel:WORD_1 dst_unused:UNUSED_PRESERVE src0_sel:WORD_1
	v_exp_f16_sdwa v117, v113 dst_sel:WORD_1 dst_unused:UNUSED_PRESERVE src0_sel:WORD_1
	v_pk_add_f16 v105, v105, v114
	v_pk_add_f16 v104, v104, v115
	v_rcp_f16_e32 v110, v105
	v_rcp_f16_sdwa v105, v105 dst_sel:DWORD dst_unused:UNUSED_PAD src0_sel:WORD_1
	v_pk_add_f16 v103, v103, v116
	v_rcp_f16_e32 v111, v104
	v_rcp_f16_sdwa v104, v104 dst_sel:DWORD dst_unused:UNUSED_PAD src0_sel:WORD_1
	v_pk_add_f16 v102, v102, v117
	v_rcp_f16_e32 v112, v103
	v_rcp_f16_sdwa v103, v103 dst_sel:DWORD dst_unused:UNUSED_PAD src0_sel:WORD_1
	v_rcp_f16_e32 v113, v102
	v_rcp_f16_sdwa v102, v102 dst_sel:DWORD dst_unused:UNUSED_PAD src0_sel:WORD_1
	v_pk_fma_f16 v78, v46, v114, v78
	v_pack_b32_f16 v105, v110, v105
	v_pk_fma_f16 v79, v47, v115, v79
	v_pk_mul_f16 v110, v78, v105
	v_pack_b32_f16 v78, v111, v104
	v_pk_fma_f16 v80, v48, v116, v80
	v_pk_mul_f16 v111, v79, v78
	v_pack_b32_f16 v78, v112, v103
	v_pk_fma_f16 v81, v49, v117, v81
	v_pk_mul_f16 v112, v80, v78
	v_pack_b32_f16 v78, v113, v102
	v_pk_mul_f16 v113, v81, v78
	s_waitcnt vmcnt(12)
	v_pk_mul_f16 v78, v182, v154 op_sel_hi:[0,1]
	v_pk_mul_f16 v81, v182, v157 op_sel_hi:[0,1]
	v_pk_mul_f16 v102, v180, v154 op_sel_hi:[0,1]
	v_pk_mul_f16 v114, v181, v154 op_sel_hi:[0,1]
	v_pk_mul_f16 v79, v182, v155 op_sel_hi:[0,1]
	v_pk_mul_f16 v80, v182, v156 op_sel_hi:[0,1]
	v_pk_mul_f16 v103, v180, v155 op_sel_hi:[0,1]
	v_pk_mul_f16 v104, v180, v156 op_sel_hi:[0,1]
	v_pk_mul_f16 v105, v180, v157 op_sel_hi:[0,1]
	v_pk_mul_f16 v115, v181, v155 op_sel_hi:[0,1]
	v_pk_mul_f16 v116, v181, v156 op_sel_hi:[0,1]
	v_pk_mul_f16 v117, v181, v157 op_sel_hi:[0,1]
	v_pk_fma_f16 v85, v85, v157, v81
	v_pk_fma_f16 v82, v82, v154, v78
	v_pk_fma_f16 v109, v109, v157, v81
	v_pk_fma_f16 v106, v106, v154, v78
	v_pk_fma_f16 v81, v125, v157, v81
	v_pk_fma_f16 v78, v122, v154, v78
	v_pk_fma_f16 v125, v50, v154, v102
	v_pk_fma_f16 v129, v66, v154, v102
	v_pk_fma_f16 v102, v94, v154, v102
	v_pk_fma_f16 v137, v18, v154, v114
	v_pk_fma_f16 v186, v30, v154, v114
	v_pk_fma_f16 v114, v54, v154, v114
	v_pk_maximum3_f16 v154, v82, v106, v78
	v_pk_fma_f16 v84, v84, v156, v80
	v_pk_fma_f16 v83, v83, v155, v79
	v_pk_fma_f16 v108, v108, v156, v80
	v_pk_fma_f16 v107, v107, v155, v79
	v_pk_fma_f16 v80, v124, v156, v80
	v_pk_fma_f16 v79, v123, v155, v79
	v_pk_fma_f16 v122, v53, v157, v105
	v_pk_fma_f16 v123, v52, v156, v104
	v_pk_fma_f16 v124, v51, v155, v103
	v_pk_fma_f16 v126, v69, v157, v105
	v_pk_fma_f16 v127, v68, v156, v104
	v_pk_fma_f16 v128, v67, v155, v103
	v_pk_fma_f16 v105, v97, v157, v105
	v_pk_fma_f16 v104, v96, v156, v104
	v_pk_fma_f16 v103, v95, v155, v103
	v_pk_fma_f16 v134, v21, v157, v117
	v_pk_fma_f16 v135, v20, v156, v116
	v_pk_fma_f16 v136, v19, v155, v115
	v_pk_fma_f16 v183, v33, v157, v117
	v_pk_fma_f16 v184, v32, v156, v116
	v_pk_fma_f16 v185, v31, v155, v115
	v_pk_fma_f16 v117, v57, v157, v117
	v_pk_fma_f16 v116, v56, v156, v116
	v_pk_fma_f16 v115, v55, v155, v115
	v_pk_maximum3_f16 v155, v83, v107, v79
	v_pk_maximum3_f16 v156, v84, v108, v80
	v_pk_maximum3_f16 v157, v85, v109, v81
	v_pk_maximum3_f16 v187, v125, v129, v102
	v_pk_maximum3_f16 v191, v137, v186, v114
	v_pk_maximum3_f16 v188, v124, v128, v103
	v_pk_maximum3_f16 v189, v123, v127, v104
	v_pk_maximum3_f16 v190, v122, v126, v105
	v_pk_maximum3_f16 v192, v136, v185, v115
	v_pk_maximum3_f16 v193, v135, v184, v116
	v_pk_maximum3_f16 v154, v154, v187, v191
	v_pk_maximum3_f16 v194, v134, v183, v117
	v_pk_maximum3_f16 v155, v155, v188, v192
	v_pk_maximum3_f16 v156, v156, v189, v193
	v_pk_maximum3_f16 v157, v157, v190, v194
	v_pk_add_f16 v82, v82, v154 neg_lo:[0,1] neg_hi:[0,1]
	v_pk_add_f16 v83, v83, v155 neg_lo:[0,1] neg_hi:[0,1]
	v_pk_add_f16 v84, v84, v156 neg_lo:[0,1] neg_hi:[0,1]
	v_pk_add_f16 v85, v85, v157 neg_lo:[0,1] neg_hi:[0,1]
	v_pk_add_f16 v106, v106, v154 neg_lo:[0,1] neg_hi:[0,1]
	v_exp_f16_sdwa v187, v82 dst_sel:WORD_0 dst_unused:UNUSED_PAD src0_sel:WORD_0
	v_exp_f16_sdwa v188, v83 dst_sel:WORD_0 dst_unused:UNUSED_PAD src0_sel:WORD_0
	v_exp_f16_sdwa v189, v84 dst_sel:WORD_0 dst_unused:UNUSED_PAD src0_sel:WORD_0
	v_exp_f16_sdwa v190, v85 dst_sel:WORD_0 dst_unused:UNUSED_PAD src0_sel:WORD_0
	v_exp_f16_sdwa v187, v82 dst_sel:WORD_1 dst_unused:UNUSED_PRESERVE src0_sel:WORD_1
	v_exp_f16_sdwa v188, v83 dst_sel:WORD_1 dst_unused:UNUSED_PRESERVE src0_sel:WORD_1
	v_exp_f16_sdwa v189, v84 dst_sel:WORD_1 dst_unused:UNUSED_PRESERVE src0_sel:WORD_1
	v_exp_f16_sdwa v190, v85 dst_sel:WORD_1 dst_unused:UNUSED_PRESERVE src0_sel:WORD_1
	v_pk_add_f16 v107, v107, v155 neg_lo:[0,1] neg_hi:[0,1]
	v_pk_add_f16 v82, v190, 0
	v_pk_fma_f16 v42, v42, v187, 0
	v_pk_add_f16 v83, v189, 0
	v_pk_add_f16 v84, v188, 0
	v_pk_add_f16 v85, v187, 0
	v_pk_fma_f16 v45, v45, v190, 0
	v_pk_fma_f16 v44, v44, v189, 0
	v_pk_fma_f16 v43, v43, v188, 0
	v_pk_add_f16 v108, v108, v156 neg_lo:[0,1] neg_hi:[0,1]
	v_pk_add_f16 v109, v109, v157 neg_lo:[0,1] neg_hi:[0,1]
	v_exp_f16_sdwa v187, v106 dst_sel:WORD_0 dst_unused:UNUSED_PAD src0_sel:WORD_0
	v_exp_f16_sdwa v188, v107 dst_sel:WORD_0 dst_unused:UNUSED_PAD src0_sel:WORD_0
	v_exp_f16_sdwa v189, v108 dst_sel:WORD_0 dst_unused:UNUSED_PAD src0_sel:WORD_0
	v_exp_f16_sdwa v190, v109 dst_sel:WORD_0 dst_unused:UNUSED_PAD src0_sel:WORD_0
	v_exp_f16_sdwa v187, v106 dst_sel:WORD_1 dst_unused:UNUSED_PRESERVE src0_sel:WORD_1
	v_exp_f16_sdwa v188, v107 dst_sel:WORD_1 dst_unused:UNUSED_PRESERVE src0_sel:WORD_1
	v_exp_f16_sdwa v189, v108 dst_sel:WORD_1 dst_unused:UNUSED_PRESERVE src0_sel:WORD_1
	v_exp_f16_sdwa v190, v109 dst_sel:WORD_1 dst_unused:UNUSED_PRESERVE src0_sel:WORD_1
	s_nop 0
	v_pk_add_f16 v82, v82, v190
	v_pk_fma_f16 v42, v62, v187, v42
	v_pk_add_f16 v62, v78, v154 neg_lo:[0,1] neg_hi:[0,1]
	v_pk_add_f16 v85, v85, v187
	v_pk_add_f16 v84, v84, v188
	v_pk_add_f16 v83, v83, v189
	v_pk_fma_f16 v43, v63, v188, v43
	v_pk_fma_f16 v44, v64, v189, v44
	v_pk_fma_f16 v45, v65, v190, v45
	v_pk_add_f16 v63, v79, v155 neg_lo:[0,1] neg_hi:[0,1]
	v_pk_add_f16 v64, v80, v156 neg_lo:[0,1] neg_hi:[0,1]
	v_pk_add_f16 v65, v81, v157 neg_lo:[0,1] neg_hi:[0,1]
	v_exp_f16_sdwa v78, v62 dst_sel:WORD_0 dst_unused:UNUSED_PAD src0_sel:WORD_0
	v_exp_f16_sdwa v79, v63 dst_sel:WORD_0 dst_unused:UNUSED_PAD src0_sel:WORD_0
	v_exp_f16_sdwa v80, v64 dst_sel:WORD_0 dst_unused:UNUSED_PAD src0_sel:WORD_0
	v_exp_f16_sdwa v81, v65 dst_sel:WORD_0 dst_unused:UNUSED_PAD src0_sel:WORD_0
	v_exp_f16_sdwa v78, v62 dst_sel:WORD_1 dst_unused:UNUSED_PRESERVE src0_sel:WORD_1
	v_exp_f16_sdwa v79, v63 dst_sel:WORD_1 dst_unused:UNUSED_PRESERVE src0_sel:WORD_1
	v_exp_f16_sdwa v80, v64 dst_sel:WORD_1 dst_unused:UNUSED_PRESERVE src0_sel:WORD_1
	v_exp_f16_sdwa v81, v65 dst_sel:WORD_1 dst_unused:UNUSED_PRESERVE src0_sel:WORD_1
	s_nop 0
	v_pk_add_f16 v62, v82, v81
	v_pk_add_f16 v63, v83, v80
	v_pk_add_f16 v64, v84, v79
	v_pk_add_f16 v65, v85, v78
	v_pk_fma_f16 v45, v89, v81, v45
	v_pk_fma_f16 v44, v88, v80, v44
	v_pk_fma_f16 v43, v87, v79, v43
	v_pk_fma_f16 v42, v86, v78, v42
	v_pk_add_f16 v78, v125, v154 neg_lo:[0,1] neg_hi:[0,1]
	v_pk_add_f16 v79, v124, v155 neg_lo:[0,1] neg_hi:[0,1]
	v_pk_add_f16 v80, v123, v156 neg_lo:[0,1] neg_hi:[0,1]
	v_pk_add_f16 v81, v122, v157 neg_lo:[0,1] neg_hi:[0,1]
	v_exp_f16_sdwa v82, v78 dst_sel:WORD_0 dst_unused:UNUSED_PAD src0_sel:WORD_0
	v_exp_f16_sdwa v83, v79 dst_sel:WORD_0 dst_unused:UNUSED_PAD src0_sel:WORD_0
	v_exp_f16_sdwa v84, v80 dst_sel:WORD_0 dst_unused:UNUSED_PAD src0_sel:WORD_0
	v_exp_f16_sdwa v85, v81 dst_sel:WORD_0 dst_unused:UNUSED_PAD src0_sel:WORD_0
	v_exp_f16_sdwa v82, v78 dst_sel:WORD_1 dst_unused:UNUSED_PRESERVE src0_sel:WORD_1
	v_exp_f16_sdwa v83, v79 dst_sel:WORD_1 dst_unused:UNUSED_PRESERVE src0_sel:WORD_1
	v_exp_f16_sdwa v84, v80 dst_sel:WORD_1 dst_unused:UNUSED_PRESERVE src0_sel:WORD_1
	v_exp_f16_sdwa v85, v81 dst_sel:WORD_1 dst_unused:UNUSED_PRESERVE src0_sel:WORD_1
	v_pk_add_f16 v78, v129, v154 neg_lo:[0,1] neg_hi:[0,1]
	v_pk_add_f16 v62, v62, v85
	v_pk_add_f16 v65, v65, v82
	v_pk_add_f16 v64, v64, v83
	v_pk_add_f16 v63, v63, v84
	v_pk_fma_f16 v42, v22, v82, v42
	v_pk_fma_f16 v43, v23, v83, v43
	v_pk_fma_f16 v44, v24, v84, v44
	v_pk_fma_f16 v45, v25, v85, v45
	v_pk_add_f16 v79, v128, v155 neg_lo:[0,1] neg_hi:[0,1]
	v_pk_add_f16 v80, v127, v156 neg_lo:[0,1] neg_hi:[0,1]
	v_pk_add_f16 v81, v126, v157 neg_lo:[0,1] neg_hi:[0,1]
	v_exp_f16_sdwa v82, v78 dst_sel:WORD_0 dst_unused:UNUSED_PAD src0_sel:WORD_0
	v_exp_f16_sdwa v83, v79 dst_sel:WORD_0 dst_unused:UNUSED_PAD src0_sel:WORD_0
	v_exp_f16_sdwa v84, v80 dst_sel:WORD_0 dst_unused:UNUSED_PAD src0_sel:WORD_0
	v_exp_f16_sdwa v85, v81 dst_sel:WORD_0 dst_unused:UNUSED_PAD src0_sel:WORD_0
	v_exp_f16_sdwa v82, v78 dst_sel:WORD_1 dst_unused:UNUSED_PRESERVE src0_sel:WORD_1
	v_exp_f16_sdwa v83, v79 dst_sel:WORD_1 dst_unused:UNUSED_PRESERVE src0_sel:WORD_1
	v_exp_f16_sdwa v84, v80 dst_sel:WORD_1 dst_unused:UNUSED_PRESERVE src0_sel:WORD_1
	v_exp_f16_sdwa v85, v81 dst_sel:WORD_1 dst_unused:UNUSED_PRESERVE src0_sel:WORD_1
	v_pk_add_f16 v78, v102, v154 neg_lo:[0,1] neg_hi:[0,1]
	v_pk_add_f16 v62, v62, v85
	v_pk_add_f16 v63, v63, v84
	v_pk_add_f16 v64, v64, v83
	v_pk_add_f16 v65, v65, v82
	v_pk_fma_f16 v45, v37, v85, v45
	v_pk_fma_f16 v44, v36, v84, v44
	v_pk_fma_f16 v43, v35, v83, v43
	v_pk_fma_f16 v42, v34, v82, v42
	v_pk_add_f16 v79, v103, v155 neg_lo:[0,1] neg_hi:[0,1]
	v_pk_add_f16 v80, v104, v156 neg_lo:[0,1] neg_hi:[0,1]
	v_pk_add_f16 v81, v105, v157 neg_lo:[0,1] neg_hi:[0,1]
	v_exp_f16_sdwa v82, v78 dst_sel:WORD_0 dst_unused:UNUSED_PAD src0_sel:WORD_0
	v_exp_f16_sdwa v83, v79 dst_sel:WORD_0 dst_unused:UNUSED_PAD src0_sel:WORD_0
	v_exp_f16_sdwa v84, v80 dst_sel:WORD_0 dst_unused:UNUSED_PAD src0_sel:WORD_0
	v_exp_f16_sdwa v85, v81 dst_sel:WORD_0 dst_unused:UNUSED_PAD src0_sel:WORD_0
	v_exp_f16_sdwa v82, v78 dst_sel:WORD_1 dst_unused:UNUSED_PRESERVE src0_sel:WORD_1
	v_exp_f16_sdwa v83, v79 dst_sel:WORD_1 dst_unused:UNUSED_PRESERVE src0_sel:WORD_1
	v_exp_f16_sdwa v84, v80 dst_sel:WORD_1 dst_unused:UNUSED_PRESERVE src0_sel:WORD_1
	v_exp_f16_sdwa v85, v81 dst_sel:WORD_1 dst_unused:UNUSED_PRESERVE src0_sel:WORD_1
	v_pk_add_f16 v78, v137, v154 neg_lo:[0,1] neg_hi:[0,1]
	v_pk_add_f16 v62, v62, v85
	v_pk_add_f16 v65, v65, v82
	v_pk_add_f16 v64, v64, v83
	v_pk_add_f16 v63, v63, v84
	v_pk_fma_f16 v42, v46, v82, v42
	v_pk_fma_f16 v43, v47, v83, v43
	v_pk_fma_f16 v44, v48, v84, v44
	v_pk_fma_f16 v45, v49, v85, v45
	v_pk_add_f16 v79, v136, v155 neg_lo:[0,1] neg_hi:[0,1]
	v_pk_add_f16 v80, v135, v156 neg_lo:[0,1] neg_hi:[0,1]
	v_pk_add_f16 v81, v134, v157 neg_lo:[0,1] neg_hi:[0,1]
	v_exp_f16_sdwa v82, v78 dst_sel:WORD_0 dst_unused:UNUSED_PAD src0_sel:WORD_0
	v_exp_f16_sdwa v83, v79 dst_sel:WORD_0 dst_unused:UNUSED_PAD src0_sel:WORD_0
	v_exp_f16_sdwa v84, v80 dst_sel:WORD_0 dst_unused:UNUSED_PAD src0_sel:WORD_0
	v_exp_f16_sdwa v85, v81 dst_sel:WORD_0 dst_unused:UNUSED_PAD src0_sel:WORD_0
	v_exp_f16_sdwa v82, v78 dst_sel:WORD_1 dst_unused:UNUSED_PRESERVE src0_sel:WORD_1
	v_exp_f16_sdwa v83, v79 dst_sel:WORD_1 dst_unused:UNUSED_PRESERVE src0_sel:WORD_1
	v_exp_f16_sdwa v84, v80 dst_sel:WORD_1 dst_unused:UNUSED_PRESERVE src0_sel:WORD_1
	v_exp_f16_sdwa v85, v81 dst_sel:WORD_1 dst_unused:UNUSED_PRESERVE src0_sel:WORD_1
	v_pk_add_f16 v78, v186, v154 neg_lo:[0,1] neg_hi:[0,1]
	v_pk_add_f16 v62, v62, v85
	v_pk_add_f16 v63, v63, v84
	v_pk_add_f16 v64, v64, v83
	v_pk_add_f16 v65, v65, v82
	v_pk_fma_f16 v45, v9, v85, v45
	v_pk_fma_f16 v44, v8, v84, v44
	v_pk_fma_f16 v43, v7, v83, v43
	v_pk_fma_f16 v42, v6, v82, v42
	v_pk_add_f16 v79, v185, v155 neg_lo:[0,1] neg_hi:[0,1]
	v_pk_add_f16 v80, v184, v156 neg_lo:[0,1] neg_hi:[0,1]
	v_pk_add_f16 v81, v183, v157 neg_lo:[0,1] neg_hi:[0,1]
	v_exp_f16_sdwa v82, v78 dst_sel:WORD_0 dst_unused:UNUSED_PAD src0_sel:WORD_0
	v_exp_f16_sdwa v83, v79 dst_sel:WORD_0 dst_unused:UNUSED_PAD src0_sel:WORD_0
	v_exp_f16_sdwa v84, v80 dst_sel:WORD_0 dst_unused:UNUSED_PAD src0_sel:WORD_0
	v_exp_f16_sdwa v85, v81 dst_sel:WORD_0 dst_unused:UNUSED_PAD src0_sel:WORD_0
	v_exp_f16_sdwa v82, v78 dst_sel:WORD_1 dst_unused:UNUSED_PRESERVE src0_sel:WORD_1
	v_exp_f16_sdwa v83, v79 dst_sel:WORD_1 dst_unused:UNUSED_PRESERVE src0_sel:WORD_1
	v_exp_f16_sdwa v84, v80 dst_sel:WORD_1 dst_unused:UNUSED_PRESERVE src0_sel:WORD_1
	v_exp_f16_sdwa v85, v81 dst_sel:WORD_1 dst_unused:UNUSED_PRESERVE src0_sel:WORD_1
	v_pk_add_f16 v78, v114, v154 neg_lo:[0,1] neg_hi:[0,1]
	v_pk_add_f16 v62, v62, v85
	v_pk_add_f16 v65, v65, v82
	v_pk_add_f16 v64, v64, v83
	v_pk_add_f16 v63, v63, v84
	v_pk_fma_f16 v42, v10, v82, v42
	v_pk_fma_f16 v43, v11, v83, v43
	v_pk_fma_f16 v44, v12, v84, v44
	v_pk_fma_f16 v45, v13, v85, v45
	v_pk_add_f16 v79, v115, v155 neg_lo:[0,1] neg_hi:[0,1]
	v_pk_add_f16 v80, v116, v156 neg_lo:[0,1] neg_hi:[0,1]
	v_pk_add_f16 v81, v117, v157 neg_lo:[0,1] neg_hi:[0,1]
	v_exp_f16_sdwa v82, v78 dst_sel:WORD_0 dst_unused:UNUSED_PAD src0_sel:WORD_0
	v_exp_f16_sdwa v83, v79 dst_sel:WORD_0 dst_unused:UNUSED_PAD src0_sel:WORD_0
	v_exp_f16_sdwa v84, v80 dst_sel:WORD_0 dst_unused:UNUSED_PAD src0_sel:WORD_0
	v_exp_f16_sdwa v85, v81 dst_sel:WORD_0 dst_unused:UNUSED_PAD src0_sel:WORD_0
	v_exp_f16_sdwa v82, v78 dst_sel:WORD_1 dst_unused:UNUSED_PRESERVE src0_sel:WORD_1
	v_exp_f16_sdwa v83, v79 dst_sel:WORD_1 dst_unused:UNUSED_PRESERVE src0_sel:WORD_1
	v_exp_f16_sdwa v84, v80 dst_sel:WORD_1 dst_unused:UNUSED_PRESERVE src0_sel:WORD_1
	v_exp_f16_sdwa v85, v81 dst_sel:WORD_1 dst_unused:UNUSED_PRESERVE src0_sel:WORD_1
	s_nop 0
	v_pk_add_f16 v62, v62, v85
	v_pk_add_f16 v63, v63, v84
	v_pk_add_f16 v64, v64, v83
	v_pk_add_f16 v65, v65, v82
	v_rcp_f16_e32 v81, v62
	v_rcp_f16_sdwa v62, v62 dst_sel:DWORD dst_unused:UNUSED_PAD src0_sel:WORD_1
	v_rcp_f16_e32 v78, v65
	v_rcp_f16_sdwa v65, v65 dst_sel:DWORD dst_unused:UNUSED_PAD src0_sel:WORD_1
	v_rcp_f16_e32 v79, v64
	v_rcp_f16_sdwa v64, v64 dst_sel:DWORD dst_unused:UNUSED_PAD src0_sel:WORD_1
	v_rcp_f16_e32 v80, v63
	v_rcp_f16_sdwa v63, v63 dst_sel:DWORD dst_unused:UNUSED_PAD src0_sel:WORD_1
	v_pk_fma_f16 v45, v17, v85, v45
	v_pack_b32_f16 v62, v81, v62
	v_pk_fma_f16 v44, v16, v84, v44
	v_pk_fma_f16 v43, v15, v83, v43
	v_pk_fma_f16 v42, v14, v82, v42
	v_pack_b32_f16 v65, v78, v65
	v_pack_b32_f16 v64, v79, v64
	v_pack_b32_f16 v63, v80, v63
	v_pk_mul_f16 v45, v45, v62
	s_waitcnt vmcnt(6)
	v_pk_mul_f16 v62, v182, v150 op_sel_hi:[0,1]
	v_pk_mul_f16 v42, v42, v65
	v_pk_mul_f16 v43, v43, v64
	v_pk_mul_f16 v44, v44, v63
	v_pk_mul_f16 v63, v182, v151 op_sel_hi:[0,1]
	v_pk_mul_f16 v64, v182, v152 op_sel_hi:[0,1]
	v_pk_mul_f16 v65, v182, v153 op_sel_hi:[0,1]
	v_pk_mul_f16 v78, v180, v150 op_sel_hi:[0,1]
	v_pk_mul_f16 v82, v181, v150 op_sel_hi:[0,1]
	v_pk_fma_f16 v50, v50, v150, v62
	v_pk_fma_f16 v66, v66, v150, v62
	v_pk_fma_f16 v62, v94, v150, v62
	v_pk_mul_f16 v79, v180, v151 op_sel_hi:[0,1]
	v_pk_maximum3_f16 v114, v50, v66, v62
	v_pk_mul_f16 v80, v180, v152 op_sel_hi:[0,1]
	v_pk_mul_f16 v81, v180, v153 op_sel_hi:[0,1]
	v_pk_mul_f16 v83, v181, v151 op_sel_hi:[0,1]
	v_pk_mul_f16 v84, v181, v152 op_sel_hi:[0,1]
	v_pk_mul_f16 v85, v181, v153 op_sel_hi:[0,1]
	v_pk_fma_f16 v53, v53, v153, v65
	v_pk_fma_f16 v52, v52, v152, v64
	v_pk_fma_f16 v51, v51, v151, v63
	v_pk_fma_f16 v69, v69, v153, v65
	v_pk_fma_f16 v68, v68, v152, v64
	v_pk_fma_f16 v67, v67, v151, v63
	v_pk_fma_f16 v65, v97, v153, v65
	v_pk_fma_f16 v64, v96, v152, v64
	v_pk_fma_f16 v63, v95, v151, v63
	v_pk_fma_f16 v89, v18, v150, v78
	v_pk_fma_f16 v97, v30, v150, v78
	v_pk_fma_f16 v78, v54, v150, v78
	v_pk_fma_f16 v105, v74, v150, v82
	v_pk_fma_f16 v109, v98, v150, v82
	v_pk_fma_f16 v82, v118, v150, v82
	v_pk_maximum3_f16 v115, v51, v67, v63
	v_pk_maximum3_f16 v116, v52, v68, v64
	v_pk_maximum3_f16 v117, v53, v69, v65
	v_pk_maximum3_f16 v122, v89, v97, v78
	v_pk_fma_f16 v86, v21, v153, v81
	v_pk_maximum3_f16 v126, v105, v109, v82
	v_pk_fma_f16 v87, v20, v152, v80
	v_pk_maximum3_f16 v114, v114, v122, v126
	v_pk_fma_f16 v88, v19, v151, v79
	v_pk_fma_f16 v94, v33, v153, v81
	v_pk_fma_f16 v95, v32, v152, v80
	v_pk_fma_f16 v96, v31, v151, v79
	v_pk_fma_f16 v81, v57, v153, v81
	v_pk_fma_f16 v80, v56, v152, v80
	v_pk_fma_f16 v79, v55, v151, v79
	v_pk_fma_f16 v102, v77, v153, v85
	v_pk_fma_f16 v103, v76, v152, v84
	v_pk_fma_f16 v104, v75, v151, v83
	v_pk_fma_f16 v106, v101, v153, v85
	v_pk_fma_f16 v107, v100, v152, v84
	v_pk_fma_f16 v108, v99, v151, v83
	v_pk_fma_f16 v85, v121, v153, v85
	v_pk_fma_f16 v84, v120, v152, v84
	v_pk_fma_f16 v83, v119, v151, v83
	v_pk_maximum3_f16 v123, v88, v96, v79
	v_pk_maximum3_f16 v124, v87, v95, v80
	v_pk_maximum3_f16 v125, v86, v94, v81
	v_pk_maximum3_f16 v128, v103, v107, v84
	v_pk_maximum3_f16 v129, v102, v106, v85
	v_pk_maximum3_f16 v127, v104, v108, v83
	v_pk_maximum3_f16 v115, v115, v123, v127
	v_pk_maximum3_f16 v116, v116, v124, v128
	v_pk_maximum3_f16 v117, v117, v125, v129
	v_pk_add_f16 v50, v50, v114 neg_lo:[0,1] neg_hi:[0,1]
	v_pk_add_f16 v51, v51, v115 neg_lo:[0,1] neg_hi:[0,1]
	v_pk_add_f16 v52, v52, v116 neg_lo:[0,1] neg_hi:[0,1]
	v_pk_add_f16 v53, v53, v117 neg_lo:[0,1] neg_hi:[0,1]
	v_pk_add_f16 v66, v66, v114 neg_lo:[0,1] neg_hi:[0,1]
	v_exp_f16_sdwa v122, v50 dst_sel:WORD_0 dst_unused:UNUSED_PAD src0_sel:WORD_0
	v_exp_f16_sdwa v123, v51 dst_sel:WORD_0 dst_unused:UNUSED_PAD src0_sel:WORD_0
	v_exp_f16_sdwa v124, v52 dst_sel:WORD_0 dst_unused:UNUSED_PAD src0_sel:WORD_0
	v_exp_f16_sdwa v125, v53 dst_sel:WORD_0 dst_unused:UNUSED_PAD src0_sel:WORD_0
	v_exp_f16_sdwa v122, v50 dst_sel:WORD_1 dst_unused:UNUSED_PRESERVE src0_sel:WORD_1
	v_exp_f16_sdwa v123, v51 dst_sel:WORD_1 dst_unused:UNUSED_PRESERVE src0_sel:WORD_1
	v_exp_f16_sdwa v124, v52 dst_sel:WORD_1 dst_unused:UNUSED_PRESERVE src0_sel:WORD_1
	v_exp_f16_sdwa v125, v53 dst_sel:WORD_1 dst_unused:UNUSED_PRESERVE src0_sel:WORD_1
	v_pk_add_f16 v67, v67, v115 neg_lo:[0,1] neg_hi:[0,1]
	v_pk_add_f16 v50, v125, 0
	v_pk_fma_f16 v22, v22, v122, 0
	v_pk_add_f16 v51, v124, 0
	v_pk_add_f16 v52, v123, 0
	v_pk_add_f16 v53, v122, 0
	v_pk_fma_f16 v23, v23, v123, 0
	v_pk_fma_f16 v24, v24, v124, 0
	v_pk_fma_f16 v25, v25, v125, 0
	v_pk_add_f16 v68, v68, v116 neg_lo:[0,1] neg_hi:[0,1]
	v_pk_add_f16 v69, v69, v117 neg_lo:[0,1] neg_hi:[0,1]
	v_exp_f16_sdwa v122, v66 dst_sel:WORD_0 dst_unused:UNUSED_PAD src0_sel:WORD_0
	v_exp_f16_sdwa v123, v67 dst_sel:WORD_0 dst_unused:UNUSED_PAD src0_sel:WORD_0
	v_exp_f16_sdwa v124, v68 dst_sel:WORD_0 dst_unused:UNUSED_PAD src0_sel:WORD_0
	v_exp_f16_sdwa v125, v69 dst_sel:WORD_0 dst_unused:UNUSED_PAD src0_sel:WORD_0
	v_exp_f16_sdwa v122, v66 dst_sel:WORD_1 dst_unused:UNUSED_PRESERVE src0_sel:WORD_1
	v_exp_f16_sdwa v123, v67 dst_sel:WORD_1 dst_unused:UNUSED_PRESERVE src0_sel:WORD_1
	v_exp_f16_sdwa v124, v68 dst_sel:WORD_1 dst_unused:UNUSED_PRESERVE src0_sel:WORD_1
	v_exp_f16_sdwa v125, v69 dst_sel:WORD_1 dst_unused:UNUSED_PRESERVE src0_sel:WORD_1
	s_nop 0
	v_pk_add_f16 v50, v50, v125
	v_pk_fma_f16 v22, v34, v122, v22
	v_pk_add_f16 v34, v62, v114 neg_lo:[0,1] neg_hi:[0,1]
	v_pk_add_f16 v53, v53, v122
	v_pk_add_f16 v52, v52, v123
	v_pk_add_f16 v51, v51, v124
	v_pk_fma_f16 v25, v37, v125, v25
	v_pk_fma_f16 v24, v36, v124, v24
	v_pk_fma_f16 v23, v35, v123, v23
	v_pk_add_f16 v35, v63, v115 neg_lo:[0,1] neg_hi:[0,1]
	v_pk_add_f16 v36, v64, v116 neg_lo:[0,1] neg_hi:[0,1]
	v_pk_add_f16 v37, v65, v117 neg_lo:[0,1] neg_hi:[0,1]
	v_exp_f16_sdwa v62, v34 dst_sel:WORD_0 dst_unused:UNUSED_PAD src0_sel:WORD_0
	v_exp_f16_sdwa v63, v35 dst_sel:WORD_0 dst_unused:UNUSED_PAD src0_sel:WORD_0
	v_exp_f16_sdwa v64, v36 dst_sel:WORD_0 dst_unused:UNUSED_PAD src0_sel:WORD_0
	v_exp_f16_sdwa v65, v37 dst_sel:WORD_0 dst_unused:UNUSED_PAD src0_sel:WORD_0
	v_exp_f16_sdwa v62, v34 dst_sel:WORD_1 dst_unused:UNUSED_PRESERVE src0_sel:WORD_1
	v_exp_f16_sdwa v63, v35 dst_sel:WORD_1 dst_unused:UNUSED_PRESERVE src0_sel:WORD_1
	v_exp_f16_sdwa v64, v36 dst_sel:WORD_1 dst_unused:UNUSED_PRESERVE src0_sel:WORD_1
	v_exp_f16_sdwa v65, v37 dst_sel:WORD_1 dst_unused:UNUSED_PRESERVE src0_sel:WORD_1
	s_nop 0
	v_pk_add_f16 v34, v50, v65
	v_pk_add_f16 v35, v51, v64
	v_pk_add_f16 v36, v52, v63
	v_pk_add_f16 v37, v53, v62
	v_pk_fma_f16 v22, v46, v62, v22
	v_pk_fma_f16 v23, v47, v63, v23
	v_pk_fma_f16 v24, v48, v64, v24
	v_pk_fma_f16 v25, v49, v65, v25
	v_pk_add_f16 v46, v89, v114 neg_lo:[0,1] neg_hi:[0,1]
	v_pk_add_f16 v47, v88, v115 neg_lo:[0,1] neg_hi:[0,1]
	v_pk_add_f16 v48, v87, v116 neg_lo:[0,1] neg_hi:[0,1]
	v_pk_add_f16 v49, v86, v117 neg_lo:[0,1] neg_hi:[0,1]
	v_exp_f16_sdwa v50, v46 dst_sel:WORD_0 dst_unused:UNUSED_PAD src0_sel:WORD_0
	v_exp_f16_sdwa v51, v47 dst_sel:WORD_0 dst_unused:UNUSED_PAD src0_sel:WORD_0
	v_exp_f16_sdwa v52, v48 dst_sel:WORD_0 dst_unused:UNUSED_PAD src0_sel:WORD_0
	v_exp_f16_sdwa v53, v49 dst_sel:WORD_0 dst_unused:UNUSED_PAD src0_sel:WORD_0
	v_exp_f16_sdwa v50, v46 dst_sel:WORD_1 dst_unused:UNUSED_PRESERVE src0_sel:WORD_1
	v_exp_f16_sdwa v51, v47 dst_sel:WORD_1 dst_unused:UNUSED_PRESERVE src0_sel:WORD_1
	v_exp_f16_sdwa v52, v48 dst_sel:WORD_1 dst_unused:UNUSED_PRESERVE src0_sel:WORD_1
	v_exp_f16_sdwa v53, v49 dst_sel:WORD_1 dst_unused:UNUSED_PRESERVE src0_sel:WORD_1
	v_pk_add_f16 v46, v97, v114 neg_lo:[0,1] neg_hi:[0,1]
	v_pk_add_f16 v34, v34, v53
	v_pk_add_f16 v37, v37, v50
	v_pk_add_f16 v36, v36, v51
	v_pk_add_f16 v35, v35, v52
	v_pk_fma_f16 v25, v9, v53, v25
	v_pk_fma_f16 v24, v8, v52, v24
	v_pk_fma_f16 v23, v7, v51, v23
	v_pk_fma_f16 v22, v6, v50, v22
	v_pk_add_f16 v47, v96, v115 neg_lo:[0,1] neg_hi:[0,1]
	v_pk_add_f16 v48, v95, v116 neg_lo:[0,1] neg_hi:[0,1]
	v_pk_add_f16 v49, v94, v117 neg_lo:[0,1] neg_hi:[0,1]
	v_exp_f16_sdwa v50, v46 dst_sel:WORD_0 dst_unused:UNUSED_PAD src0_sel:WORD_0
	v_exp_f16_sdwa v51, v47 dst_sel:WORD_0 dst_unused:UNUSED_PAD src0_sel:WORD_0
	v_exp_f16_sdwa v52, v48 dst_sel:WORD_0 dst_unused:UNUSED_PAD src0_sel:WORD_0
	v_exp_f16_sdwa v53, v49 dst_sel:WORD_0 dst_unused:UNUSED_PAD src0_sel:WORD_0
	v_exp_f16_sdwa v50, v46 dst_sel:WORD_1 dst_unused:UNUSED_PRESERVE src0_sel:WORD_1
	v_exp_f16_sdwa v51, v47 dst_sel:WORD_1 dst_unused:UNUSED_PRESERVE src0_sel:WORD_1
	v_exp_f16_sdwa v52, v48 dst_sel:WORD_1 dst_unused:UNUSED_PRESERVE src0_sel:WORD_1
	v_exp_f16_sdwa v53, v49 dst_sel:WORD_1 dst_unused:UNUSED_PRESERVE src0_sel:WORD_1
	v_pk_add_f16 v46, v78, v114 neg_lo:[0,1] neg_hi:[0,1]
	v_pk_add_f16 v34, v34, v53
	v_pk_add_f16 v35, v35, v52
	v_pk_add_f16 v36, v36, v51
	v_pk_add_f16 v37, v37, v50
	v_pk_fma_f16 v22, v10, v50, v22
	v_pk_fma_f16 v23, v11, v51, v23
	v_pk_fma_f16 v24, v12, v52, v24
	v_pk_fma_f16 v25, v13, v53, v25
	v_pk_add_f16 v47, v79, v115 neg_lo:[0,1] neg_hi:[0,1]
	v_pk_add_f16 v48, v80, v116 neg_lo:[0,1] neg_hi:[0,1]
	v_pk_add_f16 v49, v81, v117 neg_lo:[0,1] neg_hi:[0,1]
	v_exp_f16_sdwa v50, v46 dst_sel:WORD_0 dst_unused:UNUSED_PAD src0_sel:WORD_0
	v_exp_f16_sdwa v51, v47 dst_sel:WORD_0 dst_unused:UNUSED_PAD src0_sel:WORD_0
	v_exp_f16_sdwa v52, v48 dst_sel:WORD_0 dst_unused:UNUSED_PAD src0_sel:WORD_0
	v_exp_f16_sdwa v53, v49 dst_sel:WORD_0 dst_unused:UNUSED_PAD src0_sel:WORD_0
	v_exp_f16_sdwa v50, v46 dst_sel:WORD_1 dst_unused:UNUSED_PRESERVE src0_sel:WORD_1
	v_exp_f16_sdwa v51, v47 dst_sel:WORD_1 dst_unused:UNUSED_PRESERVE src0_sel:WORD_1
	v_exp_f16_sdwa v52, v48 dst_sel:WORD_1 dst_unused:UNUSED_PRESERVE src0_sel:WORD_1
	v_exp_f16_sdwa v53, v49 dst_sel:WORD_1 dst_unused:UNUSED_PRESERVE src0_sel:WORD_1
	v_pk_add_f16 v46, v105, v114 neg_lo:[0,1] neg_hi:[0,1]
	v_pk_add_f16 v34, v34, v53
	v_pk_add_f16 v37, v37, v50
	v_pk_add_f16 v36, v36, v51
	v_pk_add_f16 v35, v35, v52
	v_pk_fma_f16 v25, v17, v53, v25
	v_pk_fma_f16 v24, v16, v52, v24
	v_pk_fma_f16 v23, v15, v51, v23
	v_pk_fma_f16 v22, v14, v50, v22
	v_pk_add_f16 v47, v104, v115 neg_lo:[0,1] neg_hi:[0,1]
	v_pk_add_f16 v48, v103, v116 neg_lo:[0,1] neg_hi:[0,1]
	v_pk_add_f16 v49, v102, v117 neg_lo:[0,1] neg_hi:[0,1]
	v_exp_f16_sdwa v50, v46 dst_sel:WORD_0 dst_unused:UNUSED_PAD src0_sel:WORD_0
	v_exp_f16_sdwa v51, v47 dst_sel:WORD_0 dst_unused:UNUSED_PAD src0_sel:WORD_0
	v_exp_f16_sdwa v52, v48 dst_sel:WORD_0 dst_unused:UNUSED_PAD src0_sel:WORD_0
	v_exp_f16_sdwa v53, v49 dst_sel:WORD_0 dst_unused:UNUSED_PAD src0_sel:WORD_0
	v_exp_f16_sdwa v50, v46 dst_sel:WORD_1 dst_unused:UNUSED_PRESERVE src0_sel:WORD_1
	v_exp_f16_sdwa v51, v47 dst_sel:WORD_1 dst_unused:UNUSED_PRESERVE src0_sel:WORD_1
	v_exp_f16_sdwa v52, v48 dst_sel:WORD_1 dst_unused:UNUSED_PRESERVE src0_sel:WORD_1
	v_exp_f16_sdwa v53, v49 dst_sel:WORD_1 dst_unused:UNUSED_PRESERVE src0_sel:WORD_1
	v_pk_add_f16 v46, v109, v114 neg_lo:[0,1] neg_hi:[0,1]
	v_pk_add_f16 v34, v34, v53
	v_pk_add_f16 v35, v35, v52
	v_pk_add_f16 v36, v36, v51
	v_pk_add_f16 v37, v37, v50
	v_pk_fma_f16 v22, v26, v50, v22
	v_pk_fma_f16 v23, v27, v51, v23
	v_pk_fma_f16 v24, v28, v52, v24
	v_pk_fma_f16 v25, v29, v53, v25
	v_pk_add_f16 v47, v108, v115 neg_lo:[0,1] neg_hi:[0,1]
	v_pk_add_f16 v48, v107, v116 neg_lo:[0,1] neg_hi:[0,1]
	v_pk_add_f16 v49, v106, v117 neg_lo:[0,1] neg_hi:[0,1]
	v_exp_f16_sdwa v50, v46 dst_sel:WORD_0 dst_unused:UNUSED_PAD src0_sel:WORD_0
	v_exp_f16_sdwa v51, v47 dst_sel:WORD_0 dst_unused:UNUSED_PAD src0_sel:WORD_0
	v_exp_f16_sdwa v52, v48 dst_sel:WORD_0 dst_unused:UNUSED_PAD src0_sel:WORD_0
	v_exp_f16_sdwa v53, v49 dst_sel:WORD_0 dst_unused:UNUSED_PAD src0_sel:WORD_0
	v_exp_f16_sdwa v50, v46 dst_sel:WORD_1 dst_unused:UNUSED_PRESERVE src0_sel:WORD_1
	v_exp_f16_sdwa v51, v47 dst_sel:WORD_1 dst_unused:UNUSED_PRESERVE src0_sel:WORD_1
	v_exp_f16_sdwa v52, v48 dst_sel:WORD_1 dst_unused:UNUSED_PRESERVE src0_sel:WORD_1
	v_exp_f16_sdwa v53, v49 dst_sel:WORD_1 dst_unused:UNUSED_PRESERVE src0_sel:WORD_1
	v_pk_add_f16 v46, v82, v114 neg_lo:[0,1] neg_hi:[0,1]
	v_pk_add_f16 v34, v34, v53
	v_pk_add_f16 v37, v37, v50
	v_pk_add_f16 v36, v36, v51
	v_pk_add_f16 v35, v35, v52
	v_pk_fma_f16 v25, v41, v53, v25
	v_pk_fma_f16 v24, v40, v52, v24
	v_pk_fma_f16 v23, v39, v51, v23
	v_pk_fma_f16 v22, v38, v50, v22
	v_pk_add_f16 v47, v83, v115 neg_lo:[0,1] neg_hi:[0,1]
	v_pk_add_f16 v48, v84, v116 neg_lo:[0,1] neg_hi:[0,1]
	v_pk_add_f16 v49, v85, v117 neg_lo:[0,1] neg_hi:[0,1]
	v_exp_f16_sdwa v50, v46 dst_sel:WORD_0 dst_unused:UNUSED_PAD src0_sel:WORD_0
	v_exp_f16_sdwa v51, v47 dst_sel:WORD_0 dst_unused:UNUSED_PAD src0_sel:WORD_0
	v_exp_f16_sdwa v52, v48 dst_sel:WORD_0 dst_unused:UNUSED_PAD src0_sel:WORD_0
	v_exp_f16_sdwa v53, v49 dst_sel:WORD_0 dst_unused:UNUSED_PAD src0_sel:WORD_0
	v_exp_f16_sdwa v50, v46 dst_sel:WORD_1 dst_unused:UNUSED_PRESERVE src0_sel:WORD_1
	v_exp_f16_sdwa v51, v47 dst_sel:WORD_1 dst_unused:UNUSED_PRESERVE src0_sel:WORD_1
	v_exp_f16_sdwa v52, v48 dst_sel:WORD_1 dst_unused:UNUSED_PRESERVE src0_sel:WORD_1
	v_exp_f16_sdwa v53, v49 dst_sel:WORD_1 dst_unused:UNUSED_PRESERVE src0_sel:WORD_1
	s_nop 0
	v_pk_add_f16 v34, v34, v53
	v_pk_add_f16 v35, v35, v52
	v_rcp_f16_e32 v48, v34
	v_rcp_f16_sdwa v34, v34 dst_sel:DWORD dst_unused:UNUSED_PAD src0_sel:WORD_1
	v_pk_add_f16 v36, v36, v51
	v_rcp_f16_e32 v49, v35
	v_rcp_f16_sdwa v35, v35 dst_sel:DWORD dst_unused:UNUSED_PAD src0_sel:WORD_1
	v_pk_add_f16 v37, v37, v50
	v_rcp_f16_e32 v47, v36
	v_rcp_f16_sdwa v36, v36 dst_sel:DWORD dst_unused:UNUSED_PAD src0_sel:WORD_1
	v_rcp_f16_e32 v46, v37
	v_rcp_f16_sdwa v37, v37 dst_sel:DWORD dst_unused:UNUSED_PAD src0_sel:WORD_1
	v_pk_fma_f16 v25, v61, v53, v25
	v_pack_b32_f16 v34, v48, v34
	v_pk_fma_f16 v24, v60, v52, v24
	v_pk_mul_f16 v25, v25, v34
	v_pack_b32_f16 v34, v49, v35
	v_pk_fma_f16 v23, v59, v51, v23
	v_pk_mul_f16 v24, v24, v34
	v_pack_b32_f16 v34, v47, v36
	v_pk_fma_f16 v22, v58, v50, v22
	v_pk_mul_f16 v23, v23, v34
	v_pack_b32_f16 v34, v46, v37
	v_pk_mul_f16 v22, v22, v34
	s_waitcnt vmcnt(0)
	v_pk_mul_f16 v34, v182, v146 op_sel_hi:[0,1]
	v_pk_mul_f16 v35, v182, v147 op_sel_hi:[0,1]
	v_pk_mul_f16 v36, v182, v148 op_sel_hi:[0,1]
	v_pk_mul_f16 v37, v182, v149 op_sel_hi:[0,1]
	v_pk_mul_f16 v46, v180, v146 op_sel_hi:[0,1]
	v_pk_mul_f16 v47, v180, v147 op_sel_hi:[0,1]
	v_pk_mul_f16 v48, v180, v148 op_sel_hi:[0,1]
	v_pk_mul_f16 v49, v180, v149 op_sel_hi:[0,1]
	v_pk_mul_f16 v50, v181, v146 op_sel_hi:[0,1]
	v_pk_mul_f16 v51, v181, v147 op_sel_hi:[0,1]
	v_pk_mul_f16 v52, v181, v148 op_sel_hi:[0,1]
	v_pk_mul_f16 v53, v181, v149 op_sel_hi:[0,1]
	v_pk_fma_f16 v21, v21, v149, v37
	v_pk_fma_f16 v20, v20, v148, v36
	v_pk_fma_f16 v19, v19, v147, v35
	v_pk_fma_f16 v18, v18, v146, v34
	v_pk_fma_f16 v33, v33, v149, v37
	v_pk_fma_f16 v32, v32, v148, v36
	v_pk_fma_f16 v31, v31, v147, v35
	v_pk_fma_f16 v30, v30, v146, v34
	v_pk_fma_f16 v37, v57, v149, v37
	v_pk_fma_f16 v36, v56, v148, v36
	v_pk_fma_f16 v35, v55, v147, v35
	v_pk_fma_f16 v34, v54, v146, v34
	v_pk_maximum3_f16 v79, v19, v31, v35
	v_pk_maximum3_f16 v80, v20, v32, v36
	v_pk_maximum3_f16 v81, v21, v33, v37
	v_pk_fma_f16 v54, v77, v149, v49
	v_pk_maximum3_f16 v78, v18, v30, v34
	v_pk_fma_f16 v55, v76, v148, v48
	v_pk_fma_f16 v56, v75, v147, v47
	v_pk_fma_f16 v57, v74, v146, v46
	v_pk_fma_f16 v62, v101, v149, v49
	v_pk_fma_f16 v63, v100, v148, v48
	v_pk_fma_f16 v64, v99, v147, v47
	v_pk_fma_f16 v65, v98, v146, v46
	v_pk_fma_f16 v49, v121, v149, v49
	v_pk_fma_f16 v48, v120, v148, v48
	v_pk_fma_f16 v47, v119, v147, v47
	v_pk_fma_f16 v46, v118, v146, v46
	v_pk_fma_f16 v66, v133, v149, v53
	v_pk_fma_f16 v67, v132, v148, v52
	v_pk_fma_f16 v68, v131, v147, v51
	v_pk_fma_f16 v69, v130, v146, v50
	v_pk_fma_f16 v74, v141, v149, v53
	v_pk_fma_f16 v75, v140, v148, v52
	v_pk_fma_f16 v76, v139, v147, v51
	v_pk_fma_f16 v77, v138, v146, v50
	v_pk_fma_f16 v53, v145, v149, v53
	v_pk_fma_f16 v52, v144, v148, v52
	v_pk_fma_f16 v51, v143, v147, v51
	v_pk_fma_f16 v50, v142, v146, v50
	v_pk_maximum3_f16 v82, v57, v65, v46
	v_pk_maximum3_f16 v83, v56, v64, v47
	v_pk_maximum3_f16 v84, v55, v63, v48
	v_pk_maximum3_f16 v85, v54, v62, v49
	v_pk_maximum3_f16 v87, v68, v76, v51
	v_pk_maximum3_f16 v86, v69, v77, v50
	v_pk_maximum3_f16 v88, v67, v75, v52
	v_pk_maximum3_f16 v89, v66, v74, v53
	v_pk_maximum3_f16 v78, v78, v82, v86
	v_pk_maximum3_f16 v79, v79, v83, v87
	v_pk_maximum3_f16 v80, v80, v84, v88
	v_pk_maximum3_f16 v81, v81, v85, v89
	s_nop 0
	v_pk_add_f16 v18, v18, v78 neg_lo:[0,1] neg_hi:[0,1]
	v_pk_add_f16 v19, v19, v79 neg_lo:[0,1] neg_hi:[0,1]
	v_pk_add_f16 v20, v20, v80 neg_lo:[0,1] neg_hi:[0,1]
	v_pk_add_f16 v21, v21, v81 neg_lo:[0,1] neg_hi:[0,1]
	v_pk_add_f16 v30, v30, v78 neg_lo:[0,1] neg_hi:[0,1]
	v_exp_f16_sdwa v82, v18 dst_sel:WORD_0 dst_unused:UNUSED_PAD src0_sel:WORD_0
	v_exp_f16_sdwa v83, v19 dst_sel:WORD_0 dst_unused:UNUSED_PAD src0_sel:WORD_0
	v_exp_f16_sdwa v84, v20 dst_sel:WORD_0 dst_unused:UNUSED_PAD src0_sel:WORD_0
	v_exp_f16_sdwa v85, v21 dst_sel:WORD_0 dst_unused:UNUSED_PAD src0_sel:WORD_0
	v_exp_f16_sdwa v82, v18 dst_sel:WORD_1 dst_unused:UNUSED_PRESERVE src0_sel:WORD_1
	v_exp_f16_sdwa v83, v19 dst_sel:WORD_1 dst_unused:UNUSED_PRESERVE src0_sel:WORD_1
	v_exp_f16_sdwa v84, v20 dst_sel:WORD_1 dst_unused:UNUSED_PRESERVE src0_sel:WORD_1
	v_exp_f16_sdwa v85, v21 dst_sel:WORD_1 dst_unused:UNUSED_PRESERVE src0_sel:WORD_1
	v_pk_add_f16 v31, v31, v79 neg_lo:[0,1] neg_hi:[0,1]
	v_pk_add_f16 v18, v82, 0
	v_pk_add_f16 v19, v83, 0
	v_pk_add_f16 v20, v84, 0
	v_pk_add_f16 v21, v85, 0
	v_pk_fma_f16 v6, v6, v82, 0
	v_pk_fma_f16 v7, v7, v83, 0
	v_pk_fma_f16 v8, v8, v84, 0
	v_pk_fma_f16 v9, v9, v85, 0
	v_pk_add_f16 v32, v32, v80 neg_lo:[0,1] neg_hi:[0,1]
	v_pk_add_f16 v33, v33, v81 neg_lo:[0,1] neg_hi:[0,1]
	v_exp_f16_sdwa v82, v30 dst_sel:WORD_0 dst_unused:UNUSED_PAD src0_sel:WORD_0
	v_exp_f16_sdwa v83, v31 dst_sel:WORD_0 dst_unused:UNUSED_PAD src0_sel:WORD_0
	v_exp_f16_sdwa v84, v32 dst_sel:WORD_0 dst_unused:UNUSED_PAD src0_sel:WORD_0
	v_exp_f16_sdwa v85, v33 dst_sel:WORD_0 dst_unused:UNUSED_PAD src0_sel:WORD_0
	v_exp_f16_sdwa v82, v30 dst_sel:WORD_1 dst_unused:UNUSED_PRESERVE src0_sel:WORD_1
	v_exp_f16_sdwa v83, v31 dst_sel:WORD_1 dst_unused:UNUSED_PRESERVE src0_sel:WORD_1
	v_exp_f16_sdwa v84, v32 dst_sel:WORD_1 dst_unused:UNUSED_PRESERVE src0_sel:WORD_1
	v_exp_f16_sdwa v85, v33 dst_sel:WORD_1 dst_unused:UNUSED_PRESERVE src0_sel:WORD_1
	s_nop 0
	v_pk_add_f16 v21, v21, v85
	v_pk_add_f16 v20, v20, v84
	v_pk_add_f16 v19, v19, v83
	v_pk_add_f16 v18, v18, v82
	v_pk_fma_f16 v9, v13, v85, v9
	v_pk_fma_f16 v8, v12, v84, v8
	v_pk_fma_f16 v7, v11, v83, v7
	v_pk_fma_f16 v6, v10, v82, v6
	v_pk_add_f16 v10, v34, v78 neg_lo:[0,1] neg_hi:[0,1]
	v_pk_add_f16 v11, v35, v79 neg_lo:[0,1] neg_hi:[0,1]
	v_pk_add_f16 v12, v36, v80 neg_lo:[0,1] neg_hi:[0,1]
	v_pk_add_f16 v13, v37, v81 neg_lo:[0,1] neg_hi:[0,1]
	v_exp_f16_sdwa v30, v10 dst_sel:WORD_0 dst_unused:UNUSED_PAD src0_sel:WORD_0
	v_exp_f16_sdwa v31, v11 dst_sel:WORD_0 dst_unused:UNUSED_PAD src0_sel:WORD_0
	v_exp_f16_sdwa v32, v12 dst_sel:WORD_0 dst_unused:UNUSED_PAD src0_sel:WORD_0
	v_exp_f16_sdwa v33, v13 dst_sel:WORD_0 dst_unused:UNUSED_PAD src0_sel:WORD_0
	v_exp_f16_sdwa v30, v10 dst_sel:WORD_1 dst_unused:UNUSED_PRESERVE src0_sel:WORD_1
	v_exp_f16_sdwa v31, v11 dst_sel:WORD_1 dst_unused:UNUSED_PRESERVE src0_sel:WORD_1
	v_exp_f16_sdwa v32, v12 dst_sel:WORD_1 dst_unused:UNUSED_PRESERVE src0_sel:WORD_1
	v_exp_f16_sdwa v33, v13 dst_sel:WORD_1 dst_unused:UNUSED_PRESERVE src0_sel:WORD_1
	v_pk_add_f16 v10, v18, v30
	v_pk_add_f16 v11, v19, v31
	v_pk_add_f16 v12, v20, v32
	v_pk_add_f16 v13, v21, v33
	v_pk_fma_f16 v6, v14, v30, v6
	v_pk_fma_f16 v7, v15, v31, v7
	v_pk_fma_f16 v8, v16, v32, v8
	v_pk_fma_f16 v9, v17, v33, v9
	v_pk_add_f16 v14, v57, v78 neg_lo:[0,1] neg_hi:[0,1]
	v_pk_add_f16 v15, v56, v79 neg_lo:[0,1] neg_hi:[0,1]
	v_pk_add_f16 v16, v55, v80 neg_lo:[0,1] neg_hi:[0,1]
	v_pk_add_f16 v17, v54, v81 neg_lo:[0,1] neg_hi:[0,1]
	v_exp_f16_sdwa v18, v14 dst_sel:WORD_0 dst_unused:UNUSED_PAD src0_sel:WORD_0
	v_exp_f16_sdwa v19, v15 dst_sel:WORD_0 dst_unused:UNUSED_PAD src0_sel:WORD_0
	v_exp_f16_sdwa v20, v16 dst_sel:WORD_0 dst_unused:UNUSED_PAD src0_sel:WORD_0
	v_exp_f16_sdwa v21, v17 dst_sel:WORD_0 dst_unused:UNUSED_PAD src0_sel:WORD_0
	v_exp_f16_sdwa v18, v14 dst_sel:WORD_1 dst_unused:UNUSED_PRESERVE src0_sel:WORD_1
	v_exp_f16_sdwa v19, v15 dst_sel:WORD_1 dst_unused:UNUSED_PRESERVE src0_sel:WORD_1
	v_exp_f16_sdwa v20, v16 dst_sel:WORD_1 dst_unused:UNUSED_PRESERVE src0_sel:WORD_1
	v_exp_f16_sdwa v21, v17 dst_sel:WORD_1 dst_unused:UNUSED_PRESERVE src0_sel:WORD_1
	v_pk_add_f16 v14, v65, v78 neg_lo:[0,1] neg_hi:[0,1]
	v_pk_add_f16 v13, v13, v21
	v_pk_add_f16 v12, v12, v20
	v_pk_add_f16 v11, v11, v19
	v_pk_add_f16 v10, v10, v18
	v_pk_fma_f16 v9, v29, v21, v9
	v_pk_fma_f16 v8, v28, v20, v8
	v_pk_fma_f16 v7, v27, v19, v7
	v_pk_fma_f16 v6, v26, v18, v6
	v_pk_add_f16 v15, v64, v79 neg_lo:[0,1] neg_hi:[0,1]
	v_pk_add_f16 v16, v63, v80 neg_lo:[0,1] neg_hi:[0,1]
	v_pk_add_f16 v17, v62, v81 neg_lo:[0,1] neg_hi:[0,1]
	v_exp_f16_sdwa v18, v14 dst_sel:WORD_0 dst_unused:UNUSED_PAD src0_sel:WORD_0
	v_exp_f16_sdwa v19, v15 dst_sel:WORD_0 dst_unused:UNUSED_PAD src0_sel:WORD_0
	v_exp_f16_sdwa v20, v16 dst_sel:WORD_0 dst_unused:UNUSED_PAD src0_sel:WORD_0
	v_exp_f16_sdwa v21, v17 dst_sel:WORD_0 dst_unused:UNUSED_PAD src0_sel:WORD_0
	v_exp_f16_sdwa v18, v14 dst_sel:WORD_1 dst_unused:UNUSED_PRESERVE src0_sel:WORD_1
	v_exp_f16_sdwa v19, v15 dst_sel:WORD_1 dst_unused:UNUSED_PRESERVE src0_sel:WORD_1
	v_exp_f16_sdwa v20, v16 dst_sel:WORD_1 dst_unused:UNUSED_PRESERVE src0_sel:WORD_1
	v_exp_f16_sdwa v21, v17 dst_sel:WORD_1 dst_unused:UNUSED_PRESERVE src0_sel:WORD_1
	v_pk_add_f16 v14, v46, v78 neg_lo:[0,1] neg_hi:[0,1]
	v_pk_add_f16 v10, v10, v18
	v_pk_add_f16 v11, v11, v19
	v_pk_add_f16 v12, v12, v20
	v_pk_add_f16 v13, v13, v21
	v_pk_fma_f16 v6, v38, v18, v6
	v_pk_fma_f16 v7, v39, v19, v7
	v_pk_fma_f16 v8, v40, v20, v8
	v_pk_fma_f16 v9, v41, v21, v9
	v_pk_add_f16 v15, v47, v79 neg_lo:[0,1] neg_hi:[0,1]
	v_pk_add_f16 v16, v48, v80 neg_lo:[0,1] neg_hi:[0,1]
	v_pk_add_f16 v17, v49, v81 neg_lo:[0,1] neg_hi:[0,1]
	v_exp_f16_sdwa v18, v14 dst_sel:WORD_0 dst_unused:UNUSED_PAD src0_sel:WORD_0
	v_exp_f16_sdwa v19, v15 dst_sel:WORD_0 dst_unused:UNUSED_PAD src0_sel:WORD_0
	v_exp_f16_sdwa v20, v16 dst_sel:WORD_0 dst_unused:UNUSED_PAD src0_sel:WORD_0
	v_exp_f16_sdwa v21, v17 dst_sel:WORD_0 dst_unused:UNUSED_PAD src0_sel:WORD_0
	v_exp_f16_sdwa v18, v14 dst_sel:WORD_1 dst_unused:UNUSED_PRESERVE src0_sel:WORD_1
	v_exp_f16_sdwa v19, v15 dst_sel:WORD_1 dst_unused:UNUSED_PRESERVE src0_sel:WORD_1
	v_exp_f16_sdwa v20, v16 dst_sel:WORD_1 dst_unused:UNUSED_PRESERVE src0_sel:WORD_1
	v_exp_f16_sdwa v21, v17 dst_sel:WORD_1 dst_unused:UNUSED_PRESERVE src0_sel:WORD_1
	v_pk_add_f16 v14, v69, v78 neg_lo:[0,1] neg_hi:[0,1]
	v_pk_add_f16 v13, v13, v21
	v_pk_add_f16 v12, v12, v20
	v_pk_add_f16 v11, v11, v19
	v_pk_add_f16 v10, v10, v18
	v_pk_fma_f16 v9, v61, v21, v9
	v_pk_fma_f16 v8, v60, v20, v8
	v_pk_fma_f16 v7, v59, v19, v7
	v_pk_fma_f16 v6, v58, v18, v6
	v_pk_add_f16 v15, v68, v79 neg_lo:[0,1] neg_hi:[0,1]
	v_pk_add_f16 v16, v67, v80 neg_lo:[0,1] neg_hi:[0,1]
	v_pk_add_f16 v17, v66, v81 neg_lo:[0,1] neg_hi:[0,1]
	v_exp_f16_sdwa v18, v14 dst_sel:WORD_0 dst_unused:UNUSED_PAD src0_sel:WORD_0
	v_exp_f16_sdwa v19, v15 dst_sel:WORD_0 dst_unused:UNUSED_PAD src0_sel:WORD_0
	v_exp_f16_sdwa v20, v16 dst_sel:WORD_0 dst_unused:UNUSED_PAD src0_sel:WORD_0
	v_exp_f16_sdwa v21, v17 dst_sel:WORD_0 dst_unused:UNUSED_PAD src0_sel:WORD_0
	v_exp_f16_sdwa v18, v14 dst_sel:WORD_1 dst_unused:UNUSED_PRESERVE src0_sel:WORD_1
	v_exp_f16_sdwa v19, v15 dst_sel:WORD_1 dst_unused:UNUSED_PRESERVE src0_sel:WORD_1
	v_exp_f16_sdwa v20, v16 dst_sel:WORD_1 dst_unused:UNUSED_PRESERVE src0_sel:WORD_1
	v_exp_f16_sdwa v21, v17 dst_sel:WORD_1 dst_unused:UNUSED_PRESERVE src0_sel:WORD_1
	v_pk_add_f16 v10, v10, v18
	v_pk_add_f16 v11, v11, v19
	v_pk_add_f16 v12, v12, v20
	v_pk_add_f16 v13, v13, v21
	v_pk_fma_f16 v14, v70, v18, v6
	v_pk_fma_f16 v15, v71, v19, v7
	v_pk_fma_f16 v16, v72, v20, v8
	v_pk_fma_f16 v17, v73, v21, v9
	v_pk_add_f16 v6, v77, v78 neg_lo:[0,1] neg_hi:[0,1]
	v_pk_add_f16 v7, v76, v79 neg_lo:[0,1] neg_hi:[0,1]
	v_pk_add_f16 v8, v75, v80 neg_lo:[0,1] neg_hi:[0,1]
	v_pk_add_f16 v9, v74, v81 neg_lo:[0,1] neg_hi:[0,1]
	v_exp_f16_sdwa v18, v6 dst_sel:WORD_0 dst_unused:UNUSED_PAD src0_sel:WORD_0
	v_exp_f16_sdwa v19, v7 dst_sel:WORD_0 dst_unused:UNUSED_PAD src0_sel:WORD_0
	v_exp_f16_sdwa v20, v8 dst_sel:WORD_0 dst_unused:UNUSED_PAD src0_sel:WORD_0
	v_exp_f16_sdwa v21, v9 dst_sel:WORD_0 dst_unused:UNUSED_PAD src0_sel:WORD_0
	v_exp_f16_sdwa v18, v6 dst_sel:WORD_1 dst_unused:UNUSED_PRESERVE src0_sel:WORD_1
	v_exp_f16_sdwa v19, v7 dst_sel:WORD_1 dst_unused:UNUSED_PRESERVE src0_sel:WORD_1
	v_exp_f16_sdwa v20, v8 dst_sel:WORD_1 dst_unused:UNUSED_PRESERVE src0_sel:WORD_1
	v_exp_f16_sdwa v21, v9 dst_sel:WORD_1 dst_unused:UNUSED_PRESERVE src0_sel:WORD_1
	s_nop 0
	v_pk_add_f16 v9, v13, v21
	v_pk_add_f16 v8, v12, v20
	v_pk_add_f16 v7, v11, v19
	v_pk_add_f16 v6, v10, v18
	v_pk_fma_f16 v13, v93, v21, v17
	v_pk_fma_f16 v12, v92, v20, v16
	v_pk_fma_f16 v11, v91, v19, v15
	v_pk_fma_f16 v10, v90, v18, v14
	v_pk_add_f16 v18, v50, v78 neg_lo:[0,1] neg_hi:[0,1]
	v_pk_add_f16 v19, v51, v79 neg_lo:[0,1] neg_hi:[0,1]
	v_pk_add_f16 v20, v52, v80 neg_lo:[0,1] neg_hi:[0,1]
	v_pk_add_f16 v21, v53, v81 neg_lo:[0,1] neg_hi:[0,1]
	v_exp_f16_sdwa v14, v18 dst_sel:WORD_0 dst_unused:UNUSED_PAD src0_sel:WORD_0
	v_exp_f16_sdwa v17, v19 dst_sel:WORD_0 dst_unused:UNUSED_PAD src0_sel:WORD_0
	v_exp_f16_sdwa v15, v20 dst_sel:WORD_0 dst_unused:UNUSED_PAD src0_sel:WORD_0
	v_exp_f16_sdwa v16, v21 dst_sel:WORD_0 dst_unused:UNUSED_PAD src0_sel:WORD_0
	v_exp_f16_sdwa v14, v18 dst_sel:WORD_1 dst_unused:UNUSED_PRESERVE src0_sel:WORD_1
	v_exp_f16_sdwa v17, v19 dst_sel:WORD_1 dst_unused:UNUSED_PRESERVE src0_sel:WORD_1
	v_exp_f16_sdwa v15, v20 dst_sel:WORD_1 dst_unused:UNUSED_PRESERVE src0_sel:WORD_1
	v_exp_f16_sdwa v16, v21 dst_sel:WORD_1 dst_unused:UNUSED_PRESERVE src0_sel:WORD_1
	s_nop 0

.Lmyf_D1_7:
	s_mov_b64 exec, -1
	s_waitcnt lgkmcnt(0)
	v_cvt_f16_f32_e32 v183, s27
	v_cvt_f16_f32_e32 v185, s26
	v_cvt_f16_f32_e32 v184, s31
	s_mov_b64 s[4:5], 0
	s_cmp_lt_u32 s94, 4
	s_cbranch_scc1 .Lmylp5_0
	s_setprio 1
.Lmylp5_0:
	s_waitcnt vmcnt(3)
	v_pk_mul_f16 v193, v185, v189 op_sel_hi:[0,1]
	v_pk_mul_f16 v197, v183, v189 op_sel_hi:[0,1]
	v_pk_mul_f16 v201, v184, v189 op_sel_hi:[0,1]
	v_pk_mul_f16 v190, v185, v186 op_sel_hi:[0,1]
	v_pk_mul_f16 v191, v185, v187 op_sel_hi:[0,1]
	v_pk_mul_f16 v192, v185, v188 op_sel_hi:[0,1]
	v_pk_mul_f16 v194, v183, v186 op_sel_hi:[0,1]
	s_mov_b64 exec, s[64:65]
	buffer_load_dwordx4 v[18:21], v224, s[16:19], 0 offen
	buffer_load_dwordx4 v[6:9], v224, s[16:19], 0 offen offset:512
	s_mov_b64 exec, -1
	v_pk_mul_f16 v195, v183, v187 op_sel_hi:[0,1]
	v_pk_mul_f16 v196, v183, v188 op_sel_hi:[0,1]
	v_pk_mul_f16 v198, v184, v186 op_sel_hi:[0,1]
	v_pk_mul_f16 v199, v184, v187 op_sel_hi:[0,1]
	v_pk_mul_f16 v200, v184, v188 op_sel_hi:[0,1]
	v_pk_fma_f16 v113, v113, v189, v193
	v_pk_fma_f16 v129, v129, v189, v197
	v_pk_fma_f16 v137, v137, v189, v201
	v_pk_fma_f16 v202, v85, v189, v193
	v_pk_fma_f16 v206, v109, v189, v197
	v_pk_fma_f16 v210, v125, v189, v201
	v_pk_fma_f16 v193, v53, v189, v193
	v_pk_fma_f16 v197, v69, v189, v197
	buffer_load_dwordx4 v[34:37], v225, s[16:19], 0 offen offset:512
	buffer_load_dwordx4 v[10:13], v225, s[16:19], 0 offen offset:1024
	v_pk_fma_f16 v189, v97, v189, v201
	v_pk_maximum3_f16 v201, v113, v129, v137
	v_pk_fma_f16 v112, v112, v188, v192
	v_pk_fma_f16 v111, v111, v187, v191
	v_pk_fma_f16 v110, v110, v186, v190
	v_pk_fma_f16 v128, v128, v188, v196
	v_pk_fma_f16 v127, v127, v187, v195
	v_pk_fma_f16 v126, v126, v186, v194
	v_pk_fma_f16 v136, v136, v188, v200
	v_pk_fma_f16 v135, v135, v187, v199
	v_pk_fma_f16 v134, v134, v186, v198
	v_pk_fma_f16 v203, v84, v188, v192
	v_pk_fma_f16 v204, v83, v187, v191
	v_pk_fma_f16 v205, v82, v186, v190
	v_pk_fma_f16 v207, v108, v188, v196
	v_pk_fma_f16 v208, v107, v187, v195
	s_mov_b64 exec, s[66:67]
	buffer_load_dwordx4 v[54:57], v225, s[16:19], 0 offen offset:2048
	buffer_load_dwordx4 v[14:17], v225, s[16:19], 0 offen offset:2560
	s_mov_b64 exec, -1
	v_pk_fma_f16 v209, v106, v186, v194
	v_pk_fma_f16 v211, v124, v188, v200
	v_pk_fma_f16 v212, v123, v187, v199
	v_pk_fma_f16 v213, v122, v186, v198
	v_pk_fma_f16 v192, v52, v188, v192
	v_pk_fma_f16 v191, v51, v187, v191
	v_pk_fma_f16 v190, v50, v186, v190
	v_pk_fma_f16 v196, v68, v188, v196
	v_pk_fma_f16 v195, v67, v187, v195
	v_pk_fma_f16 v194, v66, v186, v194
	v_pk_fma_f16 v188, v96, v188, v200
	v_pk_fma_f16 v187, v95, v187, v199
	v_pk_fma_f16 v186, v94, v186, v198
	v_pk_maximum3_f16 v198, v110, v126, v134
	v_pk_maximum3_f16 v199, v111, v127, v135
	v_pk_maximum3_f16 v200, v112, v128, v136
	v_pk_maximum3_f16 v217, v202, v206, v210
	v_pk_maximum3_f16 v221, v193, v197, v189
	v_pk_maximum3_f16 v214, v205, v209, v213
	v_pk_maximum3_f16 v215, v204, v208, v212
	v_pk_maximum3_f16 v216, v203, v207, v211
	v_pk_maximum3_f16 v218, v190, v194, v186
	v_pk_maximum3_f16 v219, v191, v195, v187
	v_pk_maximum3_f16 v201, v201, v217, v221
	v_pk_maximum3_f16 v220, v192, v196, v188
	v_pk_maximum3_f16 v198, v198, v214, v218
	v_pk_maximum3_f16 v199, v199, v215, v219
	v_pk_maximum3_f16 v200, v200, v216, v220
	v_pk_add_f16 v113, v113, v201 neg_lo:[0,1] neg_hi:[0,1]
	s_mov_b64 exec, s[64:65]
	buffer_load_dwordx4 v[74:77], v226, s[16:19], 0 offen
	buffer_load_dwordx4 v[26:29], v226, s[16:19], 0 offen offset:512
	s_mov_b64 exec, -1
	v_pk_add_f16 v110, v110, v198 neg_lo:[0,1] neg_hi:[0,1]
	v_pk_add_f16 v111, v111, v199 neg_lo:[0,1] neg_hi:[0,1]
	v_pk_add_f16 v112, v112, v200 neg_lo:[0,1] neg_hi:[0,1]
	v_pk_add_f16 v126, v126, v198 neg_lo:[0,1] neg_hi:[0,1]
	v_exp_f16_sdwa v214, v110 dst_sel:WORD_0 dst_unused:UNUSED_PAD src0_sel:WORD_0
	v_exp_f16_sdwa v215, v111 dst_sel:WORD_0 dst_unused:UNUSED_PAD src0_sel:WORD_0
	v_exp_f16_sdwa v216, v112 dst_sel:WORD_0 dst_unused:UNUSED_PAD src0_sel:WORD_0
	v_exp_f16_sdwa v217, v113 dst_sel:WORD_0 dst_unused:UNUSED_PAD src0_sel:WORD_0
	v_exp_f16_sdwa v214, v110 dst_sel:WORD_1 dst_unused:UNUSED_PRESERVE src0_sel:WORD_1
	v_exp_f16_sdwa v215, v111 dst_sel:WORD_1 dst_unused:UNUSED_PRESERVE src0_sel:WORD_1
	v_exp_f16_sdwa v216, v112 dst_sel:WORD_1 dst_unused:UNUSED_PRESERVE src0_sel:WORD_1
	v_exp_f16_sdwa v217, v113 dst_sel:WORD_1 dst_unused:UNUSED_PRESERVE src0_sel:WORD_1
	v_pk_add_f16 v127, v127, v199 neg_lo:[0,1] neg_hi:[0,1]
	v_pk_add_f16 v113, v214, 0
	v_pk_fma_f16 v73, v73, v217, 0
	v_pk_add_f16 v110, v217, 0
	v_pk_add_f16 v111, v216, 0
	v_pk_add_f16 v112, v215, 0
	v_pk_fma_f16 v72, v72, v216, 0
	v_pk_fma_f16 v71, v71, v215, 0
	v_pk_fma_f16 v70, v70, v214, 0
	v_pk_add_f16 v128, v128, v200 neg_lo:[0,1] neg_hi:[0,1]
	buffer_load_dwordx4 v[102:105], v227, s[16:19], 0 offen offset:512
	buffer_load_dwordx4 v[38:41], v227, s[16:19], 0 offen offset:1024
	v_pk_add_f16 v129, v129, v201 neg_lo:[0,1] neg_hi:[0,1]
	v_exp_f16_sdwa v214, v126 dst_sel:WORD_0 dst_unused:UNUSED_PAD src0_sel:WORD_0
	v_exp_f16_sdwa v215, v127 dst_sel:WORD_0 dst_unused:UNUSED_PAD src0_sel:WORD_0
	v_exp_f16_sdwa v216, v128 dst_sel:WORD_0 dst_unused:UNUSED_PAD src0_sel:WORD_0
	v_exp_f16_sdwa v217, v129 dst_sel:WORD_0 dst_unused:UNUSED_PAD src0_sel:WORD_0
	v_exp_f16_sdwa v214, v126 dst_sel:WORD_1 dst_unused:UNUSED_PRESERVE src0_sel:WORD_1
	v_exp_f16_sdwa v215, v127 dst_sel:WORD_1 dst_unused:UNUSED_PRESERVE src0_sel:WORD_1
	v_exp_f16_sdwa v216, v128 dst_sel:WORD_1 dst_unused:UNUSED_PRESERVE src0_sel:WORD_1
	v_exp_f16_sdwa v217, v129 dst_sel:WORD_1 dst_unused:UNUSED_PRESERVE src0_sel:WORD_1
	v_pk_add_f16 v113, v113, v214
	v_pk_fma_f16 v73, v101, v217, v73
	v_pk_add_f16 v101, v137, v201 neg_lo:[0,1] neg_hi:[0,1]
	v_pk_add_f16 v112, v112, v215
	v_pk_add_f16 v111, v111, v216
	v_pk_add_f16 v110, v110, v217
	v_pk_fma_f16 v70, v98, v214, v70
	v_pk_fma_f16 v71, v99, v215, v71
	v_pk_fma_f16 v72, v100, v216, v72
	v_pk_add_f16 v98, v134, v198 neg_lo:[0,1] neg_hi:[0,1]
	v_pk_add_f16 v99, v135, v199 neg_lo:[0,1] neg_hi:[0,1]
	v_pk_add_f16 v100, v136, v200 neg_lo:[0,1] neg_hi:[0,1]
	v_exp_f16_sdwa v126, v98 dst_sel:WORD_0 dst_unused:UNUSED_PAD src0_sel:WORD_0
	v_exp_f16_sdwa v127, v99 dst_sel:WORD_0 dst_unused:UNUSED_PAD src0_sel:WORD_0
	v_exp_f16_sdwa v128, v100 dst_sel:WORD_0 dst_unused:UNUSED_PAD src0_sel:WORD_0
	v_exp_f16_sdwa v129, v101 dst_sel:WORD_0 dst_unused:UNUSED_PAD src0_sel:WORD_0
	v_exp_f16_sdwa v126, v98 dst_sel:WORD_1 dst_unused:UNUSED_PRESERVE src0_sel:WORD_1
	v_exp_f16_sdwa v127, v99 dst_sel:WORD_1 dst_unused:UNUSED_PRESERVE src0_sel:WORD_1
	v_exp_f16_sdwa v128, v100 dst_sel:WORD_1 dst_unused:UNUSED_PRESERVE src0_sel:WORD_1
	v_exp_f16_sdwa v129, v101 dst_sel:WORD_1 dst_unused:UNUSED_PRESERVE src0_sel:WORD_1
	v_pk_add_f16 v101, v113, v126
	v_pk_add_f16 v98, v110, v129
	s_mov_b64 exec, s[66:67]
	buffer_load_dwordx4 v[118:121], v227, s[16:19], 0 offen offset:2048
	buffer_load_dwordx4 v[58:61], v227, s[16:19], 0 offen offset:2560
	s_mov_b64 exec, -1
	v_pk_add_f16 v99, v111, v128
	v_pk_add_f16 v100, v112, v127
	v_pk_fma_f16 v73, v117, v129, v73
	v_pk_fma_f16 v72, v116, v128, v72
	v_pk_fma_f16 v71, v115, v127, v71
	v_pk_fma_f16 v70, v114, v126, v70
	v_pk_add_f16 v110, v205, v198 neg_lo:[0,1] neg_hi:[0,1]
	v_pk_add_f16 v111, v204, v199 neg_lo:[0,1] neg_hi:[0,1]
	v_pk_add_f16 v112, v203, v200 neg_lo:[0,1] neg_hi:[0,1]
	v_pk_add_f16 v113, v202, v201 neg_lo:[0,1] neg_hi:[0,1]
	v_exp_f16_sdwa v114, v110 dst_sel:WORD_0 dst_unused:UNUSED_PAD src0_sel:WORD_0
	v_exp_f16_sdwa v115, v111 dst_sel:WORD_0 dst_unused:UNUSED_PAD src0_sel:WORD_0
	v_exp_f16_sdwa v116, v112 dst_sel:WORD_0 dst_unused:UNUSED_PAD src0_sel:WORD_0
	v_exp_f16_sdwa v117, v113 dst_sel:WORD_0 dst_unused:UNUSED_PAD src0_sel:WORD_0
	v_exp_f16_sdwa v114, v110 dst_sel:WORD_1 dst_unused:UNUSED_PRESERVE src0_sel:WORD_1
	v_exp_f16_sdwa v115, v111 dst_sel:WORD_1 dst_unused:UNUSED_PRESERVE src0_sel:WORD_1
	v_exp_f16_sdwa v116, v112 dst_sel:WORD_1 dst_unused:UNUSED_PRESERVE src0_sel:WORD_1
	v_exp_f16_sdwa v117, v113 dst_sel:WORD_1 dst_unused:UNUSED_PRESERVE src0_sel:WORD_1
	v_pk_add_f16 v110, v209, v198 neg_lo:[0,1] neg_hi:[0,1]
	v_pk_add_f16 v101, v101, v114
	v_pk_add_f16 v100, v100, v115
	v_pk_add_f16 v99, v99, v116
	s_mov_b64 exec, s[76:77]
	buffer_load_dwordx4 v[130:133], v228, s[16:19], 0 offen
	buffer_load_dwordx4 v[78:81], v228, s[16:19], 0 offen offset:512
	s_mov_b64 exec, -1
	v_pk_add_f16 v98, v98, v117
	v_pk_fma_f16 v70, v42, v114, v70
	v_pk_fma_f16 v71, v43, v115, v71
	v_pk_fma_f16 v72, v44, v116, v72
	v_pk_fma_f16 v73, v45, v117, v73
	v_pk_add_f16 v111, v208, v199 neg_lo:[0,1] neg_hi:[0,1]
	v_pk_add_f16 v112, v207, v200 neg_lo:[0,1] neg_hi:[0,1]
	v_pk_add_f16 v113, v206, v201 neg_lo:[0,1] neg_hi:[0,1]
	v_exp_f16_sdwa v114, v110 dst_sel:WORD_0 dst_unused:UNUSED_PAD src0_sel:WORD_0
	v_exp_f16_sdwa v115, v111 dst_sel:WORD_0 dst_unused:UNUSED_PAD src0_sel:WORD_0
	v_exp_f16_sdwa v116, v112 dst_sel:WORD_0 dst_unused:UNUSED_PAD src0_sel:WORD_0
	v_exp_f16_sdwa v117, v113 dst_sel:WORD_0 dst_unused:UNUSED_PAD src0_sel:WORD_0
	v_exp_f16_sdwa v114, v110 dst_sel:WORD_1 dst_unused:UNUSED_PRESERVE src0_sel:WORD_1
	v_exp_f16_sdwa v115, v111 dst_sel:WORD_1 dst_unused:UNUSED_PRESERVE src0_sel:WORD_1
	v_exp_f16_sdwa v116, v112 dst_sel:WORD_1 dst_unused:UNUSED_PRESERVE src0_sel:WORD_1
	v_exp_f16_sdwa v117, v113 dst_sel:WORD_1 dst_unused:UNUSED_PRESERVE src0_sel:WORD_1
	v_pk_add_f16 v110, v213, v198 neg_lo:[0,1] neg_hi:[0,1]
	v_pk_add_f16 v101, v101, v114
	v_pk_add_f16 v98, v98, v117
	v_pk_add_f16 v99, v99, v116
	v_pk_add_f16 v100, v100, v115
	v_pk_fma_f16 v73, v65, v117, v73
	v_pk_fma_f16 v72, v64, v116, v72
	s_mov_b64 exec, s[70:71]
	buffer_load_dwordx4 v[138:141], v229, s[16:19], 0 offen offset:512
	buffer_load_dwordx4 v[90:93], v229, s[16:19], 0 offen offset:1024
	s_mov_b64 exec, -1
	v_pk_fma_f16 v71, v63, v115, v71
	v_pk_fma_f16 v70, v62, v114, v70
	v_pk_add_f16 v111, v212, v199 neg_lo:[0,1] neg_hi:[0,1]
	v_pk_add_f16 v112, v211, v200 neg_lo:[0,1] neg_hi:[0,1]
	v_pk_add_f16 v113, v210, v201 neg_lo:[0,1] neg_hi:[0,1]
	v_exp_f16_sdwa v114, v110 dst_sel:WORD_0 dst_unused:UNUSED_PAD src0_sel:WORD_0
	v_exp_f16_sdwa v115, v111 dst_sel:WORD_0 dst_unused:UNUSED_PAD src0_sel:WORD_0
	v_exp_f16_sdwa v116, v112 dst_sel:WORD_0 dst_unused:UNUSED_PAD src0_sel:WORD_0
	v_exp_f16_sdwa v117, v113 dst_sel:WORD_0 dst_unused:UNUSED_PAD src0_sel:WORD_0
	v_exp_f16_sdwa v114, v110 dst_sel:WORD_1 dst_unused:UNUSED_PRESERVE src0_sel:WORD_1
	v_exp_f16_sdwa v115, v111 dst_sel:WORD_1 dst_unused:UNUSED_PRESERVE src0_sel:WORD_1
	v_exp_f16_sdwa v116, v112 dst_sel:WORD_1 dst_unused:UNUSED_PRESERVE src0_sel:WORD_1
	v_exp_f16_sdwa v117, v113 dst_sel:WORD_1 dst_unused:UNUSED_PRESERVE src0_sel:WORD_1
	v_pk_add_f16 v110, v190, v198 neg_lo:[0,1] neg_hi:[0,1]
	v_pk_add_f16 v101, v101, v114
	v_pk_add_f16 v100, v100, v115
	v_pk_add_f16 v99, v99, v116
	v_pk_add_f16 v98, v98, v117
	v_pk_fma_f16 v70, v86, v114, v70
	v_pk_fma_f16 v71, v87, v115, v71
	v_pk_fma_f16 v72, v88, v116, v72
	v_pk_fma_f16 v73, v89, v117, v73
	s_mov_b64 exec, s[78:79]
	buffer_load_dwordx4 v[142:145], v229, s[16:19], 0 offen offset:2048
	buffer_load_dwordx4 v[2:5], v229, s[16:19], 0 offen offset:2560
	s_mov_b64 exec, -1
	v_pk_add_f16 v111, v191, v199 neg_lo:[0,1] neg_hi:[0,1]
	v_pk_add_f16 v112, v192, v200 neg_lo:[0,1] neg_hi:[0,1]
	v_pk_add_f16 v113, v193, v201 neg_lo:[0,1] neg_hi:[0,1]
	v_exp_f16_sdwa v114, v110 dst_sel:WORD_0 dst_unused:UNUSED_PAD src0_sel:WORD_0
	v_exp_f16_sdwa v115, v111 dst_sel:WORD_0 dst_unused:UNUSED_PAD src0_sel:WORD_0
	v_exp_f16_sdwa v116, v112 dst_sel:WORD_0 dst_unused:UNUSED_PAD src0_sel:WORD_0
	v_exp_f16_sdwa v117, v113 dst_sel:WORD_0 dst_unused:UNUSED_PAD src0_sel:WORD_0
	v_exp_f16_sdwa v114, v110 dst_sel:WORD_1 dst_unused:UNUSED_PRESERVE src0_sel:WORD_1
	v_exp_f16_sdwa v115, v111 dst_sel:WORD_1 dst_unused:UNUSED_PRESERVE src0_sel:WORD_1
	v_exp_f16_sdwa v116, v112 dst_sel:WORD_1 dst_unused:UNUSED_PRESERVE src0_sel:WORD_1
	v_exp_f16_sdwa v117, v113 dst_sel:WORD_1 dst_unused:UNUSED_PRESERVE src0_sel:WORD_1
	v_pk_add_f16 v110, v194, v198 neg_lo:[0,1] neg_hi:[0,1]
	v_pk_add_f16 v101, v101, v114
	v_pk_add_f16 v98, v98, v117
	v_pk_add_f16 v99, v99, v116
	v_pk_add_f16 v100, v100, v115
	v_pk_fma_f16 v73, v25, v117, v73
	v_pk_fma_f16 v72, v24, v116, v72
	v_pk_fma_f16 v71, v23, v115, v71
	v_pk_fma_f16 v70, v22, v114, v70
	v_pk_add_f16 v111, v195, v199 neg_lo:[0,1] neg_hi:[0,1]
	v_pk_add_f16 v112, v196, v200 neg_lo:[0,1] neg_hi:[0,1]
	v_pk_add_f16 v113, v197, v201 neg_lo:[0,1] neg_hi:[0,1]
	v_exp_f16_sdwa v114, v110 dst_sel:WORD_0 dst_unused:UNUSED_PAD src0_sel:WORD_0
	v_exp_f16_sdwa v115, v111 dst_sel:WORD_0 dst_unused:UNUSED_PAD src0_sel:WORD_0
	v_exp_f16_sdwa v116, v112 dst_sel:WORD_0 dst_unused:UNUSED_PAD src0_sel:WORD_0
	v_exp_f16_sdwa v117, v113 dst_sel:WORD_0 dst_unused:UNUSED_PAD src0_sel:WORD_0
	v_exp_f16_sdwa v114, v110 dst_sel:WORD_1 dst_unused:UNUSED_PRESERVE src0_sel:WORD_1
	v_exp_f16_sdwa v115, v111 dst_sel:WORD_1 dst_unused:UNUSED_PRESERVE src0_sel:WORD_1
	v_exp_f16_sdwa v116, v112 dst_sel:WORD_1 dst_unused:UNUSED_PRESERVE src0_sel:WORD_1
	v_exp_f16_sdwa v117, v113 dst_sel:WORD_1 dst_unused:UNUSED_PRESERVE src0_sel:WORD_1
	v_pk_add_f16 v110, v186, v198 neg_lo:[0,1] neg_hi:[0,1]
	v_pk_add_f16 v101, v101, v114
	v_pk_add_f16 v100, v100, v115
	v_pk_add_f16 v99, v99, v116
	v_pk_add_f16 v98, v98, v117
	v_pk_fma_f16 v70, v30, v114, v70
	v_pk_fma_f16 v71, v31, v115, v71
	v_pk_fma_f16 v72, v32, v116, v72
	v_pk_fma_f16 v73, v33, v117, v73
	v_pk_add_f16 v111, v187, v199 neg_lo:[0,1] neg_hi:[0,1]
	v_pk_add_f16 v112, v188, v200 neg_lo:[0,1] neg_hi:[0,1]
	v_pk_add_f16 v113, v189, v201 neg_lo:[0,1] neg_hi:[0,1]
	v_exp_f16_sdwa v114, v110 dst_sel:WORD_0 dst_unused:UNUSED_PAD src0_sel:WORD_0
	v_exp_f16_sdwa v115, v111 dst_sel:WORD_0 dst_unused:UNUSED_PAD src0_sel:WORD_0
	v_exp_f16_sdwa v116, v112 dst_sel:WORD_0 dst_unused:UNUSED_PAD src0_sel:WORD_0
	v_exp_f16_sdwa v117, v113 dst_sel:WORD_0 dst_unused:UNUSED_PAD src0_sel:WORD_0
	v_exp_f16_sdwa v114, v110 dst_sel:WORD_1 dst_unused:UNUSED_PRESERVE src0_sel:WORD_1
	v_exp_f16_sdwa v115, v111 dst_sel:WORD_1 dst_unused:UNUSED_PRESERVE src0_sel:WORD_1
	v_exp_f16_sdwa v116, v112 dst_sel:WORD_1 dst_unused:UNUSED_PRESERVE src0_sel:WORD_1
	v_exp_f16_sdwa v117, v113 dst_sel:WORD_1 dst_unused:UNUSED_PRESERVE src0_sel:WORD_1
	v_pk_add_f16 v101, v101, v114
	v_pk_add_f16 v100, v100, v115
	v_rcp_f16_e32 v110, v101
	v_rcp_f16_sdwa v101, v101 dst_sel:DWORD dst_unused:UNUSED_PAD src0_sel:WORD_1
	v_pk_add_f16 v99, v99, v116
	v_rcp_f16_e32 v111, v100
	v_rcp_f16_sdwa v100, v100 dst_sel:DWORD dst_unused:UNUSED_PAD src0_sel:WORD_1
	v_pk_add_f16 v98, v98, v117
	v_rcp_f16_e32 v112, v99
	v_rcp_f16_sdwa v99, v99 dst_sel:DWORD dst_unused:UNUSED_PAD src0_sel:WORD_1
	v_rcp_f16_e32 v113, v98
	v_rcp_f16_sdwa v98, v98 dst_sel:DWORD dst_unused:UNUSED_PAD src0_sel:WORD_1
	v_pk_fma_f16 v70, v46, v114, v70
	v_pack_b32_f16 v101, v110, v101
	v_pk_fma_f16 v71, v47, v115, v71
	v_pk_mul_f16 v110, v70, v101
	v_pack_b32_f16 v70, v111, v100
	v_pk_fma_f16 v72, v48, v116, v72
	v_pk_mul_f16 v111, v71, v70
	v_pack_b32_f16 v70, v112, v99
	v_pk_fma_f16 v73, v49, v117, v73
	v_pk_mul_f16 v112, v72, v70
	v_pack_b32_f16 v70, v113, v98
	v_pk_mul_f16 v113, v73, v70
	s_waitcnt vmcnt(12)
	v_pk_mul_f16 v70, v185, v154 op_sel_hi:[0,1]
	v_pk_mul_f16 v98, v183, v154 op_sel_hi:[0,1]
	v_pk_mul_f16 v114, v184, v154 op_sel_hi:[0,1]
	v_pk_mul_f16 v71, v185, v155 op_sel_hi:[0,1]
	v_pk_mul_f16 v72, v185, v156 op_sel_hi:[0,1]
	v_pk_mul_f16 v73, v185, v157 op_sel_hi:[0,1]
	v_pk_mul_f16 v99, v183, v155 op_sel_hi:[0,1]
	v_pk_mul_f16 v100, v183, v156 op_sel_hi:[0,1]
	v_pk_mul_f16 v101, v183, v157 op_sel_hi:[0,1]
	v_pk_mul_f16 v115, v184, v155 op_sel_hi:[0,1]
	v_pk_mul_f16 v116, v184, v156 op_sel_hi:[0,1]
	v_pk_mul_f16 v117, v184, v157 op_sel_hi:[0,1]
	v_pk_fma_f16 v82, v82, v154, v70
	v_pk_fma_f16 v106, v106, v154, v98
	v_pk_fma_f16 v122, v122, v154, v114
	v_pk_fma_f16 v129, v50, v154, v70
	v_pk_fma_f16 v137, v66, v154, v98
	v_pk_fma_f16 v189, v94, v154, v114
	v_pk_fma_f16 v70, v18, v154, v70
	v_pk_fma_f16 v98, v34, v154, v98
	v_pk_fma_f16 v114, v54, v154, v114
	v_pk_maximum3_f16 v154, v82, v106, v122
	v_pk_fma_f16 v85, v85, v157, v73
	v_pk_fma_f16 v84, v84, v156, v72
	v_pk_fma_f16 v83, v83, v155, v71
	v_pk_fma_f16 v109, v109, v157, v101
	v_pk_fma_f16 v108, v108, v156, v100
	v_pk_fma_f16 v107, v107, v155, v99
	v_pk_fma_f16 v125, v125, v157, v117
	v_pk_fma_f16 v124, v124, v156, v116
	v_pk_fma_f16 v123, v123, v155, v115
	v_pk_fma_f16 v126, v53, v157, v73
	v_pk_fma_f16 v127, v52, v156, v72
	v_pk_fma_f16 v128, v51, v155, v71
	v_pk_fma_f16 v134, v69, v157, v101
	v_pk_fma_f16 v135, v68, v156, v100
	v_pk_fma_f16 v136, v67, v155, v99
	v_pk_fma_f16 v186, v97, v157, v117
	v_pk_fma_f16 v187, v96, v156, v116
	v_pk_fma_f16 v188, v95, v155, v115
	v_pk_fma_f16 v73, v21, v157, v73
	v_pk_fma_f16 v72, v20, v156, v72
	v_pk_fma_f16 v71, v19, v155, v71
	v_pk_fma_f16 v101, v37, v157, v101
	v_pk_fma_f16 v100, v36, v156, v100
	v_pk_fma_f16 v99, v35, v155, v99
	v_pk_fma_f16 v117, v57, v157, v117
	v_pk_fma_f16 v116, v56, v156, v116
	v_pk_fma_f16 v115, v55, v155, v115
	v_pk_maximum3_f16 v155, v83, v107, v123
	v_pk_maximum3_f16 v156, v84, v108, v124
	v_pk_maximum3_f16 v157, v85, v109, v125
	v_pk_maximum3_f16 v190, v129, v137, v189
	v_pk_maximum3_f16 v194, v70, v98, v114
	v_pk_maximum3_f16 v191, v128, v136, v188
	v_pk_maximum3_f16 v192, v127, v135, v187
	v_pk_maximum3_f16 v193, v126, v134, v186
	v_pk_maximum3_f16 v195, v71, v99, v115
	v_pk_maximum3_f16 v196, v72, v100, v116
	v_pk_maximum3_f16 v154, v154, v190, v194
	v_pk_maximum3_f16 v197, v73, v101, v117
	v_pk_maximum3_f16 v155, v155, v191, v195
	v_pk_maximum3_f16 v156, v156, v192, v196
	v_pk_maximum3_f16 v157, v157, v193, v197
	v_pk_add_f16 v82, v82, v154 neg_lo:[0,1] neg_hi:[0,1]
	v_pk_add_f16 v83, v83, v155 neg_lo:[0,1] neg_hi:[0,1]
	v_pk_add_f16 v84, v84, v156 neg_lo:[0,1] neg_hi:[0,1]
	v_pk_add_f16 v85, v85, v157 neg_lo:[0,1] neg_hi:[0,1]
	v_pk_add_f16 v106, v106, v154 neg_lo:[0,1] neg_hi:[0,1]
	v_exp_f16_sdwa v190, v82 dst_sel:WORD_0 dst_unused:UNUSED_PAD src0_sel:WORD_0
	v_exp_f16_sdwa v191, v83 dst_sel:WORD_0 dst_unused:UNUSED_PAD src0_sel:WORD_0
	v_exp_f16_sdwa v192, v84 dst_sel:WORD_0 dst_unused:UNUSED_PAD src0_sel:WORD_0
	v_exp_f16_sdwa v193, v85 dst_sel:WORD_0 dst_unused:UNUSED_PAD src0_sel:WORD_0
	v_exp_f16_sdwa v190, v82 dst_sel:WORD_1 dst_unused:UNUSED_PRESERVE src0_sel:WORD_1
	v_exp_f16_sdwa v191, v83 dst_sel:WORD_1 dst_unused:UNUSED_PRESERVE src0_sel:WORD_1
	v_exp_f16_sdwa v192, v84 dst_sel:WORD_1 dst_unused:UNUSED_PRESERVE src0_sel:WORD_1
	v_exp_f16_sdwa v193, v85 dst_sel:WORD_1 dst_unused:UNUSED_PRESERVE src0_sel:WORD_1
	v_pk_add_f16 v107, v107, v155 neg_lo:[0,1] neg_hi:[0,1]
	v_pk_add_f16 v82, v193, 0
	v_pk_fma_f16 v42, v42, v190, 0
	v_pk_add_f16 v83, v192, 0
	v_pk_add_f16 v84, v191, 0
	v_pk_add_f16 v85, v190, 0
	v_pk_fma_f16 v45, v45, v193, 0
	v_pk_fma_f16 v44, v44, v192, 0
	v_pk_fma_f16 v43, v43, v191, 0
	v_pk_add_f16 v108, v108, v156 neg_lo:[0,1] neg_hi:[0,1]
	v_pk_add_f16 v109, v109, v157 neg_lo:[0,1] neg_hi:[0,1]
	v_pk_add_f16 v70, v70, v154 neg_lo:[0,1] neg_hi:[0,1]
	v_exp_f16_sdwa v190, v106 dst_sel:WORD_0 dst_unused:UNUSED_PAD src0_sel:WORD_0
	v_exp_f16_sdwa v191, v107 dst_sel:WORD_0 dst_unused:UNUSED_PAD src0_sel:WORD_0
	v_exp_f16_sdwa v192, v108 dst_sel:WORD_0 dst_unused:UNUSED_PAD src0_sel:WORD_0
	v_exp_f16_sdwa v193, v109 dst_sel:WORD_0 dst_unused:UNUSED_PAD src0_sel:WORD_0
	v_exp_f16_sdwa v190, v106 dst_sel:WORD_1 dst_unused:UNUSED_PRESERVE src0_sel:WORD_1
	v_exp_f16_sdwa v191, v107 dst_sel:WORD_1 dst_unused:UNUSED_PRESERVE src0_sel:WORD_1
	v_exp_f16_sdwa v192, v108 dst_sel:WORD_1 dst_unused:UNUSED_PRESERVE src0_sel:WORD_1
	v_exp_f16_sdwa v193, v109 dst_sel:WORD_1 dst_unused:UNUSED_PRESERVE src0_sel:WORD_1
	v_pk_add_f16 v71, v71, v155 neg_lo:[0,1] neg_hi:[0,1]
	v_pk_add_f16 v82, v82, v193
	v_pk_fma_f16 v42, v62, v190, v42
	v_pk_add_f16 v62, v122, v154 neg_lo:[0,1] neg_hi:[0,1]
	v_pk_add_f16 v85, v85, v190
	v_pk_add_f16 v84, v84, v191
	v_pk_add_f16 v83, v83, v192
	v_pk_fma_f16 v43, v63, v191, v43
	v_pk_fma_f16 v44, v64, v192, v44
	v_pk_fma_f16 v45, v65, v193, v45
	v_pk_add_f16 v63, v123, v155 neg_lo:[0,1] neg_hi:[0,1]
	v_pk_add_f16 v64, v124, v156 neg_lo:[0,1] neg_hi:[0,1]
	v_pk_add_f16 v65, v125, v157 neg_lo:[0,1] neg_hi:[0,1]
	v_pk_add_f16 v72, v72, v156 neg_lo:[0,1] neg_hi:[0,1]
	v_exp_f16_sdwa v106, v62 dst_sel:WORD_0 dst_unused:UNUSED_PAD src0_sel:WORD_0
	v_exp_f16_sdwa v107, v63 dst_sel:WORD_0 dst_unused:UNUSED_PAD src0_sel:WORD_0
	v_exp_f16_sdwa v108, v64 dst_sel:WORD_0 dst_unused:UNUSED_PAD src0_sel:WORD_0
	v_exp_f16_sdwa v109, v65 dst_sel:WORD_0 dst_unused:UNUSED_PAD src0_sel:WORD_0
	v_exp_f16_sdwa v106, v62 dst_sel:WORD_1 dst_unused:UNUSED_PRESERVE src0_sel:WORD_1
	v_exp_f16_sdwa v107, v63 dst_sel:WORD_1 dst_unused:UNUSED_PRESERVE src0_sel:WORD_1
	v_exp_f16_sdwa v108, v64 dst_sel:WORD_1 dst_unused:UNUSED_PRESERVE src0_sel:WORD_1
	v_exp_f16_sdwa v109, v65 dst_sel:WORD_1 dst_unused:UNUSED_PRESERVE src0_sel:WORD_1
	v_pk_add_f16 v73, v73, v157 neg_lo:[0,1] neg_hi:[0,1]
	v_pk_add_f16 v62, v82, v109
	v_pk_add_f16 v63, v83, v108
	v_pk_add_f16 v64, v84, v107
	v_pk_add_f16 v65, v85, v106
	v_pk_fma_f16 v45, v89, v109, v45
	v_pk_fma_f16 v44, v88, v108, v44
	v_pk_fma_f16 v43, v87, v107, v43
	v_pk_fma_f16 v42, v86, v106, v42
	v_pk_add_f16 v82, v129, v154 neg_lo:[0,1] neg_hi:[0,1]
	v_pk_add_f16 v83, v128, v155 neg_lo:[0,1] neg_hi:[0,1]
	v_pk_add_f16 v84, v127, v156 neg_lo:[0,1] neg_hi:[0,1]
	v_pk_add_f16 v85, v126, v157 neg_lo:[0,1] neg_hi:[0,1]
	v_exp_f16_sdwa v86, v82 dst_sel:WORD_0 dst_unused:UNUSED_PAD src0_sel:WORD_0
	v_exp_f16_sdwa v87, v83 dst_sel:WORD_0 dst_unused:UNUSED_PAD src0_sel:WORD_0
	v_exp_f16_sdwa v88, v84 dst_sel:WORD_0 dst_unused:UNUSED_PAD src0_sel:WORD_0
	v_exp_f16_sdwa v89, v85 dst_sel:WORD_0 dst_unused:UNUSED_PAD src0_sel:WORD_0
	v_exp_f16_sdwa v86, v82 dst_sel:WORD_1 dst_unused:UNUSED_PRESERVE src0_sel:WORD_1
	v_exp_f16_sdwa v87, v83 dst_sel:WORD_1 dst_unused:UNUSED_PRESERVE src0_sel:WORD_1
	v_exp_f16_sdwa v88, v84 dst_sel:WORD_1 dst_unused:UNUSED_PRESERVE src0_sel:WORD_1
	v_exp_f16_sdwa v89, v85 dst_sel:WORD_1 dst_unused:UNUSED_PRESERVE src0_sel:WORD_1
	v_pk_add_f16 v82, v137, v154 neg_lo:[0,1] neg_hi:[0,1]
	v_pk_add_f16 v62, v62, v89
	v_pk_add_f16 v65, v65, v86
	v_pk_add_f16 v64, v64, v87
	v_pk_add_f16 v63, v63, v88
	v_pk_fma_f16 v42, v22, v86, v42
	v_pk_fma_f16 v43, v23, v87, v43
	v_pk_fma_f16 v44, v24, v88, v44
	v_pk_fma_f16 v45, v25, v89, v45
	v_pk_add_f16 v83, v136, v155 neg_lo:[0,1] neg_hi:[0,1]
	v_pk_add_f16 v84, v135, v156 neg_lo:[0,1] neg_hi:[0,1]
	v_pk_add_f16 v85, v134, v157 neg_lo:[0,1] neg_hi:[0,1]
	v_exp_f16_sdwa v86, v82 dst_sel:WORD_0 dst_unused:UNUSED_PAD src0_sel:WORD_0
	v_exp_f16_sdwa v87, v83 dst_sel:WORD_0 dst_unused:UNUSED_PAD src0_sel:WORD_0
	v_exp_f16_sdwa v88, v84 dst_sel:WORD_0 dst_unused:UNUSED_PAD src0_sel:WORD_0
	v_exp_f16_sdwa v89, v85 dst_sel:WORD_0 dst_unused:UNUSED_PAD src0_sel:WORD_0
	v_exp_f16_sdwa v86, v82 dst_sel:WORD_1 dst_unused:UNUSED_PRESERVE src0_sel:WORD_1
	v_exp_f16_sdwa v87, v83 dst_sel:WORD_1 dst_unused:UNUSED_PRESERVE src0_sel:WORD_1
	v_exp_f16_sdwa v88, v84 dst_sel:WORD_1 dst_unused:UNUSED_PRESERVE src0_sel:WORD_1
	v_exp_f16_sdwa v89, v85 dst_sel:WORD_1 dst_unused:UNUSED_PRESERVE src0_sel:WORD_1
	v_pk_add_f16 v82, v189, v154 neg_lo:[0,1] neg_hi:[0,1]
	v_pk_add_f16 v62, v62, v89
	v_pk_add_f16 v63, v63, v88
	v_pk_add_f16 v64, v64, v87
	v_pk_add_f16 v65, v65, v86
	v_pk_fma_f16 v45, v33, v89, v45
	v_pk_fma_f16 v44, v32, v88, v44
	v_pk_fma_f16 v43, v31, v87, v43
	v_pk_fma_f16 v42, v30, v86, v42
	v_pk_add_f16 v83, v188, v155 neg_lo:[0,1] neg_hi:[0,1]
	v_pk_add_f16 v84, v187, v156 neg_lo:[0,1] neg_hi:[0,1]
	v_pk_add_f16 v85, v186, v157 neg_lo:[0,1] neg_hi:[0,1]
	v_exp_f16_sdwa v86, v82 dst_sel:WORD_0 dst_unused:UNUSED_PAD src0_sel:WORD_0
	v_exp_f16_sdwa v87, v83 dst_sel:WORD_0 dst_unused:UNUSED_PAD src0_sel:WORD_0
	v_exp_f16_sdwa v88, v84 dst_sel:WORD_0 dst_unused:UNUSED_PAD src0_sel:WORD_0
	v_exp_f16_sdwa v89, v85 dst_sel:WORD_0 dst_unused:UNUSED_PAD src0_sel:WORD_0
	v_exp_f16_sdwa v86, v82 dst_sel:WORD_1 dst_unused:UNUSED_PRESERVE src0_sel:WORD_1
	v_exp_f16_sdwa v87, v83 dst_sel:WORD_1 dst_unused:UNUSED_PRESERVE src0_sel:WORD_1
	v_exp_f16_sdwa v88, v84 dst_sel:WORD_1 dst_unused:UNUSED_PRESERVE src0_sel:WORD_1
	v_exp_f16_sdwa v89, v85 dst_sel:WORD_1 dst_unused:UNUSED_PRESERVE src0_sel:WORD_1
	v_exp_f16_sdwa v82, v70 dst_sel:WORD_0 dst_unused:UNUSED_PAD src0_sel:WORD_0
	v_exp_f16_sdwa v83, v71 dst_sel:WORD_0 dst_unused:UNUSED_PAD src0_sel:WORD_0
	v_exp_f16_sdwa v84, v72 dst_sel:WORD_0 dst_unused:UNUSED_PAD src0_sel:WORD_0
	v_exp_f16_sdwa v85, v73 dst_sel:WORD_0 dst_unused:UNUSED_PAD src0_sel:WORD_0
	v_exp_f16_sdwa v82, v70 dst_sel:WORD_1 dst_unused:UNUSED_PRESERVE src0_sel:WORD_1
	v_exp_f16_sdwa v83, v71 dst_sel:WORD_1 dst_unused:UNUSED_PRESERVE src0_sel:WORD_1
	v_exp_f16_sdwa v84, v72 dst_sel:WORD_1 dst_unused:UNUSED_PRESERVE src0_sel:WORD_1
	v_exp_f16_sdwa v85, v73 dst_sel:WORD_1 dst_unused:UNUSED_PRESERVE src0_sel:WORD_1
	v_pk_add_f16 v70, v98, v154 neg_lo:[0,1] neg_hi:[0,1]
	v_pk_add_f16 v62, v62, v89
	v_pk_add_f16 v65, v65, v86
	v_pk_add_f16 v64, v64, v87
	v_pk_add_f16 v63, v63, v88
	v_pk_fma_f16 v42, v46, v86, v42
	v_pk_fma_f16 v43, v47, v87, v43
	v_pk_fma_f16 v44, v48, v88, v44
	v_pk_fma_f16 v45, v49, v89, v45
	v_pk_add_f16 v62, v62, v85
	v_pk_add_f16 v63, v63, v84
	v_pk_add_f16 v64, v64, v83
	v_pk_add_f16 v65, v65, v82
	v_pk_fma_f16 v45, v9, v85, v45
	v_pk_fma_f16 v44, v8, v84, v44
	v_pk_fma_f16 v43, v7, v83, v43
	v_pk_fma_f16 v42, v6, v82, v42
	v_pk_add_f16 v71, v99, v155 neg_lo:[0,1] neg_hi:[0,1]
	v_pk_add_f16 v72, v100, v156 neg_lo:[0,1] neg_hi:[0,1]
	v_pk_add_f16 v73, v101, v157 neg_lo:[0,1] neg_hi:[0,1]
	v_exp_f16_sdwa v82, v70 dst_sel:WORD_0 dst_unused:UNUSED_PAD src0_sel:WORD_0
	v_exp_f16_sdwa v83, v71 dst_sel:WORD_0 dst_unused:UNUSED_PAD src0_sel:WORD_0
	v_exp_f16_sdwa v84, v72 dst_sel:WORD_0 dst_unused:UNUSED_PAD src0_sel:WORD_0
	v_exp_f16_sdwa v85, v73 dst_sel:WORD_0 dst_unused:UNUSED_PAD src0_sel:WORD_0
	v_exp_f16_sdwa v82, v70 dst_sel:WORD_1 dst_unused:UNUSED_PRESERVE src0_sel:WORD_1
	v_exp_f16_sdwa v83, v71 dst_sel:WORD_1 dst_unused:UNUSED_PRESERVE src0_sel:WORD_1
	v_exp_f16_sdwa v84, v72 dst_sel:WORD_1 dst_unused:UNUSED_PRESERVE src0_sel:WORD_1
	v_exp_f16_sdwa v85, v73 dst_sel:WORD_1 dst_unused:UNUSED_PRESERVE src0_sel:WORD_1
	v_pk_add_f16 v70, v114, v154 neg_lo:[0,1] neg_hi:[0,1]
	v_pk_add_f16 v62, v62, v85
	v_pk_add_f16 v65, v65, v82
	v_pk_add_f16 v64, v64, v83
	v_pk_add_f16 v63, v63, v84
	v_pk_fma_f16 v42, v10, v82, v42
	v_pk_fma_f16 v43, v11, v83, v43
	v_pk_fma_f16 v44, v12, v84, v44
	v_pk_fma_f16 v45, v13, v85, v45
	v_pk_add_f16 v71, v115, v155 neg_lo:[0,1] neg_hi:[0,1]
	v_pk_add_f16 v72, v116, v156 neg_lo:[0,1] neg_hi:[0,1]
	v_pk_add_f16 v73, v117, v157 neg_lo:[0,1] neg_hi:[0,1]
	v_exp_f16_sdwa v82, v70 dst_sel:WORD_0 dst_unused:UNUSED_PAD src0_sel:WORD_0
	v_exp_f16_sdwa v83, v71 dst_sel:WORD_0 dst_unused:UNUSED_PAD src0_sel:WORD_0
	v_exp_f16_sdwa v84, v72 dst_sel:WORD_0 dst_unused:UNUSED_PAD src0_sel:WORD_0
	v_exp_f16_sdwa v85, v73 dst_sel:WORD_0 dst_unused:UNUSED_PAD src0_sel:WORD_0
	v_exp_f16_sdwa v82, v70 dst_sel:WORD_1 dst_unused:UNUSED_PRESERVE src0_sel:WORD_1
	v_exp_f16_sdwa v83, v71 dst_sel:WORD_1 dst_unused:UNUSED_PRESERVE src0_sel:WORD_1
	v_exp_f16_sdwa v84, v72 dst_sel:WORD_1 dst_unused:UNUSED_PRESERVE src0_sel:WORD_1
	v_exp_f16_sdwa v85, v73 dst_sel:WORD_1 dst_unused:UNUSED_PRESERVE src0_sel:WORD_1
	s_nop 0
	v_pk_add_f16 v62, v62, v85
	v_pk_add_f16 v63, v63, v84
	v_pk_add_f16 v64, v64, v83
	v_pk_add_f16 v65, v65, v82
	v_rcp_f16_e32 v73, v62
	v_rcp_f16_sdwa v62, v62 dst_sel:DWORD dst_unused:UNUSED_PAD src0_sel:WORD_1
	v_rcp_f16_e32 v70, v65
	v_rcp_f16_sdwa v65, v65 dst_sel:DWORD dst_unused:UNUSED_PAD src0_sel:WORD_1
	v_rcp_f16_e32 v71, v64
	v_rcp_f16_sdwa v64, v64 dst_sel:DWORD dst_unused:UNUSED_PAD src0_sel:WORD_1
	v_rcp_f16_e32 v72, v63
	v_rcp_f16_sdwa v63, v63 dst_sel:DWORD dst_unused:UNUSED_PAD src0_sel:WORD_1
	v_pk_fma_f16 v45, v17, v85, v45
	v_pack_b32_f16 v62, v73, v62
	v_pk_fma_f16 v44, v16, v84, v44
	v_pk_fma_f16 v43, v15, v83, v43
	v_pk_fma_f16 v42, v14, v82, v42
	v_pack_b32_f16 v65, v70, v65
	v_pack_b32_f16 v64, v71, v64
	v_pack_b32_f16 v63, v72, v63
	v_pk_mul_f16 v45, v45, v62
	s_waitcnt vmcnt(6)
	v_pk_mul_f16 v62, v185, v150 op_sel_hi:[0,1]
	v_pk_mul_f16 v70, v183, v150 op_sel_hi:[0,1]
	v_pk_mul_f16 v82, v184, v150 op_sel_hi:[0,1]
	v_pk_mul_f16 v42, v42, v65
	v_pk_mul_f16 v43, v43, v64
	v_pk_mul_f16 v44, v44, v63
	v_pk_mul_f16 v63, v185, v151 op_sel_hi:[0,1]
	v_pk_mul_f16 v64, v185, v152 op_sel_hi:[0,1]
	v_pk_mul_f16 v65, v185, v153 op_sel_hi:[0,1]
	v_pk_mul_f16 v71, v183, v151 op_sel_hi:[0,1]
	v_pk_mul_f16 v72, v183, v152 op_sel_hi:[0,1]
	v_pk_mul_f16 v73, v183, v153 op_sel_hi:[0,1]
	v_pk_mul_f16 v83, v184, v151 op_sel_hi:[0,1]
	v_pk_mul_f16 v84, v184, v152 op_sel_hi:[0,1]
	v_pk_mul_f16 v85, v184, v153 op_sel_hi:[0,1]
	v_pk_fma_f16 v50, v50, v150, v62
	v_pk_fma_f16 v66, v66, v150, v70
	v_pk_fma_f16 v89, v94, v150, v82
	v_pk_fma_f16 v53, v53, v153, v65
	v_pk_maximum3_f16 v114, v50, v66, v89
	v_pk_fma_f16 v52, v52, v152, v64
	v_pk_fma_f16 v51, v51, v151, v63
	v_pk_fma_f16 v69, v69, v153, v73
	v_pk_fma_f16 v68, v68, v152, v72
	v_pk_fma_f16 v67, v67, v151, v71
	v_pk_fma_f16 v86, v97, v153, v85
	v_pk_fma_f16 v87, v96, v152, v84
	v_pk_fma_f16 v88, v95, v151, v83
	v_pk_fma_f16 v97, v18, v150, v62
	v_pk_fma_f16 v101, v34, v150, v70
	v_pk_fma_f16 v109, v54, v150, v82
	v_pk_fma_f16 v62, v74, v150, v62
	v_pk_fma_f16 v70, v102, v150, v70
	v_pk_fma_f16 v82, v118, v150, v82
	v_pk_maximum3_f16 v115, v51, v67, v88
	v_pk_maximum3_f16 v116, v52, v68, v87
	v_pk_maximum3_f16 v117, v53, v69, v86
	v_pk_maximum3_f16 v122, v97, v101, v109
	v_pk_fma_f16 v94, v21, v153, v65
	v_pk_maximum3_f16 v126, v62, v70, v82
	v_pk_fma_f16 v95, v20, v152, v64
	v_pk_maximum3_f16 v114, v114, v122, v126
	v_pk_fma_f16 v96, v19, v151, v63
	v_pk_fma_f16 v98, v37, v153, v73
	v_pk_fma_f16 v99, v36, v152, v72
	v_pk_fma_f16 v100, v35, v151, v71
	v_pk_fma_f16 v106, v57, v153, v85
	v_pk_fma_f16 v107, v56, v152, v84
	v_pk_fma_f16 v108, v55, v151, v83
	v_pk_fma_f16 v65, v77, v153, v65
	v_pk_fma_f16 v64, v76, v152, v64
	v_pk_fma_f16 v63, v75, v151, v63
	v_pk_fma_f16 v73, v105, v153, v73
	v_pk_fma_f16 v72, v104, v152, v72
	v_pk_fma_f16 v71, v103, v151, v71
	v_pk_fma_f16 v85, v121, v153, v85
	v_pk_fma_f16 v84, v120, v152, v84
	v_pk_fma_f16 v83, v119, v151, v83
	v_pk_maximum3_f16 v123, v96, v100, v108
	v_pk_maximum3_f16 v124, v95, v99, v107
	v_pk_maximum3_f16 v125, v94, v98, v106
	v_pk_maximum3_f16 v128, v64, v72, v84
	v_pk_maximum3_f16 v129, v65, v73, v85
	v_pk_maximum3_f16 v127, v63, v71, v83
	v_pk_maximum3_f16 v115, v115, v123, v127
	v_pk_maximum3_f16 v116, v116, v124, v128
	v_pk_maximum3_f16 v117, v117, v125, v129
	v_pk_add_f16 v50, v50, v114 neg_lo:[0,1] neg_hi:[0,1]
	v_pk_add_f16 v51, v51, v115 neg_lo:[0,1] neg_hi:[0,1]
	v_pk_add_f16 v52, v52, v116 neg_lo:[0,1] neg_hi:[0,1]
	v_pk_add_f16 v53, v53, v117 neg_lo:[0,1] neg_hi:[0,1]
	v_pk_add_f16 v66, v66, v114 neg_lo:[0,1] neg_hi:[0,1]
	v_exp_f16_sdwa v122, v50 dst_sel:WORD_0 dst_unused:UNUSED_PAD src0_sel:WORD_0
	v_exp_f16_sdwa v123, v51 dst_sel:WORD_0 dst_unused:UNUSED_PAD src0_sel:WORD_0
	v_exp_f16_sdwa v124, v52 dst_sel:WORD_0 dst_unused:UNUSED_PAD src0_sel:WORD_0
	v_exp_f16_sdwa v125, v53 dst_sel:WORD_0 dst_unused:UNUSED_PAD src0_sel:WORD_0
	v_exp_f16_sdwa v122, v50 dst_sel:WORD_1 dst_unused:UNUSED_PRESERVE src0_sel:WORD_1
	v_exp_f16_sdwa v123, v51 dst_sel:WORD_1 dst_unused:UNUSED_PRESERVE src0_sel:WORD_1
	v_exp_f16_sdwa v124, v52 dst_sel:WORD_1 dst_unused:UNUSED_PRESERVE src0_sel:WORD_1
	v_exp_f16_sdwa v125, v53 dst_sel:WORD_1 dst_unused:UNUSED_PRESERVE src0_sel:WORD_1
	v_pk_add_f16 v67, v67, v115 neg_lo:[0,1] neg_hi:[0,1]
	v_pk_add_f16 v50, v125, 0
	v_pk_fma_f16 v22, v22, v122, 0
	v_pk_add_f16 v51, v124, 0
	v_pk_add_f16 v52, v123, 0
	v_pk_add_f16 v53, v122, 0
	v_pk_fma_f16 v23, v23, v123, 0
	v_pk_fma_f16 v24, v24, v124, 0
	v_pk_fma_f16 v25, v25, v125, 0
	v_pk_add_f16 v68, v68, v116 neg_lo:[0,1] neg_hi:[0,1]
	v_pk_add_f16 v69, v69, v117 neg_lo:[0,1] neg_hi:[0,1]
	v_exp_f16_sdwa v122, v66 dst_sel:WORD_0 dst_unused:UNUSED_PAD src0_sel:WORD_0
	v_exp_f16_sdwa v123, v67 dst_sel:WORD_0 dst_unused:UNUSED_PAD src0_sel:WORD_0
	v_exp_f16_sdwa v124, v68 dst_sel:WORD_0 dst_unused:UNUSED_PAD src0_sel:WORD_0
	v_exp_f16_sdwa v125, v69 dst_sel:WORD_0 dst_unused:UNUSED_PAD src0_sel:WORD_0
	v_exp_f16_sdwa v122, v66 dst_sel:WORD_1 dst_unused:UNUSED_PRESERVE src0_sel:WORD_1
	v_exp_f16_sdwa v123, v67 dst_sel:WORD_1 dst_unused:UNUSED_PRESERVE src0_sel:WORD_1
	v_exp_f16_sdwa v124, v68 dst_sel:WORD_1 dst_unused:UNUSED_PRESERVE src0_sel:WORD_1
	v_exp_f16_sdwa v125, v69 dst_sel:WORD_1 dst_unused:UNUSED_PRESERVE src0_sel:WORD_1
	s_nop 0
	v_pk_add_f16 v50, v50, v125
	v_pk_fma_f16 v22, v30, v122, v22
	v_pk_add_f16 v30, v89, v114 neg_lo:[0,1] neg_hi:[0,1]
	v_pk_add_f16 v53, v53, v122
	v_pk_add_f16 v52, v52, v123
	v_pk_add_f16 v51, v51, v124
	v_pk_fma_f16 v25, v33, v125, v25
	v_pk_fma_f16 v24, v32, v124, v24
	v_pk_fma_f16 v23, v31, v123, v23
	v_pk_add_f16 v31, v88, v115 neg_lo:[0,1] neg_hi:[0,1]
	v_pk_add_f16 v32, v87, v116 neg_lo:[0,1] neg_hi:[0,1]
	v_pk_add_f16 v33, v86, v117 neg_lo:[0,1] neg_hi:[0,1]
	v_exp_f16_sdwa v66, v30 dst_sel:WORD_0 dst_unused:UNUSED_PAD src0_sel:WORD_0
	v_exp_f16_sdwa v67, v31 dst_sel:WORD_0 dst_unused:UNUSED_PAD src0_sel:WORD_0
	v_exp_f16_sdwa v68, v32 dst_sel:WORD_0 dst_unused:UNUSED_PAD src0_sel:WORD_0
	v_exp_f16_sdwa v69, v33 dst_sel:WORD_0 dst_unused:UNUSED_PAD src0_sel:WORD_0
	v_exp_f16_sdwa v66, v30 dst_sel:WORD_1 dst_unused:UNUSED_PRESERVE src0_sel:WORD_1
	v_exp_f16_sdwa v67, v31 dst_sel:WORD_1 dst_unused:UNUSED_PRESERVE src0_sel:WORD_1
	v_exp_f16_sdwa v68, v32 dst_sel:WORD_1 dst_unused:UNUSED_PRESERVE src0_sel:WORD_1
	v_exp_f16_sdwa v69, v33 dst_sel:WORD_1 dst_unused:UNUSED_PRESERVE src0_sel:WORD_1
	s_nop 0
	v_pk_add_f16 v30, v50, v69
	v_pk_add_f16 v31, v51, v68
	v_pk_add_f16 v32, v52, v67
	v_pk_add_f16 v33, v53, v66
	v_pk_fma_f16 v22, v46, v66, v22
	v_pk_fma_f16 v23, v47, v67, v23
	v_pk_fma_f16 v24, v48, v68, v24
	v_pk_fma_f16 v25, v49, v69, v25
	v_pk_add_f16 v46, v97, v114 neg_lo:[0,1] neg_hi:[0,1]
	v_pk_add_f16 v47, v96, v115 neg_lo:[0,1] neg_hi:[0,1]
	v_pk_add_f16 v48, v95, v116 neg_lo:[0,1] neg_hi:[0,1]
	v_pk_add_f16 v49, v94, v117 neg_lo:[0,1] neg_hi:[0,1]
	v_exp_f16_sdwa v50, v46 dst_sel:WORD_0 dst_unused:UNUSED_PAD src0_sel:WORD_0
	v_exp_f16_sdwa v51, v47 dst_sel:WORD_0 dst_unused:UNUSED_PAD src0_sel:WORD_0
	v_exp_f16_sdwa v52, v48 dst_sel:WORD_0 dst_unused:UNUSED_PAD src0_sel:WORD_0
	v_exp_f16_sdwa v53, v49 dst_sel:WORD_0 dst_unused:UNUSED_PAD src0_sel:WORD_0
	v_exp_f16_sdwa v50, v46 dst_sel:WORD_1 dst_unused:UNUSED_PRESERVE src0_sel:WORD_1
	v_exp_f16_sdwa v51, v47 dst_sel:WORD_1 dst_unused:UNUSED_PRESERVE src0_sel:WORD_1
	v_exp_f16_sdwa v52, v48 dst_sel:WORD_1 dst_unused:UNUSED_PRESERVE src0_sel:WORD_1
	v_exp_f16_sdwa v53, v49 dst_sel:WORD_1 dst_unused:UNUSED_PRESERVE src0_sel:WORD_1
	v_pk_add_f16 v46, v101, v114 neg_lo:[0,1] neg_hi:[0,1]
	v_pk_add_f16 v30, v30, v53
	v_pk_add_f16 v33, v33, v50
	v_pk_add_f16 v32, v32, v51
	v_pk_add_f16 v31, v31, v52
	v_pk_fma_f16 v25, v9, v53, v25
	v_pk_fma_f16 v24, v8, v52, v24
	v_pk_fma_f16 v23, v7, v51, v23
	v_pk_fma_f16 v22, v6, v50, v22
	v_pk_add_f16 v47, v100, v115 neg_lo:[0,1] neg_hi:[0,1]
	v_pk_add_f16 v48, v99, v116 neg_lo:[0,1] neg_hi:[0,1]
	v_pk_add_f16 v49, v98, v117 neg_lo:[0,1] neg_hi:[0,1]
	v_exp_f16_sdwa v50, v46 dst_sel:WORD_0 dst_unused:UNUSED_PAD src0_sel:WORD_0
	v_exp_f16_sdwa v51, v47 dst_sel:WORD_0 dst_unused:UNUSED_PAD src0_sel:WORD_0
	v_exp_f16_sdwa v52, v48 dst_sel:WORD_0 dst_unused:UNUSED_PAD src0_sel:WORD_0
	v_exp_f16_sdwa v53, v49 dst_sel:WORD_0 dst_unused:UNUSED_PAD src0_sel:WORD_0
	v_exp_f16_sdwa v50, v46 dst_sel:WORD_1 dst_unused:UNUSED_PRESERVE src0_sel:WORD_1
	v_exp_f16_sdwa v51, v47 dst_sel:WORD_1 dst_unused:UNUSED_PRESERVE src0_sel:WORD_1
	v_exp_f16_sdwa v52, v48 dst_sel:WORD_1 dst_unused:UNUSED_PRESERVE src0_sel:WORD_1
	v_exp_f16_sdwa v53, v49 dst_sel:WORD_1 dst_unused:UNUSED_PRESERVE src0_sel:WORD_1
	v_pk_add_f16 v46, v109, v114 neg_lo:[0,1] neg_hi:[0,1]
	v_pk_add_f16 v30, v30, v53
	v_pk_add_f16 v31, v31, v52
	v_pk_add_f16 v32, v32, v51
	v_pk_add_f16 v33, v33, v50
	v_pk_fma_f16 v22, v10, v50, v22
	v_pk_fma_f16 v23, v11, v51, v23
	v_pk_fma_f16 v24, v12, v52, v24
	v_pk_fma_f16 v25, v13, v53, v25
	v_pk_add_f16 v47, v108, v115 neg_lo:[0,1] neg_hi:[0,1]
	v_pk_add_f16 v48, v107, v116 neg_lo:[0,1] neg_hi:[0,1]
	v_pk_add_f16 v49, v106, v117 neg_lo:[0,1] neg_hi:[0,1]
	v_exp_f16_sdwa v50, v46 dst_sel:WORD_0 dst_unused:UNUSED_PAD src0_sel:WORD_0
	v_exp_f16_sdwa v51, v47 dst_sel:WORD_0 dst_unused:UNUSED_PAD src0_sel:WORD_0
	v_exp_f16_sdwa v52, v48 dst_sel:WORD_0 dst_unused:UNUSED_PAD src0_sel:WORD_0
	v_exp_f16_sdwa v53, v49 dst_sel:WORD_0 dst_unused:UNUSED_PAD src0_sel:WORD_0
	v_exp_f16_sdwa v50, v46 dst_sel:WORD_1 dst_unused:UNUSED_PRESERVE src0_sel:WORD_1
	v_exp_f16_sdwa v51, v47 dst_sel:WORD_1 dst_unused:UNUSED_PRESERVE src0_sel:WORD_1
	v_exp_f16_sdwa v52, v48 dst_sel:WORD_1 dst_unused:UNUSED_PRESERVE src0_sel:WORD_1
	v_exp_f16_sdwa v53, v49 dst_sel:WORD_1 dst_unused:UNUSED_PRESERVE src0_sel:WORD_1
	v_pk_add_f16 v46, v62, v114 neg_lo:[0,1] neg_hi:[0,1]
	v_pk_add_f16 v30, v30, v53
	v_pk_add_f16 v33, v33, v50
	v_pk_add_f16 v32, v32, v51
	v_pk_add_f16 v31, v31, v52
	v_pk_fma_f16 v25, v17, v53, v25
	v_pk_fma_f16 v24, v16, v52, v24
	v_pk_fma_f16 v23, v15, v51, v23
	v_pk_fma_f16 v22, v14, v50, v22
	v_pk_add_f16 v47, v63, v115 neg_lo:[0,1] neg_hi:[0,1]
	v_pk_add_f16 v48, v64, v116 neg_lo:[0,1] neg_hi:[0,1]
	v_pk_add_f16 v49, v65, v117 neg_lo:[0,1] neg_hi:[0,1]
	v_exp_f16_sdwa v50, v46 dst_sel:WORD_0 dst_unused:UNUSED_PAD src0_sel:WORD_0
	v_exp_f16_sdwa v51, v47 dst_sel:WORD_0 dst_unused:UNUSED_PAD src0_sel:WORD_0
	v_exp_f16_sdwa v52, v48 dst_sel:WORD_0 dst_unused:UNUSED_PAD src0_sel:WORD_0
	v_exp_f16_sdwa v53, v49 dst_sel:WORD_0 dst_unused:UNUSED_PAD src0_sel:WORD_0
	v_exp_f16_sdwa v50, v46 dst_sel:WORD_1 dst_unused:UNUSED_PRESERVE src0_sel:WORD_1
	v_exp_f16_sdwa v51, v47 dst_sel:WORD_1 dst_unused:UNUSED_PRESERVE src0_sel:WORD_1
	v_exp_f16_sdwa v52, v48 dst_sel:WORD_1 dst_unused:UNUSED_PRESERVE src0_sel:WORD_1
	v_exp_f16_sdwa v53, v49 dst_sel:WORD_1 dst_unused:UNUSED_PRESERVE src0_sel:WORD_1
	v_pk_add_f16 v46, v70, v114 neg_lo:[0,1] neg_hi:[0,1]
	v_pk_add_f16 v30, v30, v53
	v_pk_add_f16 v31, v31, v52
	v_pk_add_f16 v32, v32, v51
	v_pk_add_f16 v33, v33, v50
	v_pk_fma_f16 v22, v26, v50, v22
	v_pk_fma_f16 v23, v27, v51, v23
	v_pk_fma_f16 v24, v28, v52, v24
	v_pk_fma_f16 v25, v29, v53, v25
	v_pk_add_f16 v47, v71, v115 neg_lo:[0,1] neg_hi:[0,1]
	v_pk_add_f16 v48, v72, v116 neg_lo:[0,1] neg_hi:[0,1]
	v_pk_add_f16 v49, v73, v117 neg_lo:[0,1] neg_hi:[0,1]
	v_exp_f16_sdwa v50, v46 dst_sel:WORD_0 dst_unused:UNUSED_PAD src0_sel:WORD_0
	v_exp_f16_sdwa v51, v47 dst_sel:WORD_0 dst_unused:UNUSED_PAD src0_sel:WORD_0
	v_exp_f16_sdwa v52, v48 dst_sel:WORD_0 dst_unused:UNUSED_PAD src0_sel:WORD_0
	v_exp_f16_sdwa v53, v49 dst_sel:WORD_0 dst_unused:UNUSED_PAD src0_sel:WORD_0
	v_exp_f16_sdwa v50, v46 dst_sel:WORD_1 dst_unused:UNUSED_PRESERVE src0_sel:WORD_1
	v_exp_f16_sdwa v51, v47 dst_sel:WORD_1 dst_unused:UNUSED_PRESERVE src0_sel:WORD_1
	v_exp_f16_sdwa v52, v48 dst_sel:WORD_1 dst_unused:UNUSED_PRESERVE src0_sel:WORD_1
	v_exp_f16_sdwa v53, v49 dst_sel:WORD_1 dst_unused:UNUSED_PRESERVE src0_sel:WORD_1
	v_pk_add_f16 v46, v82, v114 neg_lo:[0,1] neg_hi:[0,1]
	v_pk_add_f16 v30, v30, v53
	v_pk_add_f16 v33, v33, v50
	v_pk_add_f16 v32, v32, v51
	v_pk_add_f16 v31, v31, v52
	v_pk_fma_f16 v25, v41, v53, v25
	v_pk_fma_f16 v24, v40, v52, v24
	v_pk_fma_f16 v23, v39, v51, v23
	v_pk_fma_f16 v22, v38, v50, v22
	v_pk_add_f16 v47, v83, v115 neg_lo:[0,1] neg_hi:[0,1]
	v_pk_add_f16 v48, v84, v116 neg_lo:[0,1] neg_hi:[0,1]
	v_pk_add_f16 v49, v85, v117 neg_lo:[0,1] neg_hi:[0,1]
	v_exp_f16_sdwa v50, v46 dst_sel:WORD_0 dst_unused:UNUSED_PAD src0_sel:WORD_0
	v_exp_f16_sdwa v51, v47 dst_sel:WORD_0 dst_unused:UNUSED_PAD src0_sel:WORD_0
	v_exp_f16_sdwa v52, v48 dst_sel:WORD_0 dst_unused:UNUSED_PAD src0_sel:WORD_0
	v_exp_f16_sdwa v53, v49 dst_sel:WORD_0 dst_unused:UNUSED_PAD src0_sel:WORD_0
	v_exp_f16_sdwa v50, v46 dst_sel:WORD_1 dst_unused:UNUSED_PRESERVE src0_sel:WORD_1
	v_exp_f16_sdwa v51, v47 dst_sel:WORD_1 dst_unused:UNUSED_PRESERVE src0_sel:WORD_1
	v_exp_f16_sdwa v52, v48 dst_sel:WORD_1 dst_unused:UNUSED_PRESERVE src0_sel:WORD_1
	v_exp_f16_sdwa v53, v49 dst_sel:WORD_1 dst_unused:UNUSED_PRESERVE src0_sel:WORD_1
	s_nop 0
	v_pk_add_f16 v30, v30, v53
	v_pk_add_f16 v31, v31, v52
	v_rcp_f16_e32 v48, v30
	v_rcp_f16_sdwa v30, v30 dst_sel:DWORD dst_unused:UNUSED_PAD src0_sel:WORD_1
	v_pk_add_f16 v32, v32, v51
	v_rcp_f16_e32 v49, v31
	v_rcp_f16_sdwa v31, v31 dst_sel:DWORD dst_unused:UNUSED_PAD src0_sel:WORD_1
	v_pk_add_f16 v33, v33, v50
	v_rcp_f16_e32 v47, v32
	v_rcp_f16_sdwa v32, v32 dst_sel:DWORD dst_unused:UNUSED_PAD src0_sel:WORD_1
	v_rcp_f16_e32 v46, v33
	v_rcp_f16_sdwa v33, v33 dst_sel:DWORD dst_unused:UNUSED_PAD src0_sel:WORD_1
	v_pk_fma_f16 v25, v61, v53, v25
	v_pack_b32_f16 v30, v48, v30
	v_pk_fma_f16 v24, v60, v52, v24
	v_pk_mul_f16 v25, v25, v30
	v_pack_b32_f16 v30, v49, v31
	v_pk_fma_f16 v23, v59, v51, v23
	v_pk_mul_f16 v24, v24, v30
	v_pack_b32_f16 v30, v47, v32
	v_pk_fma_f16 v22, v58, v50, v22
	v_pk_mul_f16 v23, v23, v30
	v_pack_b32_f16 v30, v46, v33
	v_pk_mul_f16 v22, v22, v30
	s_waitcnt vmcnt(0)
	v_pk_mul_f16 v30, v185, v146 op_sel_hi:[0,1]
	v_pk_mul_f16 v31, v185, v147 op_sel_hi:[0,1]
	v_pk_mul_f16 v32, v185, v148 op_sel_hi:[0,1]
	v_pk_mul_f16 v33, v185, v149 op_sel_hi:[0,1]
	v_pk_mul_f16 v46, v183, v146 op_sel_hi:[0,1]
	v_pk_mul_f16 v47, v183, v147 op_sel_hi:[0,1]
	v_pk_mul_f16 v48, v183, v148 op_sel_hi:[0,1]
	v_pk_mul_f16 v49, v183, v149 op_sel_hi:[0,1]
	v_pk_mul_f16 v50, v184, v146 op_sel_hi:[0,1]
	v_pk_mul_f16 v51, v184, v147 op_sel_hi:[0,1]
	v_pk_mul_f16 v52, v184, v148 op_sel_hi:[0,1]
	v_pk_mul_f16 v53, v184, v149 op_sel_hi:[0,1]
	v_pk_fma_f16 v21, v21, v149, v33
	v_pk_fma_f16 v20, v20, v148, v32
	v_pk_fma_f16 v19, v19, v147, v31
	v_pk_fma_f16 v18, v18, v146, v30
	v_pk_fma_f16 v37, v37, v149, v49
	v_pk_fma_f16 v36, v36, v148, v48
	v_pk_fma_f16 v35, v35, v147, v47
	v_pk_fma_f16 v34, v34, v146, v46
	v_pk_fma_f16 v57, v57, v149, v53
	v_pk_fma_f16 v56, v56, v148, v52
	v_pk_fma_f16 v55, v55, v147, v51
	v_pk_fma_f16 v54, v54, v146, v50
	v_pk_fma_f16 v62, v77, v149, v33
	v_pk_fma_f16 v63, v76, v148, v32
	v_pk_fma_f16 v64, v75, v147, v31
	v_pk_fma_f16 v65, v74, v146, v30
	v_pk_maximum3_f16 v74, v18, v34, v54
	v_pk_maximum3_f16 v75, v19, v35, v55
	v_pk_maximum3_f16 v76, v20, v36, v56
	v_pk_maximum3_f16 v77, v21, v37, v57
	v_pk_fma_f16 v66, v105, v149, v49
	v_pk_fma_f16 v67, v104, v148, v48
	v_pk_fma_f16 v68, v103, v147, v47
	v_pk_fma_f16 v69, v102, v146, v46
	v_pk_fma_f16 v70, v121, v149, v53
	v_pk_fma_f16 v71, v120, v148, v52
	v_pk_fma_f16 v72, v119, v147, v51
	v_pk_fma_f16 v73, v118, v146, v50
	v_pk_fma_f16 v33, v133, v149, v33
	v_pk_fma_f16 v32, v132, v148, v32
	v_pk_fma_f16 v31, v131, v147, v31
	v_pk_fma_f16 v30, v130, v146, v30
	v_pk_fma_f16 v49, v141, v149, v49
	v_pk_fma_f16 v48, v140, v148, v48
	v_pk_fma_f16 v47, v139, v147, v47
	v_pk_fma_f16 v46, v138, v146, v46
	v_pk_fma_f16 v53, v145, v149, v53
	v_pk_fma_f16 v52, v144, v148, v52
	v_pk_fma_f16 v51, v143, v147, v51
	v_pk_fma_f16 v50, v142, v146, v50
	v_pk_maximum3_f16 v82, v65, v69, v73
	v_pk_maximum3_f16 v83, v64, v68, v72
	v_pk_maximum3_f16 v84, v63, v67, v71
	v_pk_maximum3_f16 v85, v62, v66, v70
	v_pk_maximum3_f16 v87, v31, v47, v51
	v_pk_maximum3_f16 v86, v30, v46, v50
	v_pk_maximum3_f16 v88, v32, v48, v52
	v_pk_maximum3_f16 v89, v33, v49, v53
	v_pk_maximum3_f16 v74, v74, v82, v86
	v_pk_maximum3_f16 v75, v75, v83, v87
	v_pk_maximum3_f16 v76, v76, v84, v88
	v_pk_maximum3_f16 v77, v77, v85, v89
	s_nop 0
	v_pk_add_f16 v18, v18, v74 neg_lo:[0,1] neg_hi:[0,1]
	v_pk_add_f16 v19, v19, v75 neg_lo:[0,1] neg_hi:[0,1]
	v_pk_add_f16 v20, v20, v76 neg_lo:[0,1] neg_hi:[0,1]
	v_pk_add_f16 v21, v21, v77 neg_lo:[0,1] neg_hi:[0,1]
	v_pk_add_f16 v34, v34, v74 neg_lo:[0,1] neg_hi:[0,1]
	v_exp_f16_sdwa v82, v18 dst_sel:WORD_0 dst_unused:UNUSED_PAD src0_sel:WORD_0
	v_exp_f16_sdwa v83, v19 dst_sel:WORD_0 dst_unused:UNUSED_PAD src0_sel:WORD_0
	v_exp_f16_sdwa v84, v20 dst_sel:WORD_0 dst_unused:UNUSED_PAD src0_sel:WORD_0
	v_exp_f16_sdwa v85, v21 dst_sel:WORD_0 dst_unused:UNUSED_PAD src0_sel:WORD_0
	v_exp_f16_sdwa v82, v18 dst_sel:WORD_1 dst_unused:UNUSED_PRESERVE src0_sel:WORD_1
	v_exp_f16_sdwa v83, v19 dst_sel:WORD_1 dst_unused:UNUSED_PRESERVE src0_sel:WORD_1
	v_exp_f16_sdwa v84, v20 dst_sel:WORD_1 dst_unused:UNUSED_PRESERVE src0_sel:WORD_1
	v_exp_f16_sdwa v85, v21 dst_sel:WORD_1 dst_unused:UNUSED_PRESERVE src0_sel:WORD_1
	v_pk_add_f16 v35, v35, v75 neg_lo:[0,1] neg_hi:[0,1]
	v_pk_add_f16 v18, v82, 0
	v_pk_add_f16 v19, v83, 0
	v_pk_add_f16 v20, v84, 0
	v_pk_add_f16 v21, v85, 0
	v_pk_fma_f16 v6, v6, v82, 0
	v_pk_fma_f16 v7, v7, v83, 0
	v_pk_fma_f16 v8, v8, v84, 0
	v_pk_fma_f16 v9, v9, v85, 0
	v_pk_add_f16 v36, v36, v76 neg_lo:[0,1] neg_hi:[0,1]
	v_pk_add_f16 v37, v37, v77 neg_lo:[0,1] neg_hi:[0,1]
	v_exp_f16_sdwa v82, v34 dst_sel:WORD_0 dst_unused:UNUSED_PAD src0_sel:WORD_0
	v_exp_f16_sdwa v83, v35 dst_sel:WORD_0 dst_unused:UNUSED_PAD src0_sel:WORD_0
	v_exp_f16_sdwa v84, v36 dst_sel:WORD_0 dst_unused:UNUSED_PAD src0_sel:WORD_0
	v_exp_f16_sdwa v85, v37 dst_sel:WORD_0 dst_unused:UNUSED_PAD src0_sel:WORD_0
	v_exp_f16_sdwa v82, v34 dst_sel:WORD_1 dst_unused:UNUSED_PRESERVE src0_sel:WORD_1
	v_exp_f16_sdwa v83, v35 dst_sel:WORD_1 dst_unused:UNUSED_PRESERVE src0_sel:WORD_1
	v_exp_f16_sdwa v84, v36 dst_sel:WORD_1 dst_unused:UNUSED_PRESERVE src0_sel:WORD_1
	v_exp_f16_sdwa v85, v37 dst_sel:WORD_1 dst_unused:UNUSED_PRESERVE src0_sel:WORD_1
	s_nop 0
	v_pk_add_f16 v21, v21, v85
	v_pk_add_f16 v20, v20, v84
	v_pk_add_f16 v19, v19, v83
	v_pk_add_f16 v18, v18, v82
	v_pk_fma_f16 v9, v13, v85, v9
	v_pk_fma_f16 v8, v12, v84, v8
	v_pk_fma_f16 v7, v11, v83, v7
	v_pk_fma_f16 v6, v10, v82, v6
	v_pk_add_f16 v10, v54, v74 neg_lo:[0,1] neg_hi:[0,1]
	v_pk_add_f16 v11, v55, v75 neg_lo:[0,1] neg_hi:[0,1]
	v_pk_add_f16 v12, v56, v76 neg_lo:[0,1] neg_hi:[0,1]
	v_pk_add_f16 v13, v57, v77 neg_lo:[0,1] neg_hi:[0,1]
	v_exp_f16_sdwa v34, v10 dst_sel:WORD_0 dst_unused:UNUSED_PAD src0_sel:WORD_0
	v_exp_f16_sdwa v35, v11 dst_sel:WORD_0 dst_unused:UNUSED_PAD src0_sel:WORD_0
	v_exp_f16_sdwa v36, v12 dst_sel:WORD_0 dst_unused:UNUSED_PAD src0_sel:WORD_0
	v_exp_f16_sdwa v37, v13 dst_sel:WORD_0 dst_unused:UNUSED_PAD src0_sel:WORD_0
	v_exp_f16_sdwa v34, v10 dst_sel:WORD_1 dst_unused:UNUSED_PRESERVE src0_sel:WORD_1
	v_exp_f16_sdwa v35, v11 dst_sel:WORD_1 dst_unused:UNUSED_PRESERVE src0_sel:WORD_1
	v_exp_f16_sdwa v36, v12 dst_sel:WORD_1 dst_unused:UNUSED_PRESERVE src0_sel:WORD_1
	v_exp_f16_sdwa v37, v13 dst_sel:WORD_1 dst_unused:UNUSED_PRESERVE src0_sel:WORD_1
	v_pk_add_f16 v10, v18, v34
	v_pk_add_f16 v11, v19, v35
	v_pk_add_f16 v12, v20, v36
	v_pk_add_f16 v13, v21, v37
	v_pk_fma_f16 v6, v14, v34, v6
	v_pk_fma_f16 v7, v15, v35, v7
	v_pk_fma_f16 v8, v16, v36, v8
	v_pk_fma_f16 v9, v17, v37, v9
	v_pk_add_f16 v14, v65, v74 neg_lo:[0,1] neg_hi:[0,1]
	v_pk_add_f16 v15, v64, v75 neg_lo:[0,1] neg_hi:[0,1]
	v_pk_add_f16 v16, v63, v76 neg_lo:[0,1] neg_hi:[0,1]
	v_pk_add_f16 v17, v62, v77 neg_lo:[0,1] neg_hi:[0,1]
	v_exp_f16_sdwa v18, v14 dst_sel:WORD_0 dst_unused:UNUSED_PAD src0_sel:WORD_0
	v_exp_f16_sdwa v19, v15 dst_sel:WORD_0 dst_unused:UNUSED_PAD src0_sel:WORD_0
	v_exp_f16_sdwa v20, v16 dst_sel:WORD_0 dst_unused:UNUSED_PAD src0_sel:WORD_0
	v_exp_f16_sdwa v21, v17 dst_sel:WORD_0 dst_unused:UNUSED_PAD src0_sel:WORD_0
	v_exp_f16_sdwa v18, v14 dst_sel:WORD_1 dst_unused:UNUSED_PRESERVE src0_sel:WORD_1
	v_exp_f16_sdwa v19, v15 dst_sel:WORD_1 dst_unused:UNUSED_PRESERVE src0_sel:WORD_1
	v_exp_f16_sdwa v20, v16 dst_sel:WORD_1 dst_unused:UNUSED_PRESERVE src0_sel:WORD_1
	v_exp_f16_sdwa v21, v17 dst_sel:WORD_1 dst_unused:UNUSED_PRESERVE src0_sel:WORD_1
	v_pk_add_f16 v14, v69, v74 neg_lo:[0,1] neg_hi:[0,1]
	v_pk_add_f16 v13, v13, v21
	v_pk_add_f16 v12, v12, v20
	v_pk_add_f16 v11, v11, v19
	v_pk_add_f16 v10, v10, v18
	v_pk_fma_f16 v9, v29, v21, v9
	v_pk_fma_f16 v8, v28, v20, v8
	v_pk_fma_f16 v7, v27, v19, v7
	v_pk_fma_f16 v6, v26, v18, v6
	v_pk_add_f16 v15, v68, v75 neg_lo:[0,1] neg_hi:[0,1]
	v_pk_add_f16 v16, v67, v76 neg_lo:[0,1] neg_hi:[0,1]
	v_pk_add_f16 v17, v66, v77 neg_lo:[0,1] neg_hi:[0,1]
	v_exp_f16_sdwa v18, v14 dst_sel:WORD_0 dst_unused:UNUSED_PAD src0_sel:WORD_0
	v_exp_f16_sdwa v19, v15 dst_sel:WORD_0 dst_unused:UNUSED_PAD src0_sel:WORD_0
	v_exp_f16_sdwa v20, v16 dst_sel:WORD_0 dst_unused:UNUSED_PAD src0_sel:WORD_0
	v_exp_f16_sdwa v21, v17 dst_sel:WORD_0 dst_unused:UNUSED_PAD src0_sel:WORD_0
	v_exp_f16_sdwa v18, v14 dst_sel:WORD_1 dst_unused:UNUSED_PRESERVE src0_sel:WORD_1
	v_exp_f16_sdwa v19, v15 dst_sel:WORD_1 dst_unused:UNUSED_PRESERVE src0_sel:WORD_1
	v_exp_f16_sdwa v20, v16 dst_sel:WORD_1 dst_unused:UNUSED_PRESERVE src0_sel:WORD_1
	v_exp_f16_sdwa v21, v17 dst_sel:WORD_1 dst_unused:UNUSED_PRESERVE src0_sel:WORD_1
	v_pk_add_f16 v14, v73, v74 neg_lo:[0,1] neg_hi:[0,1]
	v_pk_add_f16 v10, v10, v18
	v_pk_add_f16 v11, v11, v19
	v_pk_add_f16 v12, v12, v20
	v_pk_add_f16 v13, v13, v21
	v_pk_fma_f16 v6, v38, v18, v6
	v_pk_fma_f16 v7, v39, v19, v7
	v_pk_fma_f16 v8, v40, v20, v8
	v_pk_fma_f16 v9, v41, v21, v9
	v_pk_add_f16 v15, v72, v75 neg_lo:[0,1] neg_hi:[0,1]
	v_pk_add_f16 v16, v71, v76 neg_lo:[0,1] neg_hi:[0,1]
	v_pk_add_f16 v17, v70, v77 neg_lo:[0,1] neg_hi:[0,1]
	v_exp_f16_sdwa v18, v14 dst_sel:WORD_0 dst_unused:UNUSED_PAD src0_sel:WORD_0
	v_exp_f16_sdwa v19, v15 dst_sel:WORD_0 dst_unused:UNUSED_PAD src0_sel:WORD_0
	v_exp_f16_sdwa v20, v16 dst_sel:WORD_0 dst_unused:UNUSED_PAD src0_sel:WORD_0
	v_exp_f16_sdwa v21, v17 dst_sel:WORD_0 dst_unused:UNUSED_PAD src0_sel:WORD_0
	v_exp_f16_sdwa v18, v14 dst_sel:WORD_1 dst_unused:UNUSED_PRESERVE src0_sel:WORD_1
	v_exp_f16_sdwa v19, v15 dst_sel:WORD_1 dst_unused:UNUSED_PRESERVE src0_sel:WORD_1
	v_exp_f16_sdwa v20, v16 dst_sel:WORD_1 dst_unused:UNUSED_PRESERVE src0_sel:WORD_1
	v_exp_f16_sdwa v21, v17 dst_sel:WORD_1 dst_unused:UNUSED_PRESERVE src0_sel:WORD_1
	v_pk_add_f16 v14, v30, v74 neg_lo:[0,1] neg_hi:[0,1]
	v_pk_add_f16 v13, v13, v21
	v_pk_add_f16 v12, v12, v20
	v_pk_add_f16 v11, v11, v19
	v_pk_add_f16 v10, v10, v18
	v_pk_fma_f16 v9, v61, v21, v9
	v_pk_fma_f16 v8, v60, v20, v8
	v_pk_fma_f16 v7, v59, v19, v7
	v_pk_fma_f16 v6, v58, v18, v6
	v_pk_add_f16 v15, v31, v75 neg_lo:[0,1] neg_hi:[0,1]
	v_pk_add_f16 v16, v32, v76 neg_lo:[0,1] neg_hi:[0,1]
	v_pk_add_f16 v17, v33, v77 neg_lo:[0,1] neg_hi:[0,1]
	v_exp_f16_sdwa v18, v14 dst_sel:WORD_0 dst_unused:UNUSED_PAD src0_sel:WORD_0
	v_exp_f16_sdwa v19, v15 dst_sel:WORD_0 dst_unused:UNUSED_PAD src0_sel:WORD_0
	v_exp_f16_sdwa v20, v16 dst_sel:WORD_0 dst_unused:UNUSED_PAD src0_sel:WORD_0
	v_exp_f16_sdwa v21, v17 dst_sel:WORD_0 dst_unused:UNUSED_PAD src0_sel:WORD_0
	v_exp_f16_sdwa v18, v14 dst_sel:WORD_1 dst_unused:UNUSED_PRESERVE src0_sel:WORD_1
	v_exp_f16_sdwa v19, v15 dst_sel:WORD_1 dst_unused:UNUSED_PRESERVE src0_sel:WORD_1
	v_exp_f16_sdwa v20, v16 dst_sel:WORD_1 dst_unused:UNUSED_PRESERVE src0_sel:WORD_1
	v_exp_f16_sdwa v21, v17 dst_sel:WORD_1 dst_unused:UNUSED_PRESERVE src0_sel:WORD_1
	v_pk_add_f16 v10, v10, v18
	v_pk_add_f16 v11, v11, v19
	v_pk_add_f16 v12, v12, v20
	v_pk_add_f16 v13, v13, v21
	v_pk_fma_f16 v14, v78, v18, v6
	v_pk_fma_f16 v15, v79, v19, v7
	v_pk_fma_f16 v16, v80, v20, v8
	v_pk_fma_f16 v17, v81, v21, v9
	v_pk_add_f16 v6, v46, v74 neg_lo:[0,1] neg_hi:[0,1]
	v_pk_add_f16 v7, v47, v75 neg_lo:[0,1] neg_hi:[0,1]
	v_pk_add_f16 v8, v48, v76 neg_lo:[0,1] neg_hi:[0,1]
	v_pk_add_f16 v9, v49, v77 neg_lo:[0,1] neg_hi:[0,1]
	v_exp_f16_sdwa v18, v6 dst_sel:WORD_0 dst_unused:UNUSED_PAD src0_sel:WORD_0
	v_exp_f16_sdwa v19, v7 dst_sel:WORD_0 dst_unused:UNUSED_PAD src0_sel:WORD_0
	v_exp_f16_sdwa v20, v8 dst_sel:WORD_0 dst_unused:UNUSED_PAD src0_sel:WORD_0
	v_exp_f16_sdwa v21, v9 dst_sel:WORD_0 dst_unused:UNUSED_PAD src0_sel:WORD_0
	v_exp_f16_sdwa v18, v6 dst_sel:WORD_1 dst_unused:UNUSED_PRESERVE src0_sel:WORD_1
	v_exp_f16_sdwa v19, v7 dst_sel:WORD_1 dst_unused:UNUSED_PRESERVE src0_sel:WORD_1
	v_exp_f16_sdwa v20, v8 dst_sel:WORD_1 dst_unused:UNUSED_PRESERVE src0_sel:WORD_1
	v_exp_f16_sdwa v21, v9 dst_sel:WORD_1 dst_unused:UNUSED_PRESERVE src0_sel:WORD_1
	s_nop 0
	v_pk_add_f16 v9, v13, v21
	v_pk_add_f16 v8, v12, v20
	v_pk_add_f16 v7, v11, v19
	v_pk_add_f16 v6, v10, v18
	v_pk_fma_f16 v13, v93, v21, v17
	v_pk_fma_f16 v12, v92, v20, v16
	v_pk_fma_f16 v11, v91, v19, v15
	v_pk_fma_f16 v10, v90, v18, v14
	v_pk_add_f16 v18, v50, v74 neg_lo:[0,1] neg_hi:[0,1]
	v_pk_add_f16 v19, v51, v75 neg_lo:[0,1] neg_hi:[0,1]
	v_pk_add_f16 v20, v52, v76 neg_lo:[0,1] neg_hi:[0,1]
	v_pk_add_f16 v21, v53, v77 neg_lo:[0,1] neg_hi:[0,1]
	v_exp_f16_sdwa v14, v18 dst_sel:WORD_0 dst_unused:UNUSED_PAD src0_sel:WORD_0
	v_exp_f16_sdwa v17, v19 dst_sel:WORD_0 dst_unused:UNUSED_PAD src0_sel:WORD_0
	v_exp_f16_sdwa v15, v20 dst_sel:WORD_0 dst_unused:UNUSED_PAD src0_sel:WORD_0
	v_exp_f16_sdwa v16, v21 dst_sel:WORD_0 dst_unused:UNUSED_PAD src0_sel:WORD_0
	v_exp_f16_sdwa v14, v18 dst_sel:WORD_1 dst_unused:UNUSED_PRESERVE src0_sel:WORD_1
	v_exp_f16_sdwa v17, v19 dst_sel:WORD_1 dst_unused:UNUSED_PRESERVE src0_sel:WORD_1
	v_exp_f16_sdwa v15, v20 dst_sel:WORD_1 dst_unused:UNUSED_PRESERVE src0_sel:WORD_1
	v_exp_f16_sdwa v16, v21 dst_sel:WORD_1 dst_unused:UNUSED_PRESERVE src0_sel:WORD_1
	s_nop 0

_Z7k_attn2ILi2EEv8AttnArgs:
	v_readfirstlane_b32 s94, v0
	s_nop 0
	s_lshr_b32 s94, s94, 6
	v_readfirstlane_b32 s3, v0
	s_lshl_b32 s12, s3, 1
	v_lshlrev_b32_e32 v3, 3, v0
	s_and_b32 s12, s12, 0x80
	v_and_b32_e32 v3, 0x78, v3
	s_load_dwordx4 s[8:11], s[0:1], 0x0
	s_load_dwordx2 s[4:5], s[0:1], 0x10
	s_load_dwordx2 s[6:7], s[0:1], 0x50
	v_or_b32_e32 v180, s12, v3
	s_lshl_b32 s12, s2, 5
	v_lshrrev_b32_e32 v1, 5, v0
	v_bfe_u32 v2, v0, 4, 2
	s_and_b32 s14, s12, 0xe0
	s_lshr_b32 s12, s2, 3
	v_lshrrev_b32_e32 v0, 6, v0
	v_and_b32_e32 v1, 4, v1
	s_add_i32 s14, s14, s12
	s_and_b32 s2, s2, 56
	v_and_b32_e32 v0, 4, v0
	v_and_or_b32 v181, s14, 56, v0
	v_or3_b32 v182, v2, s2, v1
	s_and_b32 s2, s14, 0x3ffffc0
	v_or_b32_e32 v4, s2, v181
	v_lshlrev_b32_e32 v0, 1, v180
	v_mov_b32_e32 v1, 0
	s_waitcnt lgkmcnt(0)
	v_lshl_add_u64 v[2:3], s[6:7], 0, v[0:1]
	v_lshl_or_b32 v0, v4, 6, v182
	v_lshlrev_b64 v[4:5], 9, v[0:1]
	v_lshl_add_u64 v[8:9], v[2:3], 0, v[4:5]
	v_or_b32_e32 v4, 64, v0
	v_mov_b32_e32 v5, v1
	v_lshlrev_b64 v[4:5], 9, v[4:5]
	v_lshlrev_b32_e32 v20, 2, v180
	v_lshl_add_u64 v[10:11], v[2:3], 0, v[4:5]
	global_load_dwordx4 v[240:243], v20, s[10:11] offset:16
	global_load_dwordx4 v[236:239], v20, s[10:11]
	global_load_dwordx4 v[248:251], v20, s[4:5] offset:16
	global_load_dwordx4 v[244:247], v20, s[4:5]
	global_load_dwordx4 v[12:15], v[8:9], off nt
	global_load_dwordx4 v[4:7], v[10:11], off nt
	v_or_b32_e32 v8, 0x80, v0
	v_mov_b32_e32 v9, v1
	v_lshlrev_b64 v[8:9], 9, v[8:9]
	v_or_b32_e32 v0, 0xc0, v0
	v_lshl_add_u64 v[20:21], v[2:3], 0, v[8:9]
	v_lshlrev_b64 v[0:1], 9, v[0:1]
	v_lshl_add_u64 v[34:35], v[2:3], 0, v[0:1]
	global_load_dwordx4 v[8:11], v[20:21], off nt
	global_load_dwordx4 v[0:3], v[34:35], off nt
	s_bitcmp1_b32 s3, 6
	s_cselect_b64 s[4:5], -1, 0
	s_and_b32 s2, s14, 0x3ffc0
	v_or_b32_e32 v20, s2, v181
	v_lshl_or_b32 v20, v20, 6, v182
	v_add_u32_e32 v184, -1, v182
	v_add_u32_e32 v185, -1, v181
	v_mul_u32_u24_e32 v20, 0x300, v20
	v_or_b32_e32 v34, v185, v184
	v_or_b32_e32 v20, v180, v20
	s_mov_b32 s11, 0x20000
	s_mov_b32 s10, 0x1800000
	s_and_b32 s9, s9, 0xffff
	v_lshlrev_b32_e32 v183, 1, v20
	v_cmp_gt_u32_e64 s[2:3], 64, v34
	s_and_b64 vcc, exec, s[4:5]
	s_cbranch_vccz .LBB6_38
	s_load_dwordx2 s[12:13], s[0:1], 0x20
	s_waitcnt lgkmcnt(0)
	s_load_dwordx2 s[4:5], s[12:13], 0x0
	s_load_dword s12, s[12:13], 0x8
	v_cmp_lt_u32_e64 s[64:65], 0, v182
	v_cmp_gt_u32_e64 s[66:67], 63, v182
	v_cmp_lt_u32_e64 s[68:69], 0, v181
	v_cmp_gt_u32_e64 s[70:71], 60, v181
	buffer_load_dwordx4 v[190:193], v183, s[8:11], 0 offen
	s_and_b64 s[72:73], s[68:69], s[64:65]
	s_and_b64 s[74:75], s[68:69], s[66:67]
	s_and_b64 s[76:77], s[70:71], s[64:65]
	s_and_b64 s[78:79], s[70:71], s[66:67]
	v_add_u32_e32 v228, 0xfffe7c00, v183
	v_add_u32_e32 v229, 0xfffe8000, v183
	s_mov_b64 exec, s[72:73]
	buffer_load_dwordx4 v[136:139], v228, s[8:11], 0 offen
	buffer_load_dwordx4 v[96:99], v228, s[8:11], 0 offen offset:512
	s_mov_b64 exec, -1
	s_mov_b64 exec, s[68:69]
	buffer_load_dwordx4 v[152:155], v229, s[8:11], 0 offen offset:512
	buffer_load_dwordx4 v[124:127], v229, s[8:11], 0 offen offset:1024
	s_mov_b64 exec, -1
	s_mov_b64 exec, s[74:75]
	buffer_load_dwordx4 v[160:163], v229, s[8:11], 0 offen offset:2048
	buffer_load_dwordx4 v[140:143], v229, s[8:11], 0 offen offset:2560
	s_mov_b64 exec, -1
	v_add_u32_e32 v228, 0xfffffc00, v183
	s_mov_b64 exec, s[64:65]
	buffer_load_dwordx4 v[112:115], v228, s[8:11], 0 offen
	buffer_load_dwordx4 v[68:71], v228, s[8:11], 0 offen offset:512
	s_mov_b64 exec, -1
	buffer_load_dwordx4 v[132:135], v183, s[8:11], 0 offen offset:512
	buffer_load_dwordx4 v[88:91], v183, s[8:11], 0 offen offset:1024
	s_mov_b64 exec, s[66:67]
	buffer_load_dwordx4 v[148:151], v183, s[8:11], 0 offen offset:2048
	buffer_load_dwordx4 v[108:111], v183, s[8:11], 0 offen offset:2560
	s_mov_b64 exec, -1
	v_add_u32_e32 v228, 0x17c00, v183
	v_add_u32_e32 v229, 0x18000, v183
	s_mov_b64 exec, s[64:65]
	buffer_load_dwordx4 v[76:79], v228, s[8:11], 0 offen
	buffer_load_dwordx4 v[48:51], v228, s[8:11], 0 offen offset:512
	s_mov_b64 exec, -1
	buffer_load_dwordx4 v[92:95], v229, s[8:11], 0 offen offset:512
	buffer_load_dwordx4 v[56:59], v229, s[8:11], 0 offen offset:1024
	s_mov_b64 exec, s[66:67]
	buffer_load_dwordx4 v[116:119], v229, s[8:11], 0 offen offset:2048
	buffer_load_dwordx4 v[72:75], v229, s[8:11], 0 offen offset:2560
	s_mov_b64 exec, -1
	v_add_u32_e32 v228, 0x18000, v183
	buffer_load_dwordx4 v[176:179], v228, s[8:11], 0 offen
	v_add_u32_e32 v229, 0x30000, v183
	buffer_load_dwordx4 v[172:175], v229, s[8:11], 0 offen
	v_add_u32_e32 v228, 0x48000, v183
	buffer_load_dwordx4 v[168:171], v228, s[8:11], 0 offen
	v_add_u32_e32 v228, 0x2fc00, v183
	v_add_u32_e32 v229, 0x30000, v183
	v_add_u32_e32 v230, 0x47c00, v183
	v_add_u32_e32 v231, 0x48000, v183
	v_add_u32_e32 v232, 0x5fc00, v183
	v_add_u32_e32 v233, 0x60000, v183
	s_waitcnt vmcnt(26)
	v_cvt_pk_f16_f32 v22, v240, v241
	v_cvt_pk_f16_f32 v20, v236, v237
	v_cvt_pk_f16_f32 v21, v238, v239
	v_cvt_pk_f16_f32 v16, v244, v245
	v_cvt_pk_f16_f32 v17, v246, v247
	v_cvt_pk_f16_f32 v18, v248, v249
	v_cvt_pk_f16_f32 v23, v242, v243
	v_cvt_pk_f16_f32 v19, v250, v251
	s_not_b64 exec, s[72:73]
	s_cbranch_execz .Lmyf_E1_0
	v_mov_b32_e32 v136, v20
	v_mov_b32_e32 v137, v21
	v_mov_b32_e32 v138, v22
	v_mov_b32_e32 v139, v23
	v_mov_b32_e32 v96, v16
	v_mov_b32_e32 v97, v17
	v_mov_b32_e32 v98, v18
	v_mov_b32_e32 v99, v19

.Lmyf_E1_7:
	s_mov_b64 exec, -1
	s_waitcnt lgkmcnt(0)
	v_cvt_f16_f32_e32 v186, s5
	v_cvt_f16_f32_e32 v188, s4
	v_cvt_f16_f32_e32 v187, s12
	s_cmp_lt_u32 s94, 4
	s_cbranch_scc1 .Lmylp6_0
	s_setprio 1
.Lmylp6_0:
	s_waitcnt vmcnt(3)
	v_pk_mul_f16 v196, v188, v193 op_sel_hi:[0,1]
	v_pk_mul_f16 v200, v186, v193 op_sel_hi:[0,1]
	v_pk_mul_f16 v204, v187, v193 op_sel_hi:[0,1]
	v_pk_mul_f16 v189, v188, v190 op_sel_hi:[0,1]
	v_pk_mul_f16 v194, v188, v191 op_sel_hi:[0,1]
	v_pk_mul_f16 v195, v188, v192 op_sel_hi:[0,1]
	v_pk_mul_f16 v197, v186, v190 op_sel_hi:[0,1]
	s_mov_b64 exec, s[64:65]
	buffer_load_dwordx4 v[44:47], v228, s[8:11], 0 offen
	buffer_load_dwordx4 v[32:35], v228, s[8:11], 0 offen offset:512
	s_mov_b64 exec, -1
	v_pk_mul_f16 v198, v186, v191 op_sel_hi:[0,1]
	v_pk_mul_f16 v199, v186, v192 op_sel_hi:[0,1]
	v_pk_mul_f16 v201, v187, v190 op_sel_hi:[0,1]
	v_pk_mul_f16 v202, v187, v191 op_sel_hi:[0,1]
	v_pk_mul_f16 v203, v187, v192 op_sel_hi:[0,1]
	v_pk_fma_f16 v139, v139, v193, v196
	v_pk_fma_f16 v155, v155, v193, v200
	v_pk_fma_f16 v163, v163, v193, v204
	v_pk_fma_f16 v205, v115, v193, v196
	v_pk_fma_f16 v209, v135, v193, v200
	v_pk_fma_f16 v213, v151, v193, v204
	v_pk_fma_f16 v196, v79, v193, v196
	v_pk_fma_f16 v200, v95, v193, v200
	buffer_load_dwordx4 v[60:63], v229, s[8:11], 0 offen offset:512
	buffer_load_dwordx4 v[36:39], v229, s[8:11], 0 offen offset:1024
	v_pk_fma_f16 v193, v119, v193, v204
	v_pk_maximum3_f16 v204, v139, v155, v163
	v_pk_fma_f16 v138, v138, v192, v195
	v_pk_fma_f16 v137, v137, v191, v194
	v_pk_fma_f16 v136, v136, v190, v189
	v_pk_fma_f16 v154, v154, v192, v199
	v_pk_fma_f16 v153, v153, v191, v198
	v_pk_fma_f16 v152, v152, v190, v197
	v_pk_fma_f16 v162, v162, v192, v203
	v_pk_fma_f16 v161, v161, v191, v202
	v_pk_fma_f16 v160, v160, v190, v201
	v_pk_fma_f16 v206, v114, v192, v195
	v_pk_fma_f16 v207, v113, v191, v194
	v_pk_fma_f16 v208, v112, v190, v189
	v_pk_fma_f16 v210, v134, v192, v199
	v_pk_fma_f16 v211, v133, v191, v198
	s_mov_b64 exec, s[66:67]
	buffer_load_dwordx4 v[80:83], v229, s[8:11], 0 offen offset:2048
	buffer_load_dwordx4 v[40:43], v229, s[8:11], 0 offen offset:2560
	s_mov_b64 exec, -1
	v_pk_fma_f16 v212, v132, v190, v197
	v_pk_fma_f16 v214, v150, v192, v203
	v_pk_fma_f16 v215, v149, v191, v202
	v_pk_fma_f16 v216, v148, v190, v201
	v_pk_fma_f16 v195, v78, v192, v195
	v_pk_fma_f16 v194, v77, v191, v194
	v_pk_fma_f16 v189, v76, v190, v189
	v_pk_fma_f16 v199, v94, v192, v199
	v_pk_fma_f16 v198, v93, v191, v198
	v_pk_fma_f16 v197, v92, v190, v197
	v_pk_fma_f16 v192, v118, v192, v203
	v_pk_fma_f16 v191, v117, v191, v202
	v_pk_fma_f16 v190, v116, v190, v201
	v_pk_maximum3_f16 v201, v136, v152, v160
	v_pk_maximum3_f16 v202, v137, v153, v161
	v_pk_maximum3_f16 v203, v138, v154, v162
	v_pk_maximum3_f16 v220, v205, v209, v213
	v_pk_maximum3_f16 v224, v196, v200, v193
	v_pk_maximum3_f16 v217, v208, v212, v216
	v_pk_maximum3_f16 v218, v207, v211, v215
	v_pk_maximum3_f16 v219, v206, v210, v214
	v_pk_maximum3_f16 v221, v189, v197, v190
	v_pk_maximum3_f16 v222, v194, v198, v191
	v_pk_maximum3_f16 v204, v204, v220, v224
	v_pk_maximum3_f16 v223, v195, v199, v192
	v_pk_maximum3_f16 v201, v201, v217, v221
	v_pk_maximum3_f16 v202, v202, v218, v222
	v_pk_maximum3_f16 v203, v203, v219, v223
	v_pk_add_f16 v139, v139, v204 neg_lo:[0,1] neg_hi:[0,1]
	s_mov_b64 exec, s[64:65]
	buffer_load_dwordx4 v[100:103], v230, s[8:11], 0 offen
	buffer_load_dwordx4 v[52:55], v230, s[8:11], 0 offen offset:512
	s_mov_b64 exec, -1
	v_pk_add_f16 v136, v136, v201 neg_lo:[0,1] neg_hi:[0,1]
	v_pk_add_f16 v137, v137, v202 neg_lo:[0,1] neg_hi:[0,1]
	v_pk_add_f16 v138, v138, v203 neg_lo:[0,1] neg_hi:[0,1]
	v_pk_add_f16 v152, v152, v201 neg_lo:[0,1] neg_hi:[0,1]
	v_exp_f16_sdwa v217, v136 dst_sel:WORD_0 dst_unused:UNUSED_PAD src0_sel:WORD_0
	v_exp_f16_sdwa v218, v137 dst_sel:WORD_0 dst_unused:UNUSED_PAD src0_sel:WORD_0
	v_exp_f16_sdwa v219, v138 dst_sel:WORD_0 dst_unused:UNUSED_PAD src0_sel:WORD_0
	v_exp_f16_sdwa v220, v139 dst_sel:WORD_0 dst_unused:UNUSED_PAD src0_sel:WORD_0
	v_exp_f16_sdwa v217, v136 dst_sel:WORD_1 dst_unused:UNUSED_PRESERVE src0_sel:WORD_1
	v_exp_f16_sdwa v218, v137 dst_sel:WORD_1 dst_unused:UNUSED_PRESERVE src0_sel:WORD_1
	v_exp_f16_sdwa v219, v138 dst_sel:WORD_1 dst_unused:UNUSED_PRESERVE src0_sel:WORD_1
	v_exp_f16_sdwa v220, v139 dst_sel:WORD_1 dst_unused:UNUSED_PRESERVE src0_sel:WORD_1
	v_pk_add_f16 v153, v153, v202 neg_lo:[0,1] neg_hi:[0,1]
	v_pk_add_f16 v139, v217, 0
	v_pk_fma_f16 v99, v99, v220, 0
	v_pk_add_f16 v136, v220, 0
	v_pk_add_f16 v137, v219, 0
	v_pk_add_f16 v138, v218, 0
	v_pk_fma_f16 v98, v98, v219, 0
	v_pk_fma_f16 v97, v97, v218, 0
	v_pk_fma_f16 v96, v96, v217, 0
	v_pk_add_f16 v154, v154, v203 neg_lo:[0,1] neg_hi:[0,1]
	buffer_load_dwordx4 v[128:131], v231, s[8:11], 0 offen offset:512
	buffer_load_dwordx4 v[64:67], v231, s[8:11], 0 offen offset:1024
	v_pk_add_f16 v155, v155, v204 neg_lo:[0,1] neg_hi:[0,1]
	v_exp_f16_sdwa v217, v152 dst_sel:WORD_0 dst_unused:UNUSED_PAD src0_sel:WORD_0
	v_exp_f16_sdwa v218, v153 dst_sel:WORD_0 dst_unused:UNUSED_PAD src0_sel:WORD_0
	v_exp_f16_sdwa v219, v154 dst_sel:WORD_0 dst_unused:UNUSED_PAD src0_sel:WORD_0
	v_exp_f16_sdwa v220, v155 dst_sel:WORD_0 dst_unused:UNUSED_PAD src0_sel:WORD_0
	v_exp_f16_sdwa v217, v152 dst_sel:WORD_1 dst_unused:UNUSED_PRESERVE src0_sel:WORD_1
	v_exp_f16_sdwa v218, v153 dst_sel:WORD_1 dst_unused:UNUSED_PRESERVE src0_sel:WORD_1
	v_exp_f16_sdwa v219, v154 dst_sel:WORD_1 dst_unused:UNUSED_PRESERVE src0_sel:WORD_1
	v_exp_f16_sdwa v220, v155 dst_sel:WORD_1 dst_unused:UNUSED_PRESERVE src0_sel:WORD_1
	v_pk_add_f16 v139, v139, v217
	v_pk_fma_f16 v99, v127, v220, v99
	v_pk_add_f16 v127, v163, v204 neg_lo:[0,1] neg_hi:[0,1]
	v_pk_add_f16 v138, v138, v218
	v_pk_add_f16 v137, v137, v219
	v_pk_add_f16 v136, v136, v220
	v_pk_fma_f16 v96, v124, v217, v96
	v_pk_fma_f16 v97, v125, v218, v97
	v_pk_fma_f16 v98, v126, v219, v98
	v_pk_add_f16 v124, v160, v201 neg_lo:[0,1] neg_hi:[0,1]
	v_pk_add_f16 v125, v161, v202 neg_lo:[0,1] neg_hi:[0,1]
	v_pk_add_f16 v126, v162, v203 neg_lo:[0,1] neg_hi:[0,1]
	v_exp_f16_sdwa v152, v124 dst_sel:WORD_0 dst_unused:UNUSED_PAD src0_sel:WORD_0
	v_exp_f16_sdwa v153, v125 dst_sel:WORD_0 dst_unused:UNUSED_PAD src0_sel:WORD_0
	v_exp_f16_sdwa v154, v126 dst_sel:WORD_0 dst_unused:UNUSED_PAD src0_sel:WORD_0
	v_exp_f16_sdwa v155, v127 dst_sel:WORD_0 dst_unused:UNUSED_PAD src0_sel:WORD_0
	v_exp_f16_sdwa v152, v124 dst_sel:WORD_1 dst_unused:UNUSED_PRESERVE src0_sel:WORD_1
	v_exp_f16_sdwa v153, v125 dst_sel:WORD_1 dst_unused:UNUSED_PRESERVE src0_sel:WORD_1
	v_exp_f16_sdwa v154, v126 dst_sel:WORD_1 dst_unused:UNUSED_PRESERVE src0_sel:WORD_1
	v_exp_f16_sdwa v155, v127 dst_sel:WORD_1 dst_unused:UNUSED_PRESERVE src0_sel:WORD_1
	v_pk_add_f16 v127, v139, v152
	v_pk_add_f16 v124, v136, v155
	s_mov_b64 exec, s[66:67]
	buffer_load_dwordx4 v[144:147], v231, s[8:11], 0 offen offset:2048
	buffer_load_dwordx4 v[84:87], v231, s[8:11], 0 offen offset:2560
	s_mov_b64 exec, -1
	v_pk_add_f16 v125, v137, v154
	v_pk_add_f16 v126, v138, v153
	v_pk_fma_f16 v99, v143, v155, v99
	v_pk_fma_f16 v98, v142, v154, v98
	v_pk_fma_f16 v97, v141, v153, v97
	v_pk_fma_f16 v96, v140, v152, v96
	v_pk_add_f16 v136, v208, v201 neg_lo:[0,1] neg_hi:[0,1]
	v_pk_add_f16 v137, v207, v202 neg_lo:[0,1] neg_hi:[0,1]
	v_pk_add_f16 v138, v206, v203 neg_lo:[0,1] neg_hi:[0,1]
	v_pk_add_f16 v139, v205, v204 neg_lo:[0,1] neg_hi:[0,1]
	v_exp_f16_sdwa v140, v136 dst_sel:WORD_0 dst_unused:UNUSED_PAD src0_sel:WORD_0
	v_exp_f16_sdwa v141, v137 dst_sel:WORD_0 dst_unused:UNUSED_PAD src0_sel:WORD_0
	v_exp_f16_sdwa v142, v138 dst_sel:WORD_0 dst_unused:UNUSED_PAD src0_sel:WORD_0
	v_exp_f16_sdwa v143, v139 dst_sel:WORD_0 dst_unused:UNUSED_PAD src0_sel:WORD_0
	v_exp_f16_sdwa v140, v136 dst_sel:WORD_1 dst_unused:UNUSED_PRESERVE src0_sel:WORD_1
	v_exp_f16_sdwa v141, v137 dst_sel:WORD_1 dst_unused:UNUSED_PRESERVE src0_sel:WORD_1
	v_exp_f16_sdwa v142, v138 dst_sel:WORD_1 dst_unused:UNUSED_PRESERVE src0_sel:WORD_1
	v_exp_f16_sdwa v143, v139 dst_sel:WORD_1 dst_unused:UNUSED_PRESERVE src0_sel:WORD_1
	v_pk_add_f16 v136, v212, v201 neg_lo:[0,1] neg_hi:[0,1]
	v_pk_add_f16 v127, v127, v140
	v_pk_add_f16 v126, v126, v141
	v_pk_add_f16 v125, v125, v142
	s_mov_b64 exec, s[76:77]
	buffer_load_dwordx4 v[156:159], v232, s[8:11], 0 offen
	buffer_load_dwordx4 v[104:107], v232, s[8:11], 0 offen offset:512
	s_mov_b64 exec, -1
	v_pk_add_f16 v124, v124, v143
	v_pk_fma_f16 v96, v68, v140, v96
	v_pk_fma_f16 v97, v69, v141, v97
	v_pk_fma_f16 v98, v70, v142, v98
	v_pk_fma_f16 v99, v71, v143, v99
	v_pk_add_f16 v137, v211, v202 neg_lo:[0,1] neg_hi:[0,1]
	v_pk_add_f16 v138, v210, v203 neg_lo:[0,1] neg_hi:[0,1]
	v_pk_add_f16 v139, v209, v204 neg_lo:[0,1] neg_hi:[0,1]
	v_exp_f16_sdwa v140, v136 dst_sel:WORD_0 dst_unused:UNUSED_PAD src0_sel:WORD_0
	v_exp_f16_sdwa v141, v137 dst_sel:WORD_0 dst_unused:UNUSED_PAD src0_sel:WORD_0
	v_exp_f16_sdwa v142, v138 dst_sel:WORD_0 dst_unused:UNUSED_PAD src0_sel:WORD_0
	v_exp_f16_sdwa v143, v139 dst_sel:WORD_0 dst_unused:UNUSED_PAD src0_sel:WORD_0
	v_exp_f16_sdwa v140, v136 dst_sel:WORD_1 dst_unused:UNUSED_PRESERVE src0_sel:WORD_1
	v_exp_f16_sdwa v141, v137 dst_sel:WORD_1 dst_unused:UNUSED_PRESERVE src0_sel:WORD_1
	v_exp_f16_sdwa v142, v138 dst_sel:WORD_1 dst_unused:UNUSED_PRESERVE src0_sel:WORD_1
	v_exp_f16_sdwa v143, v139 dst_sel:WORD_1 dst_unused:UNUSED_PRESERVE src0_sel:WORD_1
	v_pk_add_f16 v136, v216, v201 neg_lo:[0,1] neg_hi:[0,1]
	v_pk_add_f16 v127, v127, v140
	v_pk_add_f16 v124, v124, v143
	v_pk_add_f16 v125, v125, v142
	v_pk_add_f16 v126, v126, v141
	v_pk_fma_f16 v99, v91, v143, v99
	v_pk_fma_f16 v98, v90, v142, v98
	s_mov_b64 exec, s[70:71]
	buffer_load_dwordx4 v[164:167], v233, s[8:11], 0 offen offset:512
	buffer_load_dwordx4 v[120:123], v233, s[8:11], 0 offen offset:1024
	s_mov_b64 exec, -1
	v_pk_fma_f16 v97, v89, v141, v97
	v_pk_fma_f16 v96, v88, v140, v96
	v_pk_add_f16 v137, v215, v202 neg_lo:[0,1] neg_hi:[0,1]
	v_pk_add_f16 v138, v214, v203 neg_lo:[0,1] neg_hi:[0,1]
	v_pk_add_f16 v139, v213, v204 neg_lo:[0,1] neg_hi:[0,1]
	v_exp_f16_sdwa v140, v136 dst_sel:WORD_0 dst_unused:UNUSED_PAD src0_sel:WORD_0
	v_exp_f16_sdwa v141, v137 dst_sel:WORD_0 dst_unused:UNUSED_PAD src0_sel:WORD_0
	v_exp_f16_sdwa v142, v138 dst_sel:WORD_0 dst_unused:UNUSED_PAD src0_sel:WORD_0
	v_exp_f16_sdwa v143, v139 dst_sel:WORD_0 dst_unused:UNUSED_PAD src0_sel:WORD_0
	v_exp_f16_sdwa v140, v136 dst_sel:WORD_1 dst_unused:UNUSED_PRESERVE src0_sel:WORD_1
	v_exp_f16_sdwa v141, v137 dst_sel:WORD_1 dst_unused:UNUSED_PRESERVE src0_sel:WORD_1
	v_exp_f16_sdwa v142, v138 dst_sel:WORD_1 dst_unused:UNUSED_PRESERVE src0_sel:WORD_1
	v_exp_f16_sdwa v143, v139 dst_sel:WORD_1 dst_unused:UNUSED_PRESERVE src0_sel:WORD_1
	v_pk_add_f16 v136, v189, v201 neg_lo:[0,1] neg_hi:[0,1]
	v_pk_add_f16 v127, v127, v140
	v_pk_add_f16 v126, v126, v141
	v_pk_add_f16 v125, v125, v142
	v_pk_add_f16 v124, v124, v143
	v_pk_fma_f16 v96, v108, v140, v96
	v_pk_fma_f16 v97, v109, v141, v97
	v_pk_fma_f16 v98, v110, v142, v98
	v_pk_fma_f16 v99, v111, v143, v99
	s_mov_b64 exec, s[78:79]
	buffer_load_dwordx4 v[28:31], v233, s[8:11], 0 offen offset:2048
	buffer_load_dwordx4 v[24:27], v233, s[8:11], 0 offen offset:2560
	s_mov_b64 exec, -1
	v_pk_add_f16 v137, v194, v202 neg_lo:[0,1] neg_hi:[0,1]
	v_pk_add_f16 v138, v195, v203 neg_lo:[0,1] neg_hi:[0,1]
	v_pk_add_f16 v139, v196, v204 neg_lo:[0,1] neg_hi:[0,1]
	v_exp_f16_sdwa v140, v136 dst_sel:WORD_0 dst_unused:UNUSED_PAD src0_sel:WORD_0
	v_exp_f16_sdwa v141, v137 dst_sel:WORD_0 dst_unused:UNUSED_PAD src0_sel:WORD_0
	v_exp_f16_sdwa v142, v138 dst_sel:WORD_0 dst_unused:UNUSED_PAD src0_sel:WORD_0
	v_exp_f16_sdwa v143, v139 dst_sel:WORD_0 dst_unused:UNUSED_PAD src0_sel:WORD_0
	v_exp_f16_sdwa v140, v136 dst_sel:WORD_1 dst_unused:UNUSED_PRESERVE src0_sel:WORD_1
	v_exp_f16_sdwa v141, v137 dst_sel:WORD_1 dst_unused:UNUSED_PRESERVE src0_sel:WORD_1
	v_exp_f16_sdwa v142, v138 dst_sel:WORD_1 dst_unused:UNUSED_PRESERVE src0_sel:WORD_1
	v_exp_f16_sdwa v143, v139 dst_sel:WORD_1 dst_unused:UNUSED_PRESERVE src0_sel:WORD_1
	v_pk_add_f16 v136, v197, v201 neg_lo:[0,1] neg_hi:[0,1]
	v_pk_add_f16 v127, v127, v140
	v_pk_add_f16 v124, v124, v143
	v_pk_add_f16 v125, v125, v142
	v_pk_add_f16 v126, v126, v141
	v_pk_fma_f16 v99, v51, v143, v99
	v_pk_fma_f16 v98, v50, v142, v98
	v_pk_fma_f16 v97, v49, v141, v97
	v_pk_fma_f16 v96, v48, v140, v96
	v_pk_add_f16 v137, v198, v202 neg_lo:[0,1] neg_hi:[0,1]
	v_pk_add_f16 v138, v199, v203 neg_lo:[0,1] neg_hi:[0,1]
	v_pk_add_f16 v139, v200, v204 neg_lo:[0,1] neg_hi:[0,1]
	v_exp_f16_sdwa v140, v136 dst_sel:WORD_0 dst_unused:UNUSED_PAD src0_sel:WORD_0
	v_exp_f16_sdwa v141, v137 dst_sel:WORD_0 dst_unused:UNUSED_PAD src0_sel:WORD_0
	v_exp_f16_sdwa v142, v138 dst_sel:WORD_0 dst_unused:UNUSED_PAD src0_sel:WORD_0
	v_exp_f16_sdwa v143, v139 dst_sel:WORD_0 dst_unused:UNUSED_PAD src0_sel:WORD_0
	v_exp_f16_sdwa v140, v136 dst_sel:WORD_1 dst_unused:UNUSED_PRESERVE src0_sel:WORD_1
	v_exp_f16_sdwa v141, v137 dst_sel:WORD_1 dst_unused:UNUSED_PRESERVE src0_sel:WORD_1
	v_exp_f16_sdwa v142, v138 dst_sel:WORD_1 dst_unused:UNUSED_PRESERVE src0_sel:WORD_1
	v_exp_f16_sdwa v143, v139 dst_sel:WORD_1 dst_unused:UNUSED_PRESERVE src0_sel:WORD_1
	v_pk_add_f16 v136, v190, v201 neg_lo:[0,1] neg_hi:[0,1]
	v_pk_add_f16 v127, v127, v140
	v_pk_add_f16 v126, v126, v141
	v_pk_add_f16 v125, v125, v142
	v_pk_add_f16 v124, v124, v143
	v_pk_fma_f16 v96, v56, v140, v96
	v_pk_fma_f16 v97, v57, v141, v97
	v_pk_fma_f16 v98, v58, v142, v98
	v_pk_fma_f16 v99, v59, v143, v99
	v_pk_add_f16 v137, v191, v202 neg_lo:[0,1] neg_hi:[0,1]
	v_pk_add_f16 v138, v192, v203 neg_lo:[0,1] neg_hi:[0,1]
	v_pk_add_f16 v139, v193, v204 neg_lo:[0,1] neg_hi:[0,1]
	v_exp_f16_sdwa v140, v136 dst_sel:WORD_0 dst_unused:UNUSED_PAD src0_sel:WORD_0
	v_exp_f16_sdwa v141, v137 dst_sel:WORD_0 dst_unused:UNUSED_PAD src0_sel:WORD_0
	v_exp_f16_sdwa v142, v138 dst_sel:WORD_0 dst_unused:UNUSED_PAD src0_sel:WORD_0
	v_exp_f16_sdwa v143, v139 dst_sel:WORD_0 dst_unused:UNUSED_PAD src0_sel:WORD_0
	v_exp_f16_sdwa v140, v136 dst_sel:WORD_1 dst_unused:UNUSED_PRESERVE src0_sel:WORD_1
	v_exp_f16_sdwa v141, v137 dst_sel:WORD_1 dst_unused:UNUSED_PRESERVE src0_sel:WORD_1
	v_exp_f16_sdwa v142, v138 dst_sel:WORD_1 dst_unused:UNUSED_PRESERVE src0_sel:WORD_1
	v_exp_f16_sdwa v143, v139 dst_sel:WORD_1 dst_unused:UNUSED_PRESERVE src0_sel:WORD_1
	v_pk_add_f16 v127, v127, v140
	v_pk_add_f16 v126, v126, v141
	v_rcp_f16_e32 v136, v127
	v_rcp_f16_sdwa v127, v127 dst_sel:DWORD dst_unused:UNUSED_PAD src0_sel:WORD_1
	v_pk_add_f16 v125, v125, v142
	v_rcp_f16_e32 v137, v126
	v_rcp_f16_sdwa v126, v126 dst_sel:DWORD dst_unused:UNUSED_PAD src0_sel:WORD_1
	v_pk_add_f16 v124, v124, v143
	v_rcp_f16_e32 v138, v125
	v_rcp_f16_sdwa v139, v125 dst_sel:DWORD dst_unused:UNUSED_PAD src0_sel:WORD_1
	v_pk_fma_f16 v97, v73, v141, v97
	v_pk_fma_f16 v96, v72, v140, v96
	v_rcp_f16_e32 v140, v124
	v_rcp_f16_sdwa v141, v124 dst_sel:DWORD dst_unused:UNUSED_PAD src0_sel:WORD_1
	v_pack_b32_f16 v124, v136, v127
	v_pk_mul_f16 v124, v96, v124
	v_pack_b32_f16 v96, v137, v126
	v_pk_fma_f16 v98, v74, v142, v98
	v_pk_mul_f16 v125, v97, v96
	v_pack_b32_f16 v96, v138, v139
	v_pk_fma_f16 v99, v75, v143, v99
	v_pk_mul_f16 v126, v98, v96
	v_pack_b32_f16 v96, v140, v141
	v_pk_mul_f16 v127, v99, v96
	s_waitcnt vmcnt(12)
	v_pk_mul_f16 v99, v188, v179 op_sel_hi:[0,1]
	v_pk_mul_f16 v139, v186, v179 op_sel_hi:[0,1]
	v_pk_mul_f16 v143, v187, v179 op_sel_hi:[0,1]
	v_pk_mul_f16 v96, v188, v176 op_sel_hi:[0,1]
	v_pk_mul_f16 v97, v188, v177 op_sel_hi:[0,1]
	v_pk_mul_f16 v98, v188, v178 op_sel_hi:[0,1]
	v_pk_mul_f16 v136, v186, v176 op_sel_hi:[0,1]
	v_pk_mul_f16 v137, v186, v177 op_sel_hi:[0,1]
	v_pk_mul_f16 v138, v186, v178 op_sel_hi:[0,1]
	v_pk_mul_f16 v140, v187, v176 op_sel_hi:[0,1]
	v_pk_mul_f16 v141, v187, v177 op_sel_hi:[0,1]
	v_pk_mul_f16 v142, v187, v178 op_sel_hi:[0,1]
	v_pk_fma_f16 v115, v115, v179, v99
	v_pk_fma_f16 v135, v135, v179, v139
	v_pk_fma_f16 v151, v151, v179, v143
	v_pk_fma_f16 v152, v79, v179, v99
	v_pk_fma_f16 v160, v95, v179, v139
	v_pk_fma_f16 v189, v119, v179, v143
	v_pk_fma_f16 v99, v47, v179, v99
	v_pk_fma_f16 v139, v63, v179, v139
	v_pk_fma_f16 v143, v83, v179, v143
	v_pk_maximum3_f16 v179, v115, v135, v151
	v_pk_fma_f16 v114, v114, v178, v98
	v_pk_fma_f16 v113, v113, v177, v97
	v_pk_fma_f16 v112, v112, v176, v96
	v_pk_fma_f16 v134, v134, v178, v138
	v_pk_fma_f16 v133, v133, v177, v137
	v_pk_fma_f16 v132, v132, v176, v136
	v_pk_fma_f16 v150, v150, v178, v142
	v_pk_fma_f16 v149, v149, v177, v141
	v_pk_fma_f16 v148, v148, v176, v140
	v_pk_fma_f16 v153, v78, v178, v98
	v_pk_fma_f16 v154, v77, v177, v97
	v_pk_fma_f16 v155, v76, v176, v96
	v_pk_fma_f16 v161, v94, v178, v138
	v_pk_fma_f16 v162, v93, v177, v137
	v_pk_fma_f16 v163, v92, v176, v136
	v_pk_fma_f16 v190, v118, v178, v142
	v_pk_fma_f16 v191, v117, v177, v141
	v_pk_fma_f16 v192, v116, v176, v140
	v_pk_fma_f16 v98, v46, v178, v98
	v_pk_fma_f16 v97, v45, v177, v97
	v_pk_fma_f16 v96, v44, v176, v96
	v_pk_fma_f16 v138, v62, v178, v138
	v_pk_fma_f16 v137, v61, v177, v137
	v_pk_fma_f16 v136, v60, v176, v136
	v_pk_fma_f16 v142, v82, v178, v142
	v_pk_fma_f16 v141, v81, v177, v141
	v_pk_fma_f16 v140, v80, v176, v140
	v_pk_maximum3_f16 v176, v112, v132, v148
	v_pk_maximum3_f16 v177, v113, v133, v149
	v_pk_maximum3_f16 v178, v114, v134, v150
	v_pk_maximum3_f16 v196, v152, v160, v189
	v_pk_maximum3_f16 v200, v99, v139, v143
	v_pk_maximum3_f16 v193, v155, v163, v192
	v_pk_maximum3_f16 v194, v154, v162, v191
	v_pk_maximum3_f16 v195, v153, v161, v190
	v_pk_maximum3_f16 v197, v96, v136, v140
	v_pk_maximum3_f16 v198, v97, v137, v141
	v_pk_maximum3_f16 v179, v179, v196, v200
	v_pk_maximum3_f16 v199, v98, v138, v142
	v_pk_maximum3_f16 v176, v176, v193, v197
	v_pk_maximum3_f16 v177, v177, v194, v198
	v_pk_maximum3_f16 v178, v178, v195, v199
	v_pk_add_f16 v115, v115, v179 neg_lo:[0,1] neg_hi:[0,1]
	v_pk_add_f16 v112, v112, v176 neg_lo:[0,1] neg_hi:[0,1]
	v_pk_add_f16 v113, v113, v177 neg_lo:[0,1] neg_hi:[0,1]
	v_pk_add_f16 v114, v114, v178 neg_lo:[0,1] neg_hi:[0,1]
	v_pk_add_f16 v132, v132, v176 neg_lo:[0,1] neg_hi:[0,1]
	v_exp_f16_sdwa v193, v112 dst_sel:WORD_0 dst_unused:UNUSED_PAD src0_sel:WORD_0
	v_exp_f16_sdwa v194, v113 dst_sel:WORD_0 dst_unused:UNUSED_PAD src0_sel:WORD_0
	v_exp_f16_sdwa v195, v114 dst_sel:WORD_0 dst_unused:UNUSED_PAD src0_sel:WORD_0
	v_exp_f16_sdwa v196, v115 dst_sel:WORD_0 dst_unused:UNUSED_PAD src0_sel:WORD_0
	v_exp_f16_sdwa v193, v112 dst_sel:WORD_1 dst_unused:UNUSED_PRESERVE src0_sel:WORD_1
	v_exp_f16_sdwa v194, v113 dst_sel:WORD_1 dst_unused:UNUSED_PRESERVE src0_sel:WORD_1
	v_exp_f16_sdwa v195, v114 dst_sel:WORD_1 dst_unused:UNUSED_PRESERVE src0_sel:WORD_1
	v_exp_f16_sdwa v196, v115 dst_sel:WORD_1 dst_unused:UNUSED_PRESERVE src0_sel:WORD_1
	v_pk_add_f16 v133, v133, v177 neg_lo:[0,1] neg_hi:[0,1]
	v_pk_add_f16 v115, v193, 0
	v_pk_fma_f16 v71, v71, v196, 0
	v_pk_add_f16 v112, v196, 0
	v_pk_add_f16 v113, v195, 0
	v_pk_add_f16 v114, v194, 0
	v_pk_fma_f16 v70, v70, v195, 0
	v_pk_fma_f16 v69, v69, v194, 0
	v_pk_fma_f16 v68, v68, v193, 0
	v_pk_add_f16 v134, v134, v178 neg_lo:[0,1] neg_hi:[0,1]
	v_pk_add_f16 v135, v135, v179 neg_lo:[0,1] neg_hi:[0,1]
	v_pk_add_f16 v96, v96, v176 neg_lo:[0,1] neg_hi:[0,1]
	v_exp_f16_sdwa v193, v132 dst_sel:WORD_0 dst_unused:UNUSED_PAD src0_sel:WORD_0
	v_exp_f16_sdwa v194, v133 dst_sel:WORD_0 dst_unused:UNUSED_PAD src0_sel:WORD_0
	v_exp_f16_sdwa v195, v134 dst_sel:WORD_0 dst_unused:UNUSED_PAD src0_sel:WORD_0
	v_exp_f16_sdwa v196, v135 dst_sel:WORD_0 dst_unused:UNUSED_PAD src0_sel:WORD_0
	v_exp_f16_sdwa v193, v132 dst_sel:WORD_1 dst_unused:UNUSED_PRESERVE src0_sel:WORD_1
	v_exp_f16_sdwa v194, v133 dst_sel:WORD_1 dst_unused:UNUSED_PRESERVE src0_sel:WORD_1
	v_exp_f16_sdwa v195, v134 dst_sel:WORD_1 dst_unused:UNUSED_PRESERVE src0_sel:WORD_1
	v_exp_f16_sdwa v196, v135 dst_sel:WORD_1 dst_unused:UNUSED_PRESERVE src0_sel:WORD_1
	v_pk_add_f16 v97, v97, v177 neg_lo:[0,1] neg_hi:[0,1]
	v_pk_add_f16 v115, v115, v193
	v_pk_fma_f16 v71, v91, v196, v71
	v_pk_add_f16 v91, v151, v179 neg_lo:[0,1] neg_hi:[0,1]
	v_pk_add_f16 v114, v114, v194
	v_pk_add_f16 v113, v113, v195
	v_pk_add_f16 v112, v112, v196
	v_pk_fma_f16 v68, v88, v193, v68
	v_pk_fma_f16 v69, v89, v194, v69
	v_pk_fma_f16 v70, v90, v195, v70
	v_pk_add_f16 v88, v148, v176 neg_lo:[0,1] neg_hi:[0,1]
	v_pk_add_f16 v89, v149, v177 neg_lo:[0,1] neg_hi:[0,1]
	v_pk_add_f16 v90, v150, v178 neg_lo:[0,1] neg_hi:[0,1]
	v_pk_add_f16 v98, v98, v178 neg_lo:[0,1] neg_hi:[0,1]
	v_exp_f16_sdwa v132, v88 dst_sel:WORD_0 dst_unused:UNUSED_PAD src0_sel:WORD_0
	v_exp_f16_sdwa v133, v89 dst_sel:WORD_0 dst_unused:UNUSED_PAD src0_sel:WORD_0
	v_exp_f16_sdwa v134, v90 dst_sel:WORD_0 dst_unused:UNUSED_PAD src0_sel:WORD_0
	v_exp_f16_sdwa v135, v91 dst_sel:WORD_0 dst_unused:UNUSED_PAD src0_sel:WORD_0
	v_exp_f16_sdwa v132, v88 dst_sel:WORD_1 dst_unused:UNUSED_PRESERVE src0_sel:WORD_1
	v_exp_f16_sdwa v133, v89 dst_sel:WORD_1 dst_unused:UNUSED_PRESERVE src0_sel:WORD_1
	v_exp_f16_sdwa v134, v90 dst_sel:WORD_1 dst_unused:UNUSED_PRESERVE src0_sel:WORD_1
	v_exp_f16_sdwa v135, v91 dst_sel:WORD_1 dst_unused:UNUSED_PRESERVE src0_sel:WORD_1
	v_pk_add_f16 v99, v99, v179 neg_lo:[0,1] neg_hi:[0,1]
	v_pk_add_f16 v91, v115, v132
	v_pk_add_f16 v88, v112, v135
	v_pk_add_f16 v89, v113, v134
	v_pk_add_f16 v90, v114, v133
	v_pk_fma_f16 v71, v111, v135, v71
	v_pk_fma_f16 v70, v110, v134, v70
	v_pk_fma_f16 v69, v109, v133, v69
	v_pk_fma_f16 v68, v108, v132, v68
	v_pk_add_f16 v108, v155, v176 neg_lo:[0,1] neg_hi:[0,1]
	v_pk_add_f16 v109, v154, v177 neg_lo:[0,1] neg_hi:[0,1]
	v_pk_add_f16 v110, v153, v178 neg_lo:[0,1] neg_hi:[0,1]
	v_pk_add_f16 v111, v152, v179 neg_lo:[0,1] neg_hi:[0,1]
	v_exp_f16_sdwa v112, v108 dst_sel:WORD_0 dst_unused:UNUSED_PAD src0_sel:WORD_0
	v_exp_f16_sdwa v113, v109 dst_sel:WORD_0 dst_unused:UNUSED_PAD src0_sel:WORD_0
	v_exp_f16_sdwa v114, v110 dst_sel:WORD_0 dst_unused:UNUSED_PAD src0_sel:WORD_0
	v_exp_f16_sdwa v115, v111 dst_sel:WORD_0 dst_unused:UNUSED_PAD src0_sel:WORD_0
	v_exp_f16_sdwa v112, v108 dst_sel:WORD_1 dst_unused:UNUSED_PRESERVE src0_sel:WORD_1
	v_exp_f16_sdwa v113, v109 dst_sel:WORD_1 dst_unused:UNUSED_PRESERVE src0_sel:WORD_1
	v_exp_f16_sdwa v114, v110 dst_sel:WORD_1 dst_unused:UNUSED_PRESERVE src0_sel:WORD_1
	v_exp_f16_sdwa v115, v111 dst_sel:WORD_1 dst_unused:UNUSED_PRESERVE src0_sel:WORD_1
	v_pk_add_f16 v108, v163, v176 neg_lo:[0,1] neg_hi:[0,1]
	v_pk_add_f16 v91, v91, v112
	v_pk_add_f16 v90, v90, v113
	v_pk_add_f16 v89, v89, v114
	v_pk_add_f16 v88, v88, v115
	v_pk_fma_f16 v68, v48, v112, v68
	v_pk_fma_f16 v69, v49, v113, v69
	v_pk_fma_f16 v70, v50, v114, v70
	v_pk_fma_f16 v71, v51, v115, v71
	v_pk_add_f16 v109, v162, v177 neg_lo:[0,1] neg_hi:[0,1]
	v_pk_add_f16 v110, v161, v178 neg_lo:[0,1] neg_hi:[0,1]
	v_pk_add_f16 v111, v160, v179 neg_lo:[0,1] neg_hi:[0,1]
	v_exp_f16_sdwa v112, v108 dst_sel:WORD_0 dst_unused:UNUSED_PAD src0_sel:WORD_0
	v_exp_f16_sdwa v113, v109 dst_sel:WORD_0 dst_unused:UNUSED_PAD src0_sel:WORD_0
	v_exp_f16_sdwa v114, v110 dst_sel:WORD_0 dst_unused:UNUSED_PAD src0_sel:WORD_0
	v_exp_f16_sdwa v115, v111 dst_sel:WORD_0 dst_unused:UNUSED_PAD src0_sel:WORD_0
	v_exp_f16_sdwa v112, v108 dst_sel:WORD_1 dst_unused:UNUSED_PRESERVE src0_sel:WORD_1
	v_exp_f16_sdwa v113, v109 dst_sel:WORD_1 dst_unused:UNUSED_PRESERVE src0_sel:WORD_1
	v_exp_f16_sdwa v114, v110 dst_sel:WORD_1 dst_unused:UNUSED_PRESERVE src0_sel:WORD_1
	v_exp_f16_sdwa v115, v111 dst_sel:WORD_1 dst_unused:UNUSED_PRESERVE src0_sel:WORD_1
	v_pk_add_f16 v108, v192, v176 neg_lo:[0,1] neg_hi:[0,1]
	v_pk_add_f16 v91, v91, v112
	v_pk_add_f16 v88, v88, v115
	v_pk_add_f16 v89, v89, v114
	v_pk_add_f16 v90, v90, v113
	v_pk_fma_f16 v71, v59, v115, v71
	v_pk_fma_f16 v70, v58, v114, v70
	v_pk_fma_f16 v69, v57, v113, v69
	v_pk_fma_f16 v68, v56, v112, v68
	v_pk_add_f16 v109, v191, v177 neg_lo:[0,1] neg_hi:[0,1]
	v_pk_add_f16 v110, v190, v178 neg_lo:[0,1] neg_hi:[0,1]
	v_pk_add_f16 v111, v189, v179 neg_lo:[0,1] neg_hi:[0,1]
	v_exp_f16_sdwa v112, v108 dst_sel:WORD_0 dst_unused:UNUSED_PAD src0_sel:WORD_0
	v_exp_f16_sdwa v113, v109 dst_sel:WORD_0 dst_unused:UNUSED_PAD src0_sel:WORD_0
	v_exp_f16_sdwa v114, v110 dst_sel:WORD_0 dst_unused:UNUSED_PAD src0_sel:WORD_0
	v_exp_f16_sdwa v115, v111 dst_sel:WORD_0 dst_unused:UNUSED_PAD src0_sel:WORD_0
	v_exp_f16_sdwa v112, v108 dst_sel:WORD_1 dst_unused:UNUSED_PRESERVE src0_sel:WORD_1
	v_exp_f16_sdwa v113, v109 dst_sel:WORD_1 dst_unused:UNUSED_PRESERVE src0_sel:WORD_1
	v_exp_f16_sdwa v114, v110 dst_sel:WORD_1 dst_unused:UNUSED_PRESERVE src0_sel:WORD_1
	v_exp_f16_sdwa v115, v111 dst_sel:WORD_1 dst_unused:UNUSED_PRESERVE src0_sel:WORD_1
	v_exp_f16_sdwa v108, v96 dst_sel:WORD_0 dst_unused:UNUSED_PAD src0_sel:WORD_0
	v_exp_f16_sdwa v109, v97 dst_sel:WORD_0 dst_unused:UNUSED_PAD src0_sel:WORD_0
	v_exp_f16_sdwa v110, v98 dst_sel:WORD_0 dst_unused:UNUSED_PAD src0_sel:WORD_0
	v_exp_f16_sdwa v111, v99 dst_sel:WORD_0 dst_unused:UNUSED_PAD src0_sel:WORD_0
	v_exp_f16_sdwa v108, v96 dst_sel:WORD_1 dst_unused:UNUSED_PRESERVE src0_sel:WORD_1
	v_exp_f16_sdwa v109, v97 dst_sel:WORD_1 dst_unused:UNUSED_PRESERVE src0_sel:WORD_1
	v_exp_f16_sdwa v110, v98 dst_sel:WORD_1 dst_unused:UNUSED_PRESERVE src0_sel:WORD_1
	v_exp_f16_sdwa v111, v99 dst_sel:WORD_1 dst_unused:UNUSED_PRESERVE src0_sel:WORD_1
	v_pk_add_f16 v96, v136, v176 neg_lo:[0,1] neg_hi:[0,1]
	v_pk_add_f16 v91, v91, v112
	v_pk_add_f16 v90, v90, v113
	v_pk_add_f16 v89, v89, v114
	v_pk_add_f16 v88, v88, v115
	v_pk_fma_f16 v68, v72, v112, v68
	v_pk_fma_f16 v69, v73, v113, v69
	v_pk_fma_f16 v70, v74, v114, v70
	v_pk_fma_f16 v71, v75, v115, v71
	v_pk_add_f16 v91, v91, v108
	v_pk_add_f16 v88, v88, v111
	v_pk_add_f16 v89, v89, v110
	v_pk_add_f16 v90, v90, v109
	v_pk_fma_f16 v71, v35, v111, v71
	v_pk_fma_f16 v70, v34, v110, v70
	v_pk_fma_f16 v69, v33, v109, v69
	v_pk_fma_f16 v68, v32, v108, v68
	v_pk_add_f16 v97, v137, v177 neg_lo:[0,1] neg_hi:[0,1]
	v_pk_add_f16 v98, v138, v178 neg_lo:[0,1] neg_hi:[0,1]
	v_pk_add_f16 v99, v139, v179 neg_lo:[0,1] neg_hi:[0,1]
	v_exp_f16_sdwa v108, v96 dst_sel:WORD_0 dst_unused:UNUSED_PAD src0_sel:WORD_0
	v_exp_f16_sdwa v109, v97 dst_sel:WORD_0 dst_unused:UNUSED_PAD src0_sel:WORD_0
	v_exp_f16_sdwa v110, v98 dst_sel:WORD_0 dst_unused:UNUSED_PAD src0_sel:WORD_0
	v_exp_f16_sdwa v111, v99 dst_sel:WORD_0 dst_unused:UNUSED_PAD src0_sel:WORD_0
	v_exp_f16_sdwa v108, v96 dst_sel:WORD_1 dst_unused:UNUSED_PRESERVE src0_sel:WORD_1
	v_exp_f16_sdwa v109, v97 dst_sel:WORD_1 dst_unused:UNUSED_PRESERVE src0_sel:WORD_1
	v_exp_f16_sdwa v110, v98 dst_sel:WORD_1 dst_unused:UNUSED_PRESERVE src0_sel:WORD_1
	v_exp_f16_sdwa v111, v99 dst_sel:WORD_1 dst_unused:UNUSED_PRESERVE src0_sel:WORD_1
	v_pk_add_f16 v96, v140, v176 neg_lo:[0,1] neg_hi:[0,1]
	v_pk_add_f16 v91, v91, v108
	v_pk_add_f16 v90, v90, v109
	v_pk_add_f16 v89, v89, v110
	v_pk_add_f16 v88, v88, v111
	v_pk_fma_f16 v68, v36, v108, v68
	v_pk_fma_f16 v69, v37, v109, v69
	v_pk_fma_f16 v70, v38, v110, v70
	v_pk_fma_f16 v71, v39, v111, v71
	v_pk_add_f16 v97, v141, v177 neg_lo:[0,1] neg_hi:[0,1]
	v_pk_add_f16 v98, v142, v178 neg_lo:[0,1] neg_hi:[0,1]
	v_pk_add_f16 v99, v143, v179 neg_lo:[0,1] neg_hi:[0,1]
	v_exp_f16_sdwa v108, v96 dst_sel:WORD_0 dst_unused:UNUSED_PAD src0_sel:WORD_0
	v_exp_f16_sdwa v109, v97 dst_sel:WORD_0 dst_unused:UNUSED_PAD src0_sel:WORD_0
	v_exp_f16_sdwa v110, v98 dst_sel:WORD_0 dst_unused:UNUSED_PAD src0_sel:WORD_0
	v_exp_f16_sdwa v111, v99 dst_sel:WORD_0 dst_unused:UNUSED_PAD src0_sel:WORD_0
	v_exp_f16_sdwa v108, v96 dst_sel:WORD_1 dst_unused:UNUSED_PRESERVE src0_sel:WORD_1
	v_exp_f16_sdwa v109, v97 dst_sel:WORD_1 dst_unused:UNUSED_PRESERVE src0_sel:WORD_1
	v_exp_f16_sdwa v110, v98 dst_sel:WORD_1 dst_unused:UNUSED_PRESERVE src0_sel:WORD_1
	v_exp_f16_sdwa v111, v99 dst_sel:WORD_1 dst_unused:UNUSED_PRESERVE src0_sel:WORD_1
	v_pk_add_f16 v91, v91, v108
	v_pk_add_f16 v90, v90, v109
	v_rcp_f16_e32 v96, v91
	v_rcp_f16_sdwa v91, v91 dst_sel:DWORD dst_unused:UNUSED_PAD src0_sel:WORD_1
	v_pk_add_f16 v89, v89, v110
	v_rcp_f16_e32 v97, v90
	v_rcp_f16_sdwa v90, v90 dst_sel:DWORD dst_unused:UNUSED_PAD src0_sel:WORD_1
	v_pk_add_f16 v88, v88, v111
	v_rcp_f16_e32 v98, v89
	v_rcp_f16_sdwa v99, v89 dst_sel:DWORD dst_unused:UNUSED_PAD src0_sel:WORD_1
	v_pk_fma_f16 v69, v41, v109, v69
	v_pk_fma_f16 v68, v40, v108, v68
	v_rcp_f16_e32 v108, v88
	v_rcp_f16_sdwa v109, v88 dst_sel:DWORD dst_unused:UNUSED_PAD src0_sel:WORD_1
	v_pack_b32_f16 v88, v96, v91
	v_pk_mul_f16 v88, v68, v88
	v_pack_b32_f16 v68, v97, v90
	v_pk_fma_f16 v70, v42, v110, v70
	v_pk_mul_f16 v89, v69, v68
	v_pack_b32_f16 v68, v98, v99
	v_pk_fma_f16 v71, v43, v111, v71
	v_pk_mul_f16 v90, v70, v68
	v_pack_b32_f16 v68, v108, v109
	v_pk_mul_f16 v91, v71, v68
	s_waitcnt vmcnt(6)
	v_pk_mul_f16 v68, v188, v172 op_sel_hi:[0,1]
	v_pk_mul_f16 v96, v186, v172 op_sel_hi:[0,1]
	v_pk_mul_f16 v108, v187, v172 op_sel_hi:[0,1]
	v_pk_mul_f16 v69, v188, v173 op_sel_hi:[0,1]
	v_pk_mul_f16 v70, v188, v174 op_sel_hi:[0,1]
	v_pk_mul_f16 v71, v188, v175 op_sel_hi:[0,1]
	v_pk_mul_f16 v97, v186, v173 op_sel_hi:[0,1]
	v_pk_mul_f16 v98, v186, v174 op_sel_hi:[0,1]
	v_pk_mul_f16 v99, v186, v175 op_sel_hi:[0,1]
	v_pk_mul_f16 v109, v187, v173 op_sel_hi:[0,1]
	v_pk_mul_f16 v110, v187, v174 op_sel_hi:[0,1]
	v_pk_mul_f16 v111, v187, v175 op_sel_hi:[0,1]
	v_pk_fma_f16 v76, v76, v172, v68
	v_pk_fma_f16 v92, v92, v172, v96
	v_pk_fma_f16 v115, v116, v172, v108
	v_pk_fma_f16 v79, v79, v175, v71
	v_pk_maximum3_f16 v140, v76, v92, v115
	v_pk_fma_f16 v78, v78, v174, v70
	v_pk_fma_f16 v77, v77, v173, v69
	v_pk_fma_f16 v95, v95, v175, v99
	v_pk_fma_f16 v94, v94, v174, v98
	v_pk_fma_f16 v93, v93, v173, v97
	v_pk_fma_f16 v112, v119, v175, v111
	v_pk_fma_f16 v113, v118, v174, v110
	v_pk_fma_f16 v114, v117, v173, v109
	v_pk_fma_f16 v119, v44, v172, v68
	v_pk_fma_f16 v135, v60, v172, v96
	v_pk_fma_f16 v139, v80, v172, v108
	v_pk_fma_f16 v68, v100, v172, v68
	v_pk_fma_f16 v96, v128, v172, v96
	v_pk_fma_f16 v108, v144, v172, v108
	v_pk_maximum3_f16 v141, v77, v93, v114
	v_pk_maximum3_f16 v142, v78, v94, v113
	v_pk_maximum3_f16 v143, v79, v95, v112
	v_pk_maximum3_f16 v148, v119, v135, v139
	v_pk_fma_f16 v116, v47, v175, v71
	v_pk_maximum3_f16 v152, v68, v96, v108
	v_pk_fma_f16 v117, v46, v174, v70
	v_pk_maximum3_f16 v140, v140, v148, v152
	v_pk_fma_f16 v118, v45, v173, v69
	v_pk_fma_f16 v132, v63, v175, v99
	v_pk_fma_f16 v133, v62, v174, v98
	v_pk_fma_f16 v134, v61, v173, v97
	v_pk_fma_f16 v136, v83, v175, v111
	v_pk_fma_f16 v137, v82, v174, v110
	v_pk_fma_f16 v138, v81, v173, v109
	v_pk_fma_f16 v71, v103, v175, v71
	v_pk_fma_f16 v70, v102, v174, v70
	v_pk_fma_f16 v69, v101, v173, v69
	v_pk_fma_f16 v99, v131, v175, v99
	v_pk_fma_f16 v98, v130, v174, v98
	v_pk_fma_f16 v97, v129, v173, v97
	v_pk_fma_f16 v111, v147, v175, v111
	v_pk_fma_f16 v110, v146, v174, v110
	v_pk_fma_f16 v109, v145, v173, v109
	v_pk_maximum3_f16 v149, v118, v134, v138
	v_pk_maximum3_f16 v150, v117, v133, v137
	v_pk_maximum3_f16 v151, v116, v132, v136
	v_pk_maximum3_f16 v154, v70, v98, v110
	v_pk_maximum3_f16 v155, v71, v99, v111
	v_pk_maximum3_f16 v153, v69, v97, v109
	v_pk_maximum3_f16 v141, v141, v149, v153
	v_pk_maximum3_f16 v142, v142, v150, v154
	v_pk_maximum3_f16 v143, v143, v151, v155
	v_pk_add_f16 v76, v76, v140 neg_lo:[0,1] neg_hi:[0,1]
	v_pk_add_f16 v77, v77, v141 neg_lo:[0,1] neg_hi:[0,1]
	v_pk_add_f16 v78, v78, v142 neg_lo:[0,1] neg_hi:[0,1]
	v_pk_add_f16 v79, v79, v143 neg_lo:[0,1] neg_hi:[0,1]
	v_pk_add_f16 v92, v92, v140 neg_lo:[0,1] neg_hi:[0,1]
	v_exp_f16_sdwa v148, v76 dst_sel:WORD_0 dst_unused:UNUSED_PAD src0_sel:WORD_0
	v_exp_f16_sdwa v149, v77 dst_sel:WORD_0 dst_unused:UNUSED_PAD src0_sel:WORD_0
	v_exp_f16_sdwa v150, v78 dst_sel:WORD_0 dst_unused:UNUSED_PAD src0_sel:WORD_0
	v_exp_f16_sdwa v151, v79 dst_sel:WORD_0 dst_unused:UNUSED_PAD src0_sel:WORD_0
	v_exp_f16_sdwa v148, v76 dst_sel:WORD_1 dst_unused:UNUSED_PRESERVE src0_sel:WORD_1
	v_exp_f16_sdwa v149, v77 dst_sel:WORD_1 dst_unused:UNUSED_PRESERVE src0_sel:WORD_1
	v_exp_f16_sdwa v150, v78 dst_sel:WORD_1 dst_unused:UNUSED_PRESERVE src0_sel:WORD_1
	v_exp_f16_sdwa v151, v79 dst_sel:WORD_1 dst_unused:UNUSED_PRESERVE src0_sel:WORD_1
	v_pk_add_f16 v93, v93, v141 neg_lo:[0,1] neg_hi:[0,1]
	v_pk_add_f16 v76, v151, 0
	v_pk_fma_f16 v48, v48, v148, 0
	v_pk_add_f16 v77, v150, 0
	v_pk_add_f16 v78, v149, 0
	v_pk_add_f16 v79, v148, 0
	v_pk_fma_f16 v49, v49, v149, 0
	v_pk_fma_f16 v50, v50, v150, 0
	v_pk_fma_f16 v51, v51, v151, 0
	v_pk_add_f16 v94, v94, v142 neg_lo:[0,1] neg_hi:[0,1]
	v_pk_add_f16 v95, v95, v143 neg_lo:[0,1] neg_hi:[0,1]
	v_pk_add_f16 v68, v68, v140 neg_lo:[0,1] neg_hi:[0,1]
	v_exp_f16_sdwa v148, v92 dst_sel:WORD_0 dst_unused:UNUSED_PAD src0_sel:WORD_0
	v_exp_f16_sdwa v149, v93 dst_sel:WORD_0 dst_unused:UNUSED_PAD src0_sel:WORD_0
	v_exp_f16_sdwa v150, v94 dst_sel:WORD_0 dst_unused:UNUSED_PAD src0_sel:WORD_0
	v_exp_f16_sdwa v151, v95 dst_sel:WORD_0 dst_unused:UNUSED_PAD src0_sel:WORD_0
	v_exp_f16_sdwa v148, v92 dst_sel:WORD_1 dst_unused:UNUSED_PRESERVE src0_sel:WORD_1
	v_exp_f16_sdwa v149, v93 dst_sel:WORD_1 dst_unused:UNUSED_PRESERVE src0_sel:WORD_1
	v_exp_f16_sdwa v150, v94 dst_sel:WORD_1 dst_unused:UNUSED_PRESERVE src0_sel:WORD_1
	v_exp_f16_sdwa v151, v95 dst_sel:WORD_1 dst_unused:UNUSED_PRESERVE src0_sel:WORD_1
	v_pk_add_f16 v69, v69, v141 neg_lo:[0,1] neg_hi:[0,1]
	v_pk_add_f16 v76, v76, v151
	v_pk_fma_f16 v48, v56, v148, v48
	v_pk_add_f16 v56, v115, v140 neg_lo:[0,1] neg_hi:[0,1]
	v_pk_add_f16 v79, v79, v148
	v_pk_add_f16 v78, v78, v149
	v_pk_add_f16 v77, v77, v150
	v_pk_fma_f16 v51, v59, v151, v51
	v_pk_fma_f16 v50, v58, v150, v50
	v_pk_fma_f16 v49, v57, v149, v49
	v_pk_add_f16 v57, v114, v141 neg_lo:[0,1] neg_hi:[0,1]
	v_pk_add_f16 v58, v113, v142 neg_lo:[0,1] neg_hi:[0,1]
	v_pk_add_f16 v59, v112, v143 neg_lo:[0,1] neg_hi:[0,1]
	v_pk_add_f16 v70, v70, v142 neg_lo:[0,1] neg_hi:[0,1]
	v_exp_f16_sdwa v92, v56 dst_sel:WORD_0 dst_unused:UNUSED_PAD src0_sel:WORD_0
	v_exp_f16_sdwa v93, v57 dst_sel:WORD_0 dst_unused:UNUSED_PAD src0_sel:WORD_0
	v_exp_f16_sdwa v94, v58 dst_sel:WORD_0 dst_unused:UNUSED_PAD src0_sel:WORD_0
	v_exp_f16_sdwa v95, v59 dst_sel:WORD_0 dst_unused:UNUSED_PAD src0_sel:WORD_0
	v_exp_f16_sdwa v92, v56 dst_sel:WORD_1 dst_unused:UNUSED_PRESERVE src0_sel:WORD_1
	v_exp_f16_sdwa v93, v57 dst_sel:WORD_1 dst_unused:UNUSED_PRESERVE src0_sel:WORD_1
	v_exp_f16_sdwa v94, v58 dst_sel:WORD_1 dst_unused:UNUSED_PRESERVE src0_sel:WORD_1
	v_exp_f16_sdwa v95, v59 dst_sel:WORD_1 dst_unused:UNUSED_PRESERVE src0_sel:WORD_1
	v_pk_add_f16 v71, v71, v143 neg_lo:[0,1] neg_hi:[0,1]
	v_pk_add_f16 v56, v76, v95
	v_pk_add_f16 v57, v77, v94
	v_pk_add_f16 v58, v78, v93
	v_pk_add_f16 v59, v79, v92
	v_pk_fma_f16 v48, v72, v92, v48
	v_pk_fma_f16 v49, v73, v93, v49
	v_pk_fma_f16 v50, v74, v94, v50
	v_pk_fma_f16 v51, v75, v95, v51
	v_pk_add_f16 v72, v119, v140 neg_lo:[0,1] neg_hi:[0,1]
	v_pk_add_f16 v73, v118, v141 neg_lo:[0,1] neg_hi:[0,1]
	v_pk_add_f16 v74, v117, v142 neg_lo:[0,1] neg_hi:[0,1]
	v_pk_add_f16 v75, v116, v143 neg_lo:[0,1] neg_hi:[0,1]
	v_exp_f16_sdwa v76, v72 dst_sel:WORD_0 dst_unused:UNUSED_PAD src0_sel:WORD_0
	v_exp_f16_sdwa v77, v73 dst_sel:WORD_0 dst_unused:UNUSED_PAD src0_sel:WORD_0
	v_exp_f16_sdwa v78, v74 dst_sel:WORD_0 dst_unused:UNUSED_PAD src0_sel:WORD_0
	v_exp_f16_sdwa v79, v75 dst_sel:WORD_0 dst_unused:UNUSED_PAD src0_sel:WORD_0
	v_exp_f16_sdwa v76, v72 dst_sel:WORD_1 dst_unused:UNUSED_PRESERVE src0_sel:WORD_1
	v_exp_f16_sdwa v77, v73 dst_sel:WORD_1 dst_unused:UNUSED_PRESERVE src0_sel:WORD_1
	v_exp_f16_sdwa v78, v74 dst_sel:WORD_1 dst_unused:UNUSED_PRESERVE src0_sel:WORD_1
	v_exp_f16_sdwa v79, v75 dst_sel:WORD_1 dst_unused:UNUSED_PRESERVE src0_sel:WORD_1
	v_pk_add_f16 v72, v135, v140 neg_lo:[0,1] neg_hi:[0,1]
	v_pk_add_f16 v56, v56, v79
	v_pk_add_f16 v59, v59, v76
	v_pk_add_f16 v58, v58, v77
	v_pk_add_f16 v57, v57, v78
	v_pk_fma_f16 v51, v35, v79, v51
	v_pk_fma_f16 v50, v34, v78, v50
	v_pk_fma_f16 v49, v33, v77, v49
	v_pk_fma_f16 v48, v32, v76, v48
	v_pk_add_f16 v73, v134, v141 neg_lo:[0,1] neg_hi:[0,1]
	v_pk_add_f16 v74, v133, v142 neg_lo:[0,1] neg_hi:[0,1]
	v_pk_add_f16 v75, v132, v143 neg_lo:[0,1] neg_hi:[0,1]
	v_exp_f16_sdwa v76, v72 dst_sel:WORD_0 dst_unused:UNUSED_PAD src0_sel:WORD_0
	v_exp_f16_sdwa v77, v73 dst_sel:WORD_0 dst_unused:UNUSED_PAD src0_sel:WORD_0
	v_exp_f16_sdwa v78, v74 dst_sel:WORD_0 dst_unused:UNUSED_PAD src0_sel:WORD_0
	v_exp_f16_sdwa v79, v75 dst_sel:WORD_0 dst_unused:UNUSED_PAD src0_sel:WORD_0
	v_exp_f16_sdwa v76, v72 dst_sel:WORD_1 dst_unused:UNUSED_PRESERVE src0_sel:WORD_1
	v_exp_f16_sdwa v77, v73 dst_sel:WORD_1 dst_unused:UNUSED_PRESERVE src0_sel:WORD_1
	v_exp_f16_sdwa v78, v74 dst_sel:WORD_1 dst_unused:UNUSED_PRESERVE src0_sel:WORD_1
	v_exp_f16_sdwa v79, v75 dst_sel:WORD_1 dst_unused:UNUSED_PRESERVE src0_sel:WORD_1
	v_pk_add_f16 v72, v139, v140 neg_lo:[0,1] neg_hi:[0,1]
	v_pk_add_f16 v56, v56, v79
	v_pk_add_f16 v57, v57, v78
	v_pk_add_f16 v58, v58, v77
	v_pk_add_f16 v59, v59, v76
	v_pk_fma_f16 v48, v36, v76, v48
	v_pk_fma_f16 v49, v37, v77, v49
	v_pk_fma_f16 v50, v38, v78, v50
	v_pk_fma_f16 v51, v39, v79, v51
	v_pk_add_f16 v73, v138, v141 neg_lo:[0,1] neg_hi:[0,1]
	v_pk_add_f16 v74, v137, v142 neg_lo:[0,1] neg_hi:[0,1]
	v_pk_add_f16 v75, v136, v143 neg_lo:[0,1] neg_hi:[0,1]
	v_exp_f16_sdwa v76, v72 dst_sel:WORD_0 dst_unused:UNUSED_PAD src0_sel:WORD_0
	v_exp_f16_sdwa v77, v73 dst_sel:WORD_0 dst_unused:UNUSED_PAD src0_sel:WORD_0
	v_exp_f16_sdwa v78, v74 dst_sel:WORD_0 dst_unused:UNUSED_PAD src0_sel:WORD_0
	v_exp_f16_sdwa v79, v75 dst_sel:WORD_0 dst_unused:UNUSED_PAD src0_sel:WORD_0
	v_exp_f16_sdwa v76, v72 dst_sel:WORD_1 dst_unused:UNUSED_PRESERVE src0_sel:WORD_1
	v_exp_f16_sdwa v77, v73 dst_sel:WORD_1 dst_unused:UNUSED_PRESERVE src0_sel:WORD_1
	v_exp_f16_sdwa v78, v74 dst_sel:WORD_1 dst_unused:UNUSED_PRESERVE src0_sel:WORD_1
	v_exp_f16_sdwa v79, v75 dst_sel:WORD_1 dst_unused:UNUSED_PRESERVE src0_sel:WORD_1
	v_exp_f16_sdwa v72, v68 dst_sel:WORD_0 dst_unused:UNUSED_PAD src0_sel:WORD_0
	v_exp_f16_sdwa v73, v69 dst_sel:WORD_0 dst_unused:UNUSED_PAD src0_sel:WORD_0
	v_exp_f16_sdwa v74, v70 dst_sel:WORD_0 dst_unused:UNUSED_PAD src0_sel:WORD_0
	v_exp_f16_sdwa v75, v71 dst_sel:WORD_0 dst_unused:UNUSED_PAD src0_sel:WORD_0
	v_exp_f16_sdwa v72, v68 dst_sel:WORD_1 dst_unused:UNUSED_PRESERVE src0_sel:WORD_1
	v_exp_f16_sdwa v73, v69 dst_sel:WORD_1 dst_unused:UNUSED_PRESERVE src0_sel:WORD_1
	v_exp_f16_sdwa v74, v70 dst_sel:WORD_1 dst_unused:UNUSED_PRESERVE src0_sel:WORD_1
	v_exp_f16_sdwa v75, v71 dst_sel:WORD_1 dst_unused:UNUSED_PRESERVE src0_sel:WORD_1
	v_pk_add_f16 v68, v96, v140 neg_lo:[0,1] neg_hi:[0,1]
	v_pk_add_f16 v56, v56, v79
	v_pk_add_f16 v59, v59, v76
	v_pk_add_f16 v58, v58, v77
	v_pk_add_f16 v57, v57, v78
	v_pk_fma_f16 v51, v43, v79, v51
	v_pk_fma_f16 v50, v42, v78, v50
	v_pk_fma_f16 v49, v41, v77, v49
	v_pk_fma_f16 v48, v40, v76, v48
	v_pk_add_f16 v56, v56, v75
	v_pk_add_f16 v57, v57, v74
	v_pk_add_f16 v58, v58, v73
	v_pk_add_f16 v59, v59, v72
	v_pk_fma_f16 v48, v52, v72, v48
	v_pk_fma_f16 v49, v53, v73, v49
	v_pk_fma_f16 v50, v54, v74, v50
	v_pk_fma_f16 v51, v55, v75, v51
	v_pk_add_f16 v69, v97, v141 neg_lo:[0,1] neg_hi:[0,1]
	v_pk_add_f16 v70, v98, v142 neg_lo:[0,1] neg_hi:[0,1]
	v_pk_add_f16 v71, v99, v143 neg_lo:[0,1] neg_hi:[0,1]
	v_exp_f16_sdwa v72, v68 dst_sel:WORD_0 dst_unused:UNUSED_PAD src0_sel:WORD_0
	v_exp_f16_sdwa v73, v69 dst_sel:WORD_0 dst_unused:UNUSED_PAD src0_sel:WORD_0
	v_exp_f16_sdwa v74, v70 dst_sel:WORD_0 dst_unused:UNUSED_PAD src0_sel:WORD_0
	v_exp_f16_sdwa v75, v71 dst_sel:WORD_0 dst_unused:UNUSED_PAD src0_sel:WORD_0
	v_exp_f16_sdwa v72, v68 dst_sel:WORD_1 dst_unused:UNUSED_PRESERVE src0_sel:WORD_1
	v_exp_f16_sdwa v73, v69 dst_sel:WORD_1 dst_unused:UNUSED_PRESERVE src0_sel:WORD_1
	v_exp_f16_sdwa v74, v70 dst_sel:WORD_1 dst_unused:UNUSED_PRESERVE src0_sel:WORD_1
	v_exp_f16_sdwa v75, v71 dst_sel:WORD_1 dst_unused:UNUSED_PRESERVE src0_sel:WORD_1
	v_pk_add_f16 v68, v108, v140 neg_lo:[0,1] neg_hi:[0,1]
	v_pk_add_f16 v56, v56, v75
	v_pk_add_f16 v59, v59, v72
	v_pk_add_f16 v58, v58, v73
	v_pk_add_f16 v57, v57, v74
	v_pk_fma_f16 v51, v67, v75, v51
	v_pk_fma_f16 v50, v66, v74, v50
	v_pk_fma_f16 v49, v65, v73, v49
	v_pk_fma_f16 v48, v64, v72, v48
	v_pk_add_f16 v69, v109, v141 neg_lo:[0,1] neg_hi:[0,1]
	v_pk_add_f16 v70, v110, v142 neg_lo:[0,1] neg_hi:[0,1]
	v_pk_add_f16 v71, v111, v143 neg_lo:[0,1] neg_hi:[0,1]
	v_exp_f16_sdwa v72, v68 dst_sel:WORD_0 dst_unused:UNUSED_PAD src0_sel:WORD_0
	v_exp_f16_sdwa v73, v69 dst_sel:WORD_0 dst_unused:UNUSED_PAD src0_sel:WORD_0
	v_exp_f16_sdwa v74, v70 dst_sel:WORD_0 dst_unused:UNUSED_PAD src0_sel:WORD_0
	v_exp_f16_sdwa v75, v71 dst_sel:WORD_0 dst_unused:UNUSED_PAD src0_sel:WORD_0
	v_exp_f16_sdwa v72, v68 dst_sel:WORD_1 dst_unused:UNUSED_PRESERVE src0_sel:WORD_1
	v_exp_f16_sdwa v73, v69 dst_sel:WORD_1 dst_unused:UNUSED_PRESERVE src0_sel:WORD_1
	v_exp_f16_sdwa v74, v70 dst_sel:WORD_1 dst_unused:UNUSED_PRESERVE src0_sel:WORD_1
	v_exp_f16_sdwa v75, v71 dst_sel:WORD_1 dst_unused:UNUSED_PRESERVE src0_sel:WORD_1
	s_nop 0
	v_pk_add_f16 v56, v56, v75
	v_pk_add_f16 v57, v57, v74
	v_rcp_f16_e32 v70, v56
	v_rcp_f16_sdwa v56, v56 dst_sel:DWORD dst_unused:UNUSED_PAD src0_sel:WORD_1
	v_pk_add_f16 v58, v58, v73
	v_rcp_f16_e32 v71, v57
	v_rcp_f16_sdwa v57, v57 dst_sel:DWORD dst_unused:UNUSED_PAD src0_sel:WORD_1
	v_pk_add_f16 v59, v59, v72
	v_rcp_f16_e32 v69, v58
	v_rcp_f16_sdwa v58, v58 dst_sel:DWORD dst_unused:UNUSED_PAD src0_sel:WORD_1
	v_rcp_f16_e32 v68, v59
	v_rcp_f16_sdwa v59, v59 dst_sel:DWORD dst_unused:UNUSED_PAD src0_sel:WORD_1
	v_pk_fma_f16 v51, v87, v75, v51
	v_pack_b32_f16 v56, v70, v56
	v_pk_fma_f16 v50, v86, v74, v50
	v_pk_mul_f16 v51, v51, v56
	v_pack_b32_f16 v56, v71, v57
	v_pk_fma_f16 v49, v85, v73, v49
	v_pk_mul_f16 v50, v50, v56
	v_pack_b32_f16 v56, v69, v58
	v_pk_fma_f16 v48, v84, v72, v48
	v_pk_mul_f16 v49, v49, v56
	v_pack_b32_f16 v56, v68, v59
	v_pk_mul_f16 v48, v48, v56
	s_waitcnt vmcnt(0)
	v_pk_mul_f16 v56, v188, v168 op_sel_hi:[0,1]
	v_pk_mul_f16 v57, v188, v169 op_sel_hi:[0,1]
	v_pk_mul_f16 v58, v188, v170 op_sel_hi:[0,1]
	v_pk_mul_f16 v59, v188, v171 op_sel_hi:[0,1]
	v_pk_mul_f16 v68, v186, v168 op_sel_hi:[0,1]
	v_pk_mul_f16 v69, v186, v169 op_sel_hi:[0,1]
	v_pk_mul_f16 v70, v186, v170 op_sel_hi:[0,1]
	v_pk_mul_f16 v71, v186, v171 op_sel_hi:[0,1]
	v_pk_mul_f16 v72, v187, v168 op_sel_hi:[0,1]
	v_pk_mul_f16 v73, v187, v169 op_sel_hi:[0,1]
	v_pk_mul_f16 v74, v187, v170 op_sel_hi:[0,1]
	v_pk_mul_f16 v75, v187, v171 op_sel_hi:[0,1]
	v_pk_fma_f16 v47, v47, v171, v59
	v_pk_fma_f16 v46, v46, v170, v58
	v_pk_fma_f16 v45, v45, v169, v57
	v_pk_fma_f16 v44, v44, v168, v56
	v_pk_fma_f16 v63, v63, v171, v71
	v_pk_fma_f16 v62, v62, v170, v70
	v_pk_fma_f16 v61, v61, v169, v69
	v_pk_fma_f16 v60, v60, v168, v68
	v_pk_fma_f16 v76, v83, v171, v75
	v_pk_fma_f16 v77, v82, v170, v74
	v_pk_fma_f16 v78, v81, v169, v73
	v_pk_fma_f16 v79, v80, v168, v72
	v_pk_fma_f16 v80, v103, v171, v59
	v_pk_fma_f16 v81, v102, v170, v58
	v_pk_fma_f16 v82, v101, v169, v57
	v_pk_fma_f16 v83, v100, v168, v56
	v_pk_fma_f16 v92, v131, v171, v71
	v_pk_fma_f16 v93, v130, v170, v70
	v_pk_fma_f16 v94, v129, v169, v69
	v_pk_fma_f16 v95, v128, v168, v68
	v_pk_fma_f16 v96, v147, v171, v75
	v_pk_fma_f16 v97, v146, v170, v74
	v_pk_fma_f16 v98, v145, v169, v73
	v_pk_fma_f16 v99, v144, v168, v72
	v_pk_fma_f16 v75, v31, v171, v75
	v_pk_fma_f16 v74, v30, v170, v74
	v_pk_fma_f16 v73, v29, v169, v73
	v_pk_fma_f16 v72, v28, v168, v72
	v_pk_maximum3_f16 v28, v44, v60, v79
	v_pk_maximum3_f16 v29, v45, v61, v78
	v_pk_maximum3_f16 v30, v46, v62, v77
	v_pk_maximum3_f16 v31, v47, v63, v76
	v_pk_maximum3_f16 v100, v83, v95, v99
	v_pk_maximum3_f16 v101, v82, v94, v98
	v_pk_maximum3_f16 v102, v81, v93, v97
	v_pk_maximum3_f16 v103, v80, v92, v96
	v_pk_fma_f16 v59, v159, v171, v59
	v_pk_fma_f16 v58, v158, v170, v58
	v_pk_fma_f16 v57, v157, v169, v57
	v_pk_fma_f16 v56, v156, v168, v56
	v_pk_fma_f16 v71, v167, v171, v71
	v_pk_fma_f16 v70, v166, v170, v70
	v_pk_fma_f16 v69, v165, v169, v69
	v_pk_fma_f16 v68, v164, v168, v68
	v_pk_maximum3_f16 v109, v57, v69, v73
	v_pk_maximum3_f16 v110, v58, v70, v74
	v_pk_maximum3_f16 v111, v59, v71, v75
	v_pk_maximum3_f16 v108, v56, v68, v72
	v_pk_maximum3_f16 v29, v29, v101, v109
	v_pk_maximum3_f16 v30, v30, v102, v110
	v_pk_maximum3_f16 v31, v31, v103, v111
	v_pk_maximum3_f16 v28, v28, v100, v108
	v_xor_b32_e32 v100, 0x80008000, v31
	v_xor_b32_e32 v101, 0x80008000, v30
	v_xor_b32_e32 v102, 0x80008000, v29
	v_xor_b32_e32 v103, 0x80008000, v28
	v_pk_add_f16 v28, v44, v103
	v_pk_add_f16 v29, v45, v102
	v_pk_add_f16 v30, v46, v101
	v_pk_add_f16 v31, v47, v100
	v_exp_f16_sdwa v44, v28 dst_sel:WORD_0 dst_unused:UNUSED_PAD src0_sel:WORD_0
	v_exp_f16_sdwa v45, v29 dst_sel:WORD_0 dst_unused:UNUSED_PAD src0_sel:WORD_0
	v_exp_f16_sdwa v46, v30 dst_sel:WORD_0 dst_unused:UNUSED_PAD src0_sel:WORD_0
	v_exp_f16_sdwa v47, v31 dst_sel:WORD_0 dst_unused:UNUSED_PAD src0_sel:WORD_0
	v_exp_f16_sdwa v44, v28 dst_sel:WORD_1 dst_unused:UNUSED_PRESERVE src0_sel:WORD_1
	v_exp_f16_sdwa v45, v29 dst_sel:WORD_1 dst_unused:UNUSED_PRESERVE src0_sel:WORD_1
	v_exp_f16_sdwa v46, v30 dst_sel:WORD_1 dst_unused:UNUSED_PRESERVE src0_sel:WORD_1
	v_exp_f16_sdwa v47, v31 dst_sel:WORD_1 dst_unused:UNUSED_PRESERVE src0_sel:WORD_1
	v_pk_add_f16 v28, v44, 0
	v_pk_add_f16 v29, v45, 0
	v_pk_add_f16 v30, v46, 0
	v_pk_add_f16 v31, v47, 0
	v_pk_fma_f16 v32, v32, v44, 0
	v_pk_fma_f16 v33, v33, v45, 0
	v_pk_fma_f16 v34, v34, v46, 0
	v_pk_fma_f16 v35, v35, v47, 0
	v_pk_add_f16 v44, v60, v103
	v_pk_add_f16 v45, v61, v102
	v_pk_add_f16 v46, v62, v101
	v_pk_add_f16 v47, v63, v100
	v_exp_f16_sdwa v60, v44 dst_sel:WORD_0 dst_unused:UNUSED_PAD src0_sel:WORD_0
	v_exp_f16_sdwa v61, v45 dst_sel:WORD_0 dst_unused:UNUSED_PAD src0_sel:WORD_0
	v_exp_f16_sdwa v62, v46 dst_sel:WORD_0 dst_unused:UNUSED_PAD src0_sel:WORD_0
	v_exp_f16_sdwa v63, v47 dst_sel:WORD_0 dst_unused:UNUSED_PAD src0_sel:WORD_0
	v_exp_f16_sdwa v60, v44 dst_sel:WORD_1 dst_unused:UNUSED_PRESERVE src0_sel:WORD_1
	v_exp_f16_sdwa v61, v45 dst_sel:WORD_1 dst_unused:UNUSED_PRESERVE src0_sel:WORD_1
	v_exp_f16_sdwa v62, v46 dst_sel:WORD_1 dst_unused:UNUSED_PRESERVE src0_sel:WORD_1
	v_exp_f16_sdwa v63, v47 dst_sel:WORD_1 dst_unused:UNUSED_PRESERVE src0_sel:WORD_1
	s_nop 0
	v_pk_add_f16 v31, v31, v63
	v_pk_add_f16 v30, v30, v62
	v_pk_add_f16 v29, v29, v61
	v_pk_add_f16 v28, v28, v60
	v_pk_fma_f16 v35, v39, v63, v35
	v_pk_fma_f16 v34, v38, v62, v34
	v_pk_fma_f16 v33, v37, v61, v33
	v_pk_fma_f16 v32, v36, v60, v32
	v_pk_add_f16 v36, v79, v103
	v_pk_add_f16 v37, v78, v102
	v_pk_add_f16 v38, v77, v101
	v_pk_add_f16 v39, v76, v100
	v_exp_f16_sdwa v44, v36 dst_sel:WORD_0 dst_unused:UNUSED_PAD src0_sel:WORD_0
	v_exp_f16_sdwa v45, v37 dst_sel:WORD_0 dst_unused:UNUSED_PAD src0_sel:WORD_0
	v_exp_f16_sdwa v46, v38 dst_sel:WORD_0 dst_unused:UNUSED_PAD src0_sel:WORD_0
	v_exp_f16_sdwa v47, v39 dst_sel:WORD_0 dst_unused:UNUSED_PAD src0_sel:WORD_0
	v_exp_f16_sdwa v44, v36 dst_sel:WORD_1 dst_unused:UNUSED_PRESERVE src0_sel:WORD_1
	v_exp_f16_sdwa v45, v37 dst_sel:WORD_1 dst_unused:UNUSED_PRESERVE src0_sel:WORD_1
	v_exp_f16_sdwa v46, v38 dst_sel:WORD_1 dst_unused:UNUSED_PRESERVE src0_sel:WORD_1
	v_exp_f16_sdwa v47, v39 dst_sel:WORD_1 dst_unused:UNUSED_PRESERVE src0_sel:WORD_1
	v_pk_add_f16 v36, v83, v103
	v_pk_add_f16 v28, v28, v44
	v_pk_add_f16 v29, v29, v45
	v_pk_add_f16 v30, v30, v46
	v_pk_add_f16 v31, v31, v47
	v_pk_fma_f16 v32, v40, v44, v32
	v_pk_fma_f16 v33, v41, v45, v33
	v_pk_fma_f16 v34, v42, v46, v34
	v_pk_fma_f16 v35, v43, v47, v35
	v_pk_add_f16 v37, v82, v102
	v_pk_add_f16 v38, v81, v101
	v_pk_add_f16 v39, v80, v100
	v_exp_f16_sdwa v40, v36 dst_sel:WORD_0 dst_unused:UNUSED_PAD src0_sel:WORD_0
	v_exp_f16_sdwa v41, v37 dst_sel:WORD_0 dst_unused:UNUSED_PAD src0_sel:WORD_0
	v_exp_f16_sdwa v42, v38 dst_sel:WORD_0 dst_unused:UNUSED_PAD src0_sel:WORD_0
	v_exp_f16_sdwa v43, v39 dst_sel:WORD_0 dst_unused:UNUSED_PAD src0_sel:WORD_0
	v_exp_f16_sdwa v40, v36 dst_sel:WORD_1 dst_unused:UNUSED_PRESERVE src0_sel:WORD_1
	v_exp_f16_sdwa v41, v37 dst_sel:WORD_1 dst_unused:UNUSED_PRESERVE src0_sel:WORD_1
	v_exp_f16_sdwa v42, v38 dst_sel:WORD_1 dst_unused:UNUSED_PRESERVE src0_sel:WORD_1
	v_exp_f16_sdwa v43, v39 dst_sel:WORD_1 dst_unused:UNUSED_PRESERVE src0_sel:WORD_1
	v_pk_add_f16 v36, v95, v103
	v_pk_add_f16 v31, v31, v43
	v_pk_add_f16 v30, v30, v42
	v_pk_add_f16 v29, v29, v41
	v_pk_add_f16 v28, v28, v40
	v_pk_fma_f16 v35, v55, v43, v35
	v_pk_fma_f16 v34, v54, v42, v34
	v_pk_fma_f16 v33, v53, v41, v33
	v_pk_fma_f16 v32, v52, v40, v32
	v_pk_add_f16 v37, v94, v102
	v_pk_add_f16 v38, v93, v101
	v_pk_add_f16 v39, v92, v100
	v_exp_f16_sdwa v40, v36 dst_sel:WORD_0 dst_unused:UNUSED_PAD src0_sel:WORD_0
	v_exp_f16_sdwa v41, v37 dst_sel:WORD_0 dst_unused:UNUSED_PAD src0_sel:WORD_0
	v_exp_f16_sdwa v42, v38 dst_sel:WORD_0 dst_unused:UNUSED_PAD src0_sel:WORD_0
	v_exp_f16_sdwa v43, v39 dst_sel:WORD_0 dst_unused:UNUSED_PAD src0_sel:WORD_0
	v_exp_f16_sdwa v40, v36 dst_sel:WORD_1 dst_unused:UNUSED_PRESERVE src0_sel:WORD_1
	v_exp_f16_sdwa v41, v37 dst_sel:WORD_1 dst_unused:UNUSED_PRESERVE src0_sel:WORD_1
	v_exp_f16_sdwa v42, v38 dst_sel:WORD_1 dst_unused:UNUSED_PRESERVE src0_sel:WORD_1
	v_exp_f16_sdwa v43, v39 dst_sel:WORD_1 dst_unused:UNUSED_PRESERVE src0_sel:WORD_1
	v_pk_add_f16 v36, v99, v103
	v_pk_add_f16 v28, v28, v40
	v_pk_add_f16 v29, v29, v41
	v_pk_add_f16 v30, v30, v42
	v_pk_add_f16 v31, v31, v43
	v_pk_fma_f16 v32, v64, v40, v32
	v_pk_fma_f16 v33, v65, v41, v33
	v_pk_fma_f16 v34, v66, v42, v34
	v_pk_fma_f16 v35, v67, v43, v35
	v_pk_add_f16 v37, v98, v102
	v_pk_add_f16 v38, v97, v101
	v_pk_add_f16 v39, v96, v100
	v_exp_f16_sdwa v40, v36 dst_sel:WORD_0 dst_unused:UNUSED_PAD src0_sel:WORD_0
	v_exp_f16_sdwa v41, v37 dst_sel:WORD_0 dst_unused:UNUSED_PAD src0_sel:WORD_0
	v_exp_f16_sdwa v42, v38 dst_sel:WORD_0 dst_unused:UNUSED_PAD src0_sel:WORD_0
	v_exp_f16_sdwa v43, v39 dst_sel:WORD_0 dst_unused:UNUSED_PAD src0_sel:WORD_0
	v_exp_f16_sdwa v40, v36 dst_sel:WORD_1 dst_unused:UNUSED_PRESERVE src0_sel:WORD_1
	v_exp_f16_sdwa v41, v37 dst_sel:WORD_1 dst_unused:UNUSED_PRESERVE src0_sel:WORD_1
	v_exp_f16_sdwa v42, v38 dst_sel:WORD_1 dst_unused:UNUSED_PRESERVE src0_sel:WORD_1
	v_exp_f16_sdwa v43, v39 dst_sel:WORD_1 dst_unused:UNUSED_PRESERVE src0_sel:WORD_1
	v_pk_add_f16 v36, v56, v103
	v_pk_add_f16 v31, v31, v43
	v_pk_add_f16 v30, v30, v42
	v_pk_add_f16 v29, v29, v41
	v_pk_add_f16 v28, v28, v40
	v_pk_fma_f16 v35, v87, v43, v35
	v_pk_fma_f16 v34, v86, v42, v34
	v_pk_fma_f16 v33, v85, v41, v33
	v_pk_fma_f16 v32, v84, v40, v32
	v_pk_add_f16 v37, v57, v102
	v_pk_add_f16 v38, v58, v101
	v_pk_add_f16 v39, v59, v100
	v_exp_f16_sdwa v40, v36 dst_sel:WORD_0 dst_unused:UNUSED_PAD src0_sel:WORD_0
	v_exp_f16_sdwa v41, v37 dst_sel:WORD_0 dst_unused:UNUSED_PAD src0_sel:WORD_0
	v_exp_f16_sdwa v42, v38 dst_sel:WORD_0 dst_unused:UNUSED_PAD src0_sel:WORD_0
	v_exp_f16_sdwa v43, v39 dst_sel:WORD_0 dst_unused:UNUSED_PAD src0_sel:WORD_0
	v_exp_f16_sdwa v40, v36 dst_sel:WORD_1 dst_unused:UNUSED_PRESERVE src0_sel:WORD_1
	v_exp_f16_sdwa v41, v37 dst_sel:WORD_1 dst_unused:UNUSED_PRESERVE src0_sel:WORD_1
	v_exp_f16_sdwa v42, v38 dst_sel:WORD_1 dst_unused:UNUSED_PRESERVE src0_sel:WORD_1
	v_exp_f16_sdwa v43, v39 dst_sel:WORD_1 dst_unused:UNUSED_PRESERVE src0_sel:WORD_1
	v_pk_add_f16 v36, v68, v103
	v_pk_add_f16 v28, v28, v40
	v_pk_add_f16 v29, v29, v41
	v_pk_add_f16 v30, v30, v42
	v_pk_add_f16 v31, v31, v43
	v_pk_fma_f16 v32, v104, v40, v32
	v_pk_fma_f16 v33, v105, v41, v33
	v_pk_fma_f16 v34, v106, v42, v34
	v_pk_fma_f16 v35, v107, v43, v35
	v_pk_add_f16 v37, v69, v102
	v_pk_add_f16 v38, v70, v101
	v_pk_add_f16 v39, v71, v100
	v_exp_f16_sdwa v40, v36 dst_sel:WORD_0 dst_unused:UNUSED_PAD src0_sel:WORD_0
	v_exp_f16_sdwa v41, v37 dst_sel:WORD_0 dst_unused:UNUSED_PAD src0_sel:WORD_0
	v_exp_f16_sdwa v42, v38 dst_sel:WORD_0 dst_unused:UNUSED_PAD src0_sel:WORD_0
	v_exp_f16_sdwa v43, v39 dst_sel:WORD_0 dst_unused:UNUSED_PAD src0_sel:WORD_0
	v_exp_f16_sdwa v40, v36 dst_sel:WORD_1 dst_unused:UNUSED_PRESERVE src0_sel:WORD_1
	v_exp_f16_sdwa v41, v37 dst_sel:WORD_1 dst_unused:UNUSED_PRESERVE src0_sel:WORD_1
	v_exp_f16_sdwa v42, v38 dst_sel:WORD_1 dst_unused:UNUSED_PRESERVE src0_sel:WORD_1
	v_exp_f16_sdwa v43, v39 dst_sel:WORD_1 dst_unused:UNUSED_PRESERVE src0_sel:WORD_1
	s_nop 0
	v_pk_add_f16 v31, v31, v43
	v_pk_add_f16 v30, v30, v42
	v_pk_add_f16 v29, v29, v41
	v_pk_add_f16 v28, v28, v40
	v_pk_fma_f16 v35, v123, v43, v35
	v_pk_fma_f16 v34, v122, v42, v34
	v_pk_fma_f16 v33, v121, v41, v33
	v_pk_fma_f16 v32, v120, v40, v32
	v_pk_add_f16 v40, v72, v103
	v_pk_add_f16 v41, v73, v102
	v_pk_add_f16 v42, v74, v101
	v_pk_add_f16 v43, v75, v100
	v_exp_f16_sdwa v36, v40 dst_sel:WORD_0 dst_unused:UNUSED_PAD src0_sel:WORD_0
	v_exp_f16_sdwa v37, v41 dst_sel:WORD_0 dst_unused:UNUSED_PAD src0_sel:WORD_0
	v_exp_f16_sdwa v38, v42 dst_sel:WORD_0 dst_unused:UNUSED_PAD src0_sel:WORD_0
	v_exp_f16_sdwa v39, v43 dst_sel:WORD_0 dst_unused:UNUSED_PAD src0_sel:WORD_0
	v_exp_f16_sdwa v36, v40 dst_sel:WORD_1 dst_unused:UNUSED_PRESERVE src0_sel:WORD_1
	v_exp_f16_sdwa v37, v41 dst_sel:WORD_1 dst_unused:UNUSED_PRESERVE src0_sel:WORD_1
	v_exp_f16_sdwa v38, v42 dst_sel:WORD_1 dst_unused:UNUSED_PRESERVE src0_sel:WORD_1
	v_exp_f16_sdwa v39, v43 dst_sel:WORD_1 dst_unused:UNUSED_PRESERVE src0_sel:WORD_1
	s_nop 0
	s_load_dwordx2 s[12:13], s[0:1], 0x60
	s_branch .LBB6_76
